# v43 with the 52 mid-block s_setprio 0/1 flip pairs of the 8-phase GEMM loops deleted (asm doc 6.3 rule 2 A/B)
# speedup vs baseline: 1.0069x; 1.0059x over previous
; #define FG_STAGE(bufoff, gbase, v0, v1) do { \
;         __builtin_amdgcn_global_load_lds((const unsigned*)((const char*)(gbase) + (v0)), (LAS unsigned*)(lds + (bufoff) + ldsw), 16, 0, 0); \
;         __builtin_amdgcn_global_load_lds((const unsigned*)((const char*)(gbase) + (v1)), (LAS unsigned*)(lds + (bufoff) + ldsw + 8192), 16, 0, 0); } while (0)
; #define FG_LDA(dst, b, h) do { _Pragma("unroll") for (int m = 0; m < 4; ++m) _Pragma("unroll") for (int k = 0; k < 2; ++k) dst[m][k] = *(const LAS bf16x8*)(lds + FG_SA(b, h) + aoff + m * 2048 + k * 1024); } while (0)
; #define FG_LDB(dst, b, h) do { _Pragma("unroll") for (int n = 0; n < 2; ++n) _Pragma("unroll") for (int k = 0; k < 2; ++k) dst[n][k] = *(const LAS bf16x8*)(lds + FG_SB(b, h) + boff + n * 2048 + k * 1024); } while (0)
; #define FG_MMA(ai, bj, At, Bt) do { __builtin_amdgcn_s_setprio(1); _Pragma("unroll") for (int m = 0; m < 4; ++m) _Pragma("unroll") for (int n = 0; n < 2; ++n) _Pragma("unroll") for (int k = 0; k < 2; ++k) \
;         acc[ai][bj][m][n] = __builtin_amdgcn_mfma_f32_16x16x32_bf16(Bt[n][k], At[m][k], acc[ai][bj][m][n], 0, 0, 0); __builtin_amdgcn_s_setprio(0); } while (0)
; #define FG_WAIT_V(n) asm volatile("s_waitcnt vmcnt(" #n ")" ::: "memory")
; #define FG_BAR __builtin_amdgcn_s_barrier()
; template <bool GATHER, class Unit, class Epi, class Sched>
; __device__ __forceinline__ void gemm_phase(LAS unsigned char* lds, const int K, const Sched& S, const Epi& E) {
;     ...
;         for (int t = 0; t < nt; t += 2) {
;             const bool last = (t == nt - 2);
;             const char* a1 = cA + (size_t)(t + 1) * kstep;
;             const char* a2 = last ? nA : cA + (size_t)(t + 2) * kstep; const char* b2 = last ? nB : cB + (size_t)(t + 2) * kstep;
;             const char* a3 = a2 + kstep; const char* b3 = b2 + kstep;
;             const unsigned x00 = (GATHER && last) ? vN00 : vA00, x01 = (GATHER && last) ? vN01 : vA01, x10 = (GATHER && last) ? vN10 : vA10, x11 = (GATHER && last) ? vN11 : vA11;
;             FG_LDB(B0, 0, 0); FG_LDB(B1, 0, 1); FG_SCHED; FG_LDA(At, 0, 0); FG_STAGE(FG_SA(1, 1), a1, vA10, vA11);
;             FG_WAIT_V(8); FG_WAIT_L(0); FG_BAR; FG_MMA(0, 0, At, B0); FG_MMA(0, 1, At, B1); FG_BAR; FG_SCHED;
;             FG_LDA(At, 0, 1); FG_STAGE(FG_SB(0, 0), b2, voffB0, voffB1); FG_STAGE(FG_SB(0, 1), b2 + hstepB, voffB0, voffB1); FG_STAGE(FG_SA(0, 0), a2, x00, x01);
.LBB0_273:
	ds_read_b128 v[158:161], v154
	ds_read_b128 v[162:165], v154 offset:1024
	ds_read_b128 v[166:169], v154 offset:2048
	ds_read_b128 v[170:173], v154 offset:3072
	ds_read_b128 v[174:177], v155
	ds_read_b128 v[178:181], v155 offset:1024
	ds_read_b128 v[182:185], v155 offset:2048
	ds_read_b128 v[186:189], v155 offset:3072
	s_add_u32 s46, s44, 0x100
	s_addc_u32 s47, s45, 0
	s_cmp_eq_u32 s68, 28
	s_cselect_b32 s51, s37, s47
	s_cselect_b32 s50, s43, s46
	s_cselect_b32 s49, s35, s67
	s_cselect_b32 s48, s65, s66
	v_lshl_add_u64 v[152:153], s[44:45], 0, v[146:147]
	s_add_i32 m0, s28, 0xc000
	ds_read_b128 v[190:193], v156
	ds_read_b128 v[194:197], v156 offset:1024
	ds_read_b128 v[198:201], v156 offset:2048
	ds_read_b128 v[202:205], v156 offset:3072
	ds_read_b128 v[206:209], v156 offset:4096
	ds_read_b128 v[210:213], v156 offset:5120
	ds_read_b128 v[214:217], v156 offset:6144
	ds_read_b128 v[218:221], v156 offset:7168
	global_load_lds_dwordx4 v[152:153], off
	v_lshl_add_u64 v[152:153], s[44:45], 0, v[144:145]
	s_add_i32 m0, s28, 0xe000
	s_nop 0
	global_load_lds_dwordx4 v[152:153], off
	s_waitcnt vmcnt(8)
	s_waitcnt lgkmcnt(0)
	s_barrier
	s_setprio 1
	s_waitcnt lgkmcnt(0)
	v_mfma_f32_16x16x32_bf16 v[126:129], v[158:161], v[190:193], v[126:129]
	v_mfma_f32_16x16x32_bf16 v[122:125], v[166:169], v[190:193], v[122:125]
	v_mfma_f32_16x16x32_bf16 v[118:121], v[158:161], v[198:201], v[118:121]
	v_mfma_f32_16x16x32_bf16 v[110:113], v[166:169], v[198:201], v[110:113]
	v_mfma_f32_16x16x32_bf16 v[102:105], v[158:161], v[206:209], v[102:105]
	v_mfma_f32_16x16x32_bf16 v[94:97], v[166:169], v[206:209], v[94:97]
	v_mfma_f32_16x16x32_bf16 v[86:89], v[158:161], v[214:217], v[86:89]
	v_mfma_f32_16x16x32_bf16 v[78:81], v[166:169], v[214:217], v[78:81]
	v_mfma_f32_16x16x32_bf16 v[126:129], v[162:165], v[194:197], v[126:129]
	v_mfma_f32_16x16x32_bf16 v[122:125], v[170:173], v[194:197], v[122:125]
	v_mfma_f32_16x16x32_bf16 v[118:121], v[162:165], v[202:205], v[118:121]
	v_mfma_f32_16x16x32_bf16 v[110:113], v[170:173], v[202:205], v[110:113]
	v_mfma_f32_16x16x32_bf16 v[102:105], v[162:165], v[210:213], v[102:105]
	v_mfma_f32_16x16x32_bf16 v[94:97], v[170:173], v[210:213], v[94:97]
	v_mfma_f32_16x16x32_bf16 v[86:89], v[162:165], v[218:221], v[86:89]
	v_mfma_f32_16x16x32_bf16 v[78:81], v[170:173], v[218:221], v[78:81]
	v_mfma_f32_16x16x32_bf16 v[114:117], v[174:177], v[190:193], v[114:117]
	v_mfma_f32_16x16x32_bf16 v[106:109], v[182:185], v[190:193], v[106:109]
	v_mfma_f32_16x16x32_bf16 v[98:101], v[174:177], v[198:201], v[98:101]
	v_mfma_f32_16x16x32_bf16 v[90:93], v[182:185], v[198:201], v[90:93]
	v_mfma_f32_16x16x32_bf16 v[82:85], v[174:177], v[206:209], v[82:85]
	v_mfma_f32_16x16x32_bf16 v[74:77], v[182:185], v[206:209], v[74:77]
	v_mfma_f32_16x16x32_bf16 v[70:73], v[174:177], v[214:217], v[70:73]
	v_mfma_f32_16x16x32_bf16 v[66:69], v[182:185], v[214:217], v[66:69]
	v_mfma_f32_16x16x32_bf16 v[114:117], v[178:181], v[194:197], v[114:117]
	v_mfma_f32_16x16x32_bf16 v[106:109], v[186:189], v[194:197], v[106:109]
	v_mfma_f32_16x16x32_bf16 v[98:101], v[178:181], v[202:205], v[98:101]
	v_mfma_f32_16x16x32_bf16 v[90:93], v[186:189], v[202:205], v[90:93]
	v_mfma_f32_16x16x32_bf16 v[82:85], v[178:181], v[210:213], v[82:85]
	v_mfma_f32_16x16x32_bf16 v[74:77], v[186:189], v[210:213], v[74:77]
	v_mfma_f32_16x16x32_bf16 v[70:73], v[178:181], v[218:221], v[70:73]
	v_mfma_f32_16x16x32_bf16 v[66:69], v[186:189], v[218:221], v[66:69]
	s_setprio 0
	s_barrier
	s_add_i32 s44, s57, s27
	v_lshl_add_u64 v[152:153], s[48:49], 0, v[132:133]
	s_mov_b32 m0, s44
	ds_read_b128 v[190:193], v156 offset:16384
	ds_read_b128 v[194:197], v156 offset:17408
	ds_read_b128 v[198:201], v156 offset:18432
	ds_read_b128 v[202:205], v156 offset:19456
	ds_read_b128 v[206:209], v156 offset:20480
	ds_read_b128 v[210:213], v156 offset:21504
	ds_read_b128 v[214:217], v156 offset:22528
	ds_read_b128 v[218:221], v156 offset:23552
	global_load_lds_dwordx4 v[152:153], off
	s_add_i32 m0, s44, 0x2000
	s_add_u32 s44, s48, 0x80000
	v_lshl_add_u64 v[222:223], s[48:49], 0, v[130:131]
	s_addc_u32 s45, s49, 0
	s_add_i32 s69, s58, s27
	global_load_lds_dwordx4 v[222:223], off
	v_lshl_add_u64 v[224:225], s[44:45], 0, v[132:133]
	s_mov_b32 m0, s69
	v_lshl_add_u64 v[226:227], s[50:51], 0, v[136:137]
	global_load_lds_dwordx4 v[224:225], off
	v_lshl_add_u64 v[224:225], s[44:45], 0, v[130:131]
	s_add_i32 m0, s69, 0x2000
	s_nop 0
	global_load_lds_dwordx4 v[224:225], off
	v_lshl_add_u64 v[224:225], s[50:51], 0, v[134:135]
	s_mov_b32 m0, s28
	s_nop 0
	global_load_lds_dwordx4 v[224:225], off
	s_mov_b32 m0, s29
	s_nop 0
	global_load_lds_dwordx4 v[226:227], off
	s_waitcnt vmcnt(8)
	s_waitcnt lgkmcnt(0)
	s_barrier
; #define FG_STAGE(bufoff, gbase, v0, v1) do { \
;         __builtin_amdgcn_global_load_lds((const unsigned*)((const char*)(gbase) + (v0)), (LAS unsigned*)(lds + (bufoff) + ldsw), 16, 0, 0); \
;         __builtin_amdgcn_global_load_lds((const unsigned*)((const char*)(gbase) + (v1)), (LAS unsigned*)(lds + (bufoff) + ldsw + 8192), 16, 0, 0); } while (0)
; #define FG_LDA(dst, b, h) do { _Pragma("unroll") for (int m = 0; m < 4; ++m) _Pragma("unroll") for (int k = 0; k < 2; ++k) dst[m][k] = *(const LAS bf16x8*)(lds + FG_SA(b, h) + aoff + m * 2048 + k * 1024); } while (0)
; #define FG_LDB(dst, b, h) do { _Pragma("unroll") for (int n = 0; n < 2; ++n) _Pragma("unroll") for (int k = 0; k < 2; ++k) dst[n][k] = *(const LAS bf16x8*)(lds + FG_SB(b, h) + boff + n * 2048 + k * 1024); } while (0)
; #define FG_MMA(ai, bj, At, Bt) do { __builtin_amdgcn_s_setprio(1); _Pragma("unroll") for (int m = 0; m < 4; ++m) _Pragma("unroll") for (int n = 0; n < 2; ++n) _Pragma("unroll") for (int k = 0; k < 2; ++k) \
;         acc[ai][bj][m][n] = __builtin_amdgcn_mfma_f32_16x16x32_bf16(Bt[n][k], At[m][k], acc[ai][bj][m][n], 0, 0, 0); __builtin_amdgcn_s_setprio(0); } while (0)
; #define FG_WAIT_V(n) asm volatile("s_waitcnt vmcnt(" #n ")" ::: "memory")
; #define FG_WAIT_L(n) asm volatile("s_waitcnt lgkmcnt(" #n ")" ::: "memory")
; #define FG_BAR __builtin_amdgcn_s_barrier()
; #define FG_SCHED __builtin_amdgcn_sched_barrier(0)
; template <bool GATHER, class Unit, class Epi, class Sched>
; __device__ __forceinline__ void gemm_phase(LAS unsigned char* lds, const int K, const Sched& S, const Epi& E) {
;     ...
;             FG_LDA(At, 0, 1); FG_STAGE(FG_SB(0, 0), b2, voffB0, voffB1); FG_STAGE(FG_SB(0, 1), b2 + hstepB, voffB0, voffB1); FG_STAGE(FG_SA(0, 0), a2, x00, x01);
;             FG_WAIT_V(8); FG_WAIT_L(0); FG_BAR; if (hi_on) { FG_MMA(1, 0, At, B0); FG_MMA(1, 1, At, B1); } FG_BAR; FG_SCHED;
;             FG_LDB(B0, 1, 0); FG_LDB(B1, 1, 1); FG_SCHED; FG_LDA(At, 1, 0); FG_STAGE(FG_SA(0, 1), a2, x10, x11);
;             FG_WAIT_V(8); FG_WAIT_L(0); FG_BAR; FG_MMA(0, 0, At, B0); FG_MMA(0, 1, At, B1); FG_BAR; FG_SCHED;
;             FG_LDA(At, 1, 1); FG_STAGE(FG_SB(1, 0), b3, voffB0, voffB1); FG_STAGE(FG_SB(1, 1), b3 + hstepB, voffB0, voffB1); FG_STAGE(FG_SA(1, 0), a3, x00, x01);
	s_setprio 1
	s_waitcnt lgkmcnt(0)
	v_mfma_f32_16x16x32_bf16 v[62:65], v[158:161], v[190:193], v[62:65]
	v_mfma_f32_16x16x32_bf16 v[58:61], v[166:169], v[190:193], v[58:61]
	v_mfma_f32_16x16x32_bf16 v[54:57], v[158:161], v[198:201], v[54:57]
	v_mfma_f32_16x16x32_bf16 v[46:49], v[166:169], v[198:201], v[46:49]
	v_mfma_f32_16x16x32_bf16 v[38:41], v[158:161], v[206:209], v[38:41]
	v_mfma_f32_16x16x32_bf16 v[30:33], v[166:169], v[206:209], v[30:33]
	v_mfma_f32_16x16x32_bf16 v[22:25], v[158:161], v[214:217], v[22:25]
	v_mfma_f32_16x16x32_bf16 v[14:17], v[166:169], v[214:217], v[14:17]
	v_mfma_f32_16x16x32_bf16 v[62:65], v[162:165], v[194:197], v[62:65]
	v_mfma_f32_16x16x32_bf16 v[58:61], v[170:173], v[194:197], v[58:61]
	v_mfma_f32_16x16x32_bf16 v[54:57], v[162:165], v[202:205], v[54:57]
	v_mfma_f32_16x16x32_bf16 v[46:49], v[170:173], v[202:205], v[46:49]
	v_mfma_f32_16x16x32_bf16 v[38:41], v[162:165], v[210:213], v[38:41]
	v_mfma_f32_16x16x32_bf16 v[30:33], v[170:173], v[210:213], v[30:33]
	v_mfma_f32_16x16x32_bf16 v[22:25], v[162:165], v[218:221], v[22:25]
	v_mfma_f32_16x16x32_bf16 v[14:17], v[170:173], v[218:221], v[14:17]
	v_mfma_f32_16x16x32_bf16 v[50:53], v[174:177], v[190:193], v[50:53]
	v_mfma_f32_16x16x32_bf16 v[42:45], v[182:185], v[190:193], v[42:45]
	v_mfma_f32_16x16x32_bf16 v[34:37], v[174:177], v[198:201], v[34:37]
	v_mfma_f32_16x16x32_bf16 v[26:29], v[182:185], v[198:201], v[26:29]
	v_mfma_f32_16x16x32_bf16 v[18:21], v[174:177], v[206:209], v[18:21]
	v_mfma_f32_16x16x32_bf16 v[10:13], v[182:185], v[206:209], v[10:13]
	v_mfma_f32_16x16x32_bf16 v[6:9], v[174:177], v[214:217], v[6:9]
	v_mfma_f32_16x16x32_bf16 v[2:5], v[182:185], v[214:217], v[2:5]
	v_mfma_f32_16x16x32_bf16 v[50:53], v[178:181], v[194:197], v[50:53]
	v_mfma_f32_16x16x32_bf16 v[42:45], v[186:189], v[194:197], v[42:45]
	v_mfma_f32_16x16x32_bf16 v[34:37], v[178:181], v[202:205], v[34:37]
	v_mfma_f32_16x16x32_bf16 v[26:29], v[186:189], v[202:205], v[26:29]
	v_mfma_f32_16x16x32_bf16 v[18:21], v[178:181], v[210:213], v[18:21]
	v_mfma_f32_16x16x32_bf16 v[10:13], v[186:189], v[210:213], v[10:13]
	v_mfma_f32_16x16x32_bf16 v[6:9], v[178:181], v[218:221], v[6:9]
	v_mfma_f32_16x16x32_bf16 v[2:5], v[186:189], v[218:221], v[2:5]
	s_setprio 0
	s_barrier
	s_add_i32 s44, 0, 0x18000
	v_add_u32_e32 v142, s44, v1
	s_add_i32 s69, 0, 0x1c000
	ds_read_b128 v[158:161], v142
	ds_read_b128 v[162:165], v142 offset:1024
	ds_read_b128 v[166:169], v142 offset:2048
	ds_read_b128 v[170:173], v142 offset:3072
	v_add_u32_e32 v142, s69, v1
	ds_read_b128 v[174:177], v142
	ds_read_b128 v[178:181], v142 offset:1024
	ds_read_b128 v[182:185], v142 offset:2048
	ds_read_b128 v[186:189], v142 offset:3072
	s_mov_b32 m0, s30
	v_lshl_add_u64 v[228:229], s[50:51], 0, v[138:139]
	ds_read_b128 v[190:193], v156 offset:32768
	ds_read_b128 v[194:197], v156 offset:33792
	ds_read_b128 v[198:201], v156 offset:34816
	ds_read_b128 v[202:205], v156 offset:35840
	ds_read_b128 v[206:209], v156 offset:36864
	ds_read_b128 v[210:213], v156 offset:37888
	ds_read_b128 v[214:217], v156 offset:38912
	ds_read_b128 v[218:221], v156 offset:39936
	global_load_lds_dwordx4 v[228:229], off
	v_lshl_add_u64 v[228:229], s[50:51], 0, v[140:141]
	s_mov_b32 m0, s31
	s_nop 0
	global_load_lds_dwordx4 v[228:229], off
	s_waitcnt vmcnt(8)
	s_waitcnt lgkmcnt(0)
	s_barrier
	s_setprio 1
	s_waitcnt lgkmcnt(0)
	v_mfma_f32_16x16x32_bf16 v[126:129], v[158:161], v[190:193], v[126:129]
	v_mfma_f32_16x16x32_bf16 v[122:125], v[166:169], v[190:193], v[122:125]
	v_mfma_f32_16x16x32_bf16 v[118:121], v[158:161], v[198:201], v[118:121]
	v_mfma_f32_16x16x32_bf16 v[110:113], v[166:169], v[198:201], v[110:113]
	v_mfma_f32_16x16x32_bf16 v[102:105], v[158:161], v[206:209], v[102:105]
	v_mfma_f32_16x16x32_bf16 v[94:97], v[166:169], v[206:209], v[94:97]
	v_mfma_f32_16x16x32_bf16 v[86:89], v[158:161], v[214:217], v[86:89]
	v_mfma_f32_16x16x32_bf16 v[78:81], v[166:169], v[214:217], v[78:81]
	v_mfma_f32_16x16x32_bf16 v[126:129], v[162:165], v[194:197], v[126:129]
	v_mfma_f32_16x16x32_bf16 v[122:125], v[170:173], v[194:197], v[122:125]
	v_mfma_f32_16x16x32_bf16 v[118:121], v[162:165], v[202:205], v[118:121]
	v_mfma_f32_16x16x32_bf16 v[110:113], v[170:173], v[202:205], v[110:113]
	v_mfma_f32_16x16x32_bf16 v[102:105], v[162:165], v[210:213], v[102:105]
	v_mfma_f32_16x16x32_bf16 v[94:97], v[170:173], v[210:213], v[94:97]
	v_mfma_f32_16x16x32_bf16 v[86:89], v[162:165], v[218:221], v[86:89]
	v_mfma_f32_16x16x32_bf16 v[78:81], v[170:173], v[218:221], v[78:81]
	v_mfma_f32_16x16x32_bf16 v[114:117], v[174:177], v[190:193], v[114:117]
	v_mfma_f32_16x16x32_bf16 v[106:109], v[182:185], v[190:193], v[106:109]
	v_mfma_f32_16x16x32_bf16 v[98:101], v[174:177], v[198:201], v[98:101]
	v_mfma_f32_16x16x32_bf16 v[90:93], v[182:185], v[198:201], v[90:93]
	v_mfma_f32_16x16x32_bf16 v[82:85], v[174:177], v[206:209], v[82:85]
	v_mfma_f32_16x16x32_bf16 v[74:77], v[182:185], v[206:209], v[74:77]
	v_mfma_f32_16x16x32_bf16 v[70:73], v[174:177], v[214:217], v[70:73]
	v_mfma_f32_16x16x32_bf16 v[66:69], v[182:185], v[214:217], v[66:69]
	v_mfma_f32_16x16x32_bf16 v[114:117], v[178:181], v[194:197], v[114:117]
	v_mfma_f32_16x16x32_bf16 v[106:109], v[186:189], v[194:197], v[106:109]
	v_mfma_f32_16x16x32_bf16 v[98:101], v[178:181], v[202:205], v[98:101]
	v_mfma_f32_16x16x32_bf16 v[90:93], v[186:189], v[202:205], v[90:93]
	v_mfma_f32_16x16x32_bf16 v[82:85], v[178:181], v[210:213], v[82:85]
	v_mfma_f32_16x16x32_bf16 v[74:77], v[186:189], v[210:213], v[74:77]
	v_mfma_f32_16x16x32_bf16 v[70:73], v[178:181], v[218:221], v[70:73]
	v_mfma_f32_16x16x32_bf16 v[66:69], v[186:189], v[218:221], v[66:69]
	s_setprio 0
	s_barrier
; #define FG_STAGE(bufoff, gbase, v0, v1) do { \
;         __builtin_amdgcn_global_load_lds((const unsigned*)((const char*)(gbase) + (v0)), (LAS unsigned*)(lds + (bufoff) + ldsw), 16, 0, 0); \
;         __builtin_amdgcn_global_load_lds((const unsigned*)((const char*)(gbase) + (v1)), (LAS unsigned*)(lds + (bufoff) + ldsw + 8192), 16, 0, 0); } while (0)
; #define FG_LDA(dst, b, h) do { _Pragma("unroll") for (int m = 0; m < 4; ++m) _Pragma("unroll") for (int k = 0; k < 2; ++k) dst[m][k] = *(const LAS bf16x8*)(lds + FG_SA(b, h) + aoff + m * 2048 + k * 1024); } while (0)
; #define FG_MMA(ai, bj, At, Bt) do { __builtin_amdgcn_s_setprio(1); _Pragma("unroll") for (int m = 0; m < 4; ++m) _Pragma("unroll") for (int n = 0; n < 2; ++n) _Pragma("unroll") for (int k = 0; k < 2; ++k) \
;         acc[ai][bj][m][n] = __builtin_amdgcn_mfma_f32_16x16x32_bf16(Bt[n][k], At[m][k], acc[ai][bj][m][n], 0, 0, 0); __builtin_amdgcn_s_setprio(0); } while (0)
; #define FG_WAIT_V(n) asm volatile("s_waitcnt vmcnt(" #n ")" ::: "memory")
; #define FG_WAIT_L(n) asm volatile("s_waitcnt lgkmcnt(" #n ")" ::: "memory")
; #define FG_BAR __builtin_amdgcn_s_barrier()
; #define FG_SCHED __builtin_amdgcn_sched_barrier(0)
; template <bool GATHER, class Unit, class Epi, class Sched>
; __device__ __forceinline__ void gemm_phase(LAS unsigned char* lds, const int K, const Sched& S, const Epi& E) {
;     ...
;             FG_LDA(At, 1, 1); FG_STAGE(FG_SB(1, 0), b3, voffB0, voffB1); FG_STAGE(FG_SB(1, 1), b3 + hstepB, voffB0, voffB1); FG_STAGE(FG_SA(1, 0), a3, x00, x01);
;             FG_WAIT_V(8); FG_WAIT_L(0); FG_BAR; if (hi_on) { FG_MMA(1, 0, At, B0); FG_MMA(1, 1, At, B1); } FG_BAR; FG_SCHED;
;         }
;         if (wr == 0) FG_BAR;
	s_add_i32 s44, s44, s27
	v_lshl_add_u64 v[152:153], v[152:153], 0, s[12:13]
	s_mov_b32 m0, s44
	ds_read_b128 v[190:193], v156 offset:49152
	ds_read_b128 v[194:197], v156 offset:50176
	ds_read_b128 v[198:201], v156 offset:51200
	ds_read_b128 v[202:205], v156 offset:52224
	ds_read_b128 v[206:209], v156 offset:53248
	ds_read_b128 v[210:213], v156 offset:54272
	ds_read_b128 v[214:217], v156 offset:55296
	ds_read_b128 v[218:221], v156 offset:56320
	global_load_lds_dwordx4 v[152:153], off
	s_add_i32 m0, s44, 0x2000
	s_add_u32 s44, s48, 0x80080
	v_lshl_add_u64 v[152:153], v[222:223], 0, s[12:13]
	s_addc_u32 s45, s49, 0
	s_add_i32 s48, s69, s27
	global_load_lds_dwordx4 v[152:153], off
	v_lshl_add_u64 v[152:153], s[44:45], 0, v[132:133]
	s_mov_b32 m0, s48
	s_nop 0
	global_load_lds_dwordx4 v[152:153], off
	v_lshl_add_u64 v[152:153], s[44:45], 0, v[130:131]
	s_add_i32 m0, s48, 0x2000
	s_nop 0
	global_load_lds_dwordx4 v[152:153], off
	v_lshl_add_u64 v[152:153], v[224:225], 0, s[12:13]
	s_mov_b32 m0, s54
	s_nop 0
	global_load_lds_dwordx4 v[152:153], off
	v_lshl_add_u64 v[152:153], v[226:227], 0, s[12:13]
	s_mov_b32 m0, s55
	s_nop 0
	global_load_lds_dwordx4 v[152:153], off
	s_waitcnt vmcnt(8)
	s_waitcnt lgkmcnt(0)
	s_barrier
	s_setprio 1
	s_waitcnt lgkmcnt(0)
	v_mfma_f32_16x16x32_bf16 v[62:65], v[158:161], v[190:193], v[62:65]
	v_mfma_f32_16x16x32_bf16 v[58:61], v[166:169], v[190:193], v[58:61]
	v_mfma_f32_16x16x32_bf16 v[54:57], v[158:161], v[198:201], v[54:57]
	v_mfma_f32_16x16x32_bf16 v[46:49], v[166:169], v[198:201], v[46:49]
	v_mfma_f32_16x16x32_bf16 v[38:41], v[158:161], v[206:209], v[38:41]
	v_mfma_f32_16x16x32_bf16 v[30:33], v[166:169], v[206:209], v[30:33]
	v_mfma_f32_16x16x32_bf16 v[22:25], v[158:161], v[214:217], v[22:25]
	v_mfma_f32_16x16x32_bf16 v[14:17], v[166:169], v[214:217], v[14:17]
	v_mfma_f32_16x16x32_bf16 v[62:65], v[162:165], v[194:197], v[62:65]
	v_mfma_f32_16x16x32_bf16 v[58:61], v[170:173], v[194:197], v[58:61]
	v_mfma_f32_16x16x32_bf16 v[54:57], v[162:165], v[202:205], v[54:57]
	v_mfma_f32_16x16x32_bf16 v[46:49], v[170:173], v[202:205], v[46:49]
	v_mfma_f32_16x16x32_bf16 v[38:41], v[162:165], v[210:213], v[38:41]
	v_mfma_f32_16x16x32_bf16 v[30:33], v[170:173], v[210:213], v[30:33]
	v_mfma_f32_16x16x32_bf16 v[22:25], v[162:165], v[218:221], v[22:25]
	v_mfma_f32_16x16x32_bf16 v[14:17], v[170:173], v[218:221], v[14:17]
	v_mfma_f32_16x16x32_bf16 v[50:53], v[174:177], v[190:193], v[50:53]
	v_mfma_f32_16x16x32_bf16 v[42:45], v[182:185], v[190:193], v[42:45]
	v_mfma_f32_16x16x32_bf16 v[34:37], v[174:177], v[198:201], v[34:37]
	v_mfma_f32_16x16x32_bf16 v[26:29], v[182:185], v[198:201], v[26:29]
	v_mfma_f32_16x16x32_bf16 v[18:21], v[174:177], v[206:209], v[18:21]
	v_mfma_f32_16x16x32_bf16 v[10:13], v[182:185], v[206:209], v[10:13]
	v_mfma_f32_16x16x32_bf16 v[6:9], v[174:177], v[214:217], v[6:9]
	v_mfma_f32_16x16x32_bf16 v[2:5], v[182:185], v[214:217], v[2:5]
	v_mfma_f32_16x16x32_bf16 v[50:53], v[178:181], v[194:197], v[50:53]
	v_mfma_f32_16x16x32_bf16 v[42:45], v[186:189], v[194:197], v[42:45]
	v_mfma_f32_16x16x32_bf16 v[34:37], v[178:181], v[202:205], v[34:37]
	v_mfma_f32_16x16x32_bf16 v[26:29], v[186:189], v[202:205], v[26:29]
	v_mfma_f32_16x16x32_bf16 v[18:21], v[178:181], v[210:213], v[18:21]
	v_mfma_f32_16x16x32_bf16 v[10:13], v[186:189], v[210:213], v[10:13]
	v_mfma_f32_16x16x32_bf16 v[6:9], v[178:181], v[218:221], v[6:9]
	v_mfma_f32_16x16x32_bf16 v[2:5], v[186:189], v[218:221], v[2:5]
	s_setprio 0
	s_barrier
	s_add_i32 s68, s68, 2
	s_add_u32 s66, s66, 0x100
	s_addc_u32 s67, s67, 0
	s_cmp_gt_u32 s68, 29
	s_mov_b64 s[44:45], s[46:47]
	s_cbranch_scc0 .LBB0_273
	s_and_b64 vcc, exec, s[14:15]
	s_cbranch_vccz .LBB0_276
	s_barrier

; #define FG_STAGE(bufoff, gbase, v0, v1) do { \
;         __builtin_amdgcn_global_load_lds((const unsigned*)((const char*)(gbase) + (v0)), (LAS unsigned*)(lds + (bufoff) + ldsw), 16, 0, 0); \
;         __builtin_amdgcn_global_load_lds((const unsigned*)((const char*)(gbase) + (v1)), (LAS unsigned*)(lds + (bufoff) + ldsw + 8192), 16, 0, 0); } while (0)
; #define FG_LDA(dst, b, h) do { _Pragma("unroll") for (int m = 0; m < 4; ++m) _Pragma("unroll") for (int k = 0; k < 2; ++k) dst[m][k] = *(const LAS bf16x8*)(lds + FG_SA(b, h) + aoff + m * 2048 + k * 1024); } while (0)
; #define FG_LDB(dst, b, h) do { _Pragma("unroll") for (int n = 0; n < 2; ++n) _Pragma("unroll") for (int k = 0; k < 2; ++k) dst[n][k] = *(const LAS bf16x8*)(lds + FG_SB(b, h) + boff + n * 2048 + k * 1024); } while (0)
; #define FG_WAIT_V(n) asm volatile("s_waitcnt vmcnt(" #n ")" ::: "memory")
; #define FG_WAIT_L(n) asm volatile("s_waitcnt lgkmcnt(" #n ")" ::: "memory")
; #define FG_BAR __builtin_amdgcn_s_barrier()
; #define FG_SCHED __builtin_amdgcn_sched_barrier(0)
; template <bool GATHER, class Unit, class Epi, class Sched>
; __device__ __forceinline__ void gemm_phase(LAS unsigned char* lds, const int K, const Sched& S, const Epi& E) {
;     ...
;         for (int t = 0; t < nt; t += 2) {
;             const bool last = (t == nt - 2);
;             const char* a1 = cA + (size_t)(t + 1) * kstep;
;             const char* a2 = last ? nA : cA + (size_t)(t + 2) * kstep; const char* b2 = last ? nB : cB + (size_t)(t + 2) * kstep;
;             const char* a3 = a2 + kstep; const char* b3 = b2 + kstep;
;             const unsigned x00 = (GATHER && last) ? vN00 : vA00, x01 = (GATHER && last) ? vN01 : vA01, x10 = (GATHER && last) ? vN10 : vA10, x11 = (GATHER && last) ? vN11 : vA11;
;             FG_LDB(B0, 0, 0); FG_LDB(B1, 0, 1); FG_SCHED; FG_LDA(At, 0, 0); FG_STAGE(FG_SA(1, 1), a1, vA10, vA11);
;             FG_WAIT_V(8); FG_WAIT_L(0); FG_BAR; FG_MMA(0, 0, At, B0); FG_MMA(0, 1, At, B1); FG_BAR; FG_SCHED;
;             FG_LDA(At, 0, 1); FG_STAGE(FG_SB(0, 0), b2, voffB0, voffB1); FG_STAGE(FG_SB(0, 1), b2 + hstepB, voffB0, voffB1); FG_STAGE(FG_SA(0, 0), a2, x00, x01);
;             FG_WAIT_V(8); FG_WAIT_L(0); FG_BAR; if (hi_on) { FG_MMA(1, 0, At, B0); FG_MMA(1, 1, At, B1); } FG_BAR; FG_SCHED;
;             FG_LDB(B0, 1, 0); FG_LDB(B1, 1, 1); FG_SCHED; FG_LDA(At, 1, 0); FG_STAGE(FG_SA(0, 1), a2, x10, x11);
.LBB0_287:
	ds_read_b128 v[86:89], v84
	ds_read_b128 v[90:93], v84 offset:1024
	ds_read_b128 v[94:97], v84 offset:2048
	ds_read_b128 v[98:101], v84 offset:3072
	s_add_u32 s40, s38, 0x80
	s_addc_u32 s41, s39, 0
	s_cmp_eq_u32 s60, 4
	s_cselect_b32 s43, s54, s41
	s_cselect_b32 s42, s55, s40
	s_cselect_b32 s41, s56, s59
	s_cselect_b32 s40, s57, s58
	v_lshl_add_u64 v[134:135], s[38:39], 0, v[82:83]
	s_add_i32 m0, s5, 0xc000
	ds_read_b128 v[102:105], v85
	ds_read_b128 v[106:109], v85 offset:1024
	ds_read_b128 v[110:113], v85 offset:2048
	ds_read_b128 v[114:117], v85 offset:3072
	ds_read_b128 v[118:121], v85 offset:4096
	ds_read_b128 v[122:125], v85 offset:5120
	ds_read_b128 v[126:129], v85 offset:6144
	ds_read_b128 v[130:133], v85 offset:7168
	global_load_lds_dwordx4 v[134:135], off
	v_lshl_add_u64 v[134:135], s[38:39], 0, v[80:81]
	s_add_i32 m0, s5, 0xe000
	s_nop 0
	global_load_lds_dwordx4 v[134:135], off
	s_waitcnt vmcnt(8)
	s_waitcnt lgkmcnt(0)
	s_barrier
	s_setprio 1
	s_waitcnt lgkmcnt(0)
	v_mfma_f32_16x16x32_bf16 v[62:65], v[86:89], v[102:105], v[62:65]
	v_mfma_f32_16x16x32_bf16 v[58:61], v[94:97], v[102:105], v[58:61]
	v_mfma_f32_16x16x32_bf16 v[54:57], v[86:89], v[110:113], v[54:57]
	v_mfma_f32_16x16x32_bf16 v[50:53], v[94:97], v[110:113], v[50:53]
	v_mfma_f32_16x16x32_bf16 v[46:49], v[86:89], v[118:121], v[46:49]
	v_mfma_f32_16x16x32_bf16 v[42:45], v[94:97], v[118:121], v[42:45]
	v_mfma_f32_16x16x32_bf16 v[38:41], v[86:89], v[126:129], v[38:41]
	v_mfma_f32_16x16x32_bf16 v[34:37], v[94:97], v[126:129], v[34:37]
	v_mfma_f32_16x16x32_bf16 v[62:65], v[90:93], v[106:109], v[62:65]
	v_mfma_f32_16x16x32_bf16 v[58:61], v[98:101], v[106:109], v[58:61]
	v_mfma_f32_16x16x32_bf16 v[54:57], v[90:93], v[114:117], v[54:57]
	v_mfma_f32_16x16x32_bf16 v[50:53], v[98:101], v[114:117], v[50:53]
	v_mfma_f32_16x16x32_bf16 v[46:49], v[90:93], v[122:125], v[46:49]
	v_mfma_f32_16x16x32_bf16 v[42:45], v[98:101], v[122:125], v[42:45]
	v_mfma_f32_16x16x32_bf16 v[38:41], v[90:93], v[130:133], v[38:41]
	v_mfma_f32_16x16x32_bf16 v[34:37], v[98:101], v[130:133], v[34:37]
	s_setprio 0
	s_barrier
	s_add_i32 s61, s52, s26
	v_lshl_add_u64 v[134:135], s[40:41], 0, v[68:69]
	s_mov_b32 m0, s61
	ds_read_b128 v[102:105], v85 offset:16384
	ds_read_b128 v[106:109], v85 offset:17408
	ds_read_b128 v[110:113], v85 offset:18432
	ds_read_b128 v[114:117], v85 offset:19456
	ds_read_b128 v[118:121], v85 offset:20480
	ds_read_b128 v[122:125], v85 offset:21504
	ds_read_b128 v[126:129], v85 offset:22528
	ds_read_b128 v[130:133], v85 offset:23552
	global_load_lds_dwordx4 v[134:135], off
	s_add_i32 m0, s61, 0x2000
	s_add_u32 s62, s40, 0x20000
	v_lshl_add_u64 v[136:137], s[40:41], 0, v[66:67]
	s_addc_u32 s63, s41, 0
	global_load_lds_dwordx4 v[136:137], off
	v_lshl_add_u64 v[138:139], s[62:63], 0, v[68:69]
	s_mov_b32 m0, s28
	v_lshl_add_u64 v[140:141], s[42:43], 0, v[72:73]
	global_load_lds_dwordx4 v[138:139], off
	v_lshl_add_u64 v[138:139], s[62:63], 0, v[66:67]
	s_mov_b32 m0, s29
	s_nop 0
	global_load_lds_dwordx4 v[138:139], off
	v_lshl_add_u64 v[138:139], s[42:43], 0, v[70:71]
	s_mov_b32 m0, s5
	s_nop 0
	global_load_lds_dwordx4 v[138:139], off
	s_mov_b32 m0, s30
	s_nop 0
	global_load_lds_dwordx4 v[140:141], off
	s_waitcnt vmcnt(8)
	s_waitcnt lgkmcnt(0)
	s_barrier
	s_setprio 1
	s_waitcnt lgkmcnt(0)
	v_mfma_f32_16x16x32_bf16 v[30:33], v[86:89], v[102:105], v[30:33]
	v_mfma_f32_16x16x32_bf16 v[26:29], v[94:97], v[102:105], v[26:29]
	v_mfma_f32_16x16x32_bf16 v[22:25], v[86:89], v[110:113], v[22:25]
	v_mfma_f32_16x16x32_bf16 v[18:21], v[94:97], v[110:113], v[18:21]
	v_mfma_f32_16x16x32_bf16 v[14:17], v[86:89], v[118:121], v[14:17]
	v_mfma_f32_16x16x32_bf16 v[10:13], v[94:97], v[118:121], v[10:13]
	v_mfma_f32_16x16x32_bf16 v[6:9], v[86:89], v[126:129], v[6:9]
	v_mfma_f32_16x16x32_bf16 v[2:5], v[94:97], v[126:129], v[2:5]
	v_mfma_f32_16x16x32_bf16 v[30:33], v[90:93], v[106:109], v[30:33]
	v_mfma_f32_16x16x32_bf16 v[26:29], v[98:101], v[106:109], v[26:29]
	v_mfma_f32_16x16x32_bf16 v[22:25], v[90:93], v[114:117], v[22:25]
	v_mfma_f32_16x16x32_bf16 v[18:21], v[98:101], v[114:117], v[18:21]
	v_mfma_f32_16x16x32_bf16 v[14:17], v[90:93], v[122:125], v[14:17]
	v_mfma_f32_16x16x32_bf16 v[10:13], v[98:101], v[122:125], v[10:13]
	v_mfma_f32_16x16x32_bf16 v[6:9], v[90:93], v[130:133], v[6:9]
	v_mfma_f32_16x16x32_bf16 v[2:5], v[98:101], v[130:133], v[2:5]
	s_setprio 0
	s_barrier
; #define FG_STAGE(bufoff, gbase, v0, v1) do { \
;         __builtin_amdgcn_global_load_lds((const unsigned*)((const char*)(gbase) + (v0)), (LAS unsigned*)(lds + (bufoff) + ldsw), 16, 0, 0); \
;         __builtin_amdgcn_global_load_lds((const unsigned*)((const char*)(gbase) + (v1)), (LAS unsigned*)(lds + (bufoff) + ldsw + 8192), 16, 0, 0); } while (0)
; #define FG_LDA(dst, b, h) do { _Pragma("unroll") for (int m = 0; m < 4; ++m) _Pragma("unroll") for (int k = 0; k < 2; ++k) dst[m][k] = *(const LAS bf16x8*)(lds + FG_SA(b, h) + aoff + m * 2048 + k * 1024); } while (0)
; #define FG_LDB(dst, b, h) do { _Pragma("unroll") for (int n = 0; n < 2; ++n) _Pragma("unroll") for (int k = 0; k < 2; ++k) dst[n][k] = *(const LAS bf16x8*)(lds + FG_SB(b, h) + boff + n * 2048 + k * 1024); } while (0)
; #define FG_MMA(ai, bj, At, Bt) do { __builtin_amdgcn_s_setprio(1); _Pragma("unroll") for (int m = 0; m < 4; ++m) _Pragma("unroll") for (int n = 0; n < 2; ++n) _Pragma("unroll") for (int k = 0; k < 2; ++k) \
;         acc[ai][bj][m][n] = __builtin_amdgcn_mfma_f32_16x16x32_bf16(Bt[n][k], At[m][k], acc[ai][bj][m][n], 0, 0, 0); __builtin_amdgcn_s_setprio(0); } while (0)
; #define FG_WAIT_V(n) asm volatile("s_waitcnt vmcnt(" #n ")" ::: "memory")
; #define FG_WAIT_L(n) asm volatile("s_waitcnt lgkmcnt(" #n ")" ::: "memory")
; #define FG_BAR __builtin_amdgcn_s_barrier()
; #define FG_SCHED __builtin_amdgcn_sched_barrier(0)
; template <bool GATHER, class Unit, class Epi, class Sched>
; __device__ __forceinline__ void gemm_phase(LAS unsigned char* lds, const int K, const Sched& S, const Epi& E) {
;     ...
;             FG_LDB(B0, 1, 0); FG_LDB(B1, 1, 1); FG_SCHED; FG_LDA(At, 1, 0); FG_STAGE(FG_SA(0, 1), a2, x10, x11);
;             FG_WAIT_V(8); FG_WAIT_L(0); FG_BAR; FG_MMA(0, 0, At, B0); FG_MMA(0, 1, At, B1); FG_BAR; FG_SCHED;
;             FG_LDA(At, 1, 1); FG_STAGE(FG_SB(1, 0), b3, voffB0, voffB1); FG_STAGE(FG_SB(1, 1), b3 + hstepB, voffB0, voffB1); FG_STAGE(FG_SA(1, 0), a3, x00, x01);
;             FG_WAIT_V(8); FG_WAIT_L(0); FG_BAR; if (hi_on) { FG_MMA(1, 0, At, B0); FG_MMA(1, 1, At, B1); } FG_BAR; FG_SCHED;
;         }
;         if (wr == 0) FG_BAR;
	s_add_i32 s61, 0, 0x18000
	v_add_u32_e32 v78, s61, v1
	ds_read_b128 v[86:89], v78
	ds_read_b128 v[90:93], v78 offset:1024
	ds_read_b128 v[94:97], v78 offset:2048
	ds_read_b128 v[98:101], v78 offset:3072
	s_mov_b32 m0, s31
	v_lshl_add_u64 v[142:143], s[42:43], 0, v[74:75]
	ds_read_b128 v[102:105], v85 offset:32768
	ds_read_b128 v[106:109], v85 offset:33792
	ds_read_b128 v[110:113], v85 offset:34816
	ds_read_b128 v[114:117], v85 offset:35840
	ds_read_b128 v[118:121], v85 offset:36864
	ds_read_b128 v[122:125], v85 offset:37888
	ds_read_b128 v[126:129], v85 offset:38912
	ds_read_b128 v[130:133], v85 offset:39936
	global_load_lds_dwordx4 v[142:143], off
	v_lshl_add_u64 v[142:143], s[42:43], 0, v[76:77]
	s_mov_b32 m0, s33
	s_nop 0
	global_load_lds_dwordx4 v[142:143], off
	s_waitcnt vmcnt(8)
	s_waitcnt lgkmcnt(0)
	s_barrier
	s_setprio 1
	s_waitcnt lgkmcnt(0)
	v_mfma_f32_16x16x32_bf16 v[62:65], v[86:89], v[102:105], v[62:65]
	v_mfma_f32_16x16x32_bf16 v[58:61], v[94:97], v[102:105], v[58:61]
	v_mfma_f32_16x16x32_bf16 v[54:57], v[86:89], v[110:113], v[54:57]
	v_mfma_f32_16x16x32_bf16 v[50:53], v[94:97], v[110:113], v[50:53]
	v_mfma_f32_16x16x32_bf16 v[46:49], v[86:89], v[118:121], v[46:49]
	v_mfma_f32_16x16x32_bf16 v[42:45], v[94:97], v[118:121], v[42:45]
	v_mfma_f32_16x16x32_bf16 v[38:41], v[86:89], v[126:129], v[38:41]
	v_mfma_f32_16x16x32_bf16 v[34:37], v[94:97], v[126:129], v[34:37]
	v_mfma_f32_16x16x32_bf16 v[62:65], v[90:93], v[106:109], v[62:65]
	v_mfma_f32_16x16x32_bf16 v[58:61], v[98:101], v[106:109], v[58:61]
	v_mfma_f32_16x16x32_bf16 v[54:57], v[90:93], v[114:117], v[54:57]
	v_mfma_f32_16x16x32_bf16 v[50:53], v[98:101], v[114:117], v[50:53]
	v_mfma_f32_16x16x32_bf16 v[46:49], v[90:93], v[122:125], v[46:49]
	v_mfma_f32_16x16x32_bf16 v[42:45], v[98:101], v[122:125], v[42:45]
	v_mfma_f32_16x16x32_bf16 v[38:41], v[90:93], v[130:133], v[38:41]
	v_mfma_f32_16x16x32_bf16 v[34:37], v[98:101], v[130:133], v[34:37]
	s_setprio 0
	s_barrier
	s_add_i32 s42, s61, s26
	v_lshl_add_u64 v[134:135], v[134:135], 0, s[6:7]
	s_mov_b32 m0, s42
	ds_read_b128 v[102:105], v85 offset:49152
	ds_read_b128 v[106:109], v85 offset:50176
	ds_read_b128 v[110:113], v85 offset:51200
	ds_read_b128 v[114:117], v85 offset:52224
	ds_read_b128 v[118:121], v85 offset:53248
	ds_read_b128 v[122:125], v85 offset:54272
	ds_read_b128 v[126:129], v85 offset:55296
	ds_read_b128 v[130:133], v85 offset:56320
	global_load_lds_dwordx4 v[134:135], off
	s_add_i32 m0, s42, 0x2000
	s_add_u32 s40, s40, 0x20080
	v_lshl_add_u64 v[134:135], v[136:137], 0, s[6:7]
	s_addc_u32 s41, s41, 0
	global_load_lds_dwordx4 v[134:135], off
	v_lshl_add_u64 v[134:135], s[40:41], 0, v[68:69]
	s_mov_b32 m0, s49
	s_nop 0
	global_load_lds_dwordx4 v[134:135], off
	v_lshl_add_u64 v[134:135], s[40:41], 0, v[66:67]
	s_mov_b32 m0, s50
	s_nop 0
	global_load_lds_dwordx4 v[134:135], off
	v_lshl_add_u64 v[134:135], v[138:139], 0, s[6:7]
	s_mov_b32 m0, s47
	s_nop 0
	global_load_lds_dwordx4 v[134:135], off
	v_lshl_add_u64 v[134:135], v[140:141], 0, s[6:7]
	s_mov_b32 m0, s48
	s_nop 0
	global_load_lds_dwordx4 v[134:135], off
	s_waitcnt vmcnt(8)
	s_waitcnt lgkmcnt(0)
	s_barrier
	s_setprio 1
	s_waitcnt lgkmcnt(0)
	v_mfma_f32_16x16x32_bf16 v[30:33], v[86:89], v[102:105], v[30:33]
	v_mfma_f32_16x16x32_bf16 v[26:29], v[94:97], v[102:105], v[26:29]
	v_mfma_f32_16x16x32_bf16 v[22:25], v[86:89], v[110:113], v[22:25]
	v_mfma_f32_16x16x32_bf16 v[18:21], v[94:97], v[110:113], v[18:21]
	v_mfma_f32_16x16x32_bf16 v[14:17], v[86:89], v[118:121], v[14:17]
	v_mfma_f32_16x16x32_bf16 v[10:13], v[94:97], v[118:121], v[10:13]
	v_mfma_f32_16x16x32_bf16 v[6:9], v[86:89], v[126:129], v[6:9]
	v_mfma_f32_16x16x32_bf16 v[2:5], v[94:97], v[126:129], v[2:5]
	v_mfma_f32_16x16x32_bf16 v[30:33], v[90:93], v[106:109], v[30:33]
	v_mfma_f32_16x16x32_bf16 v[26:29], v[98:101], v[106:109], v[26:29]
	v_mfma_f32_16x16x32_bf16 v[22:25], v[90:93], v[114:117], v[22:25]
	v_mfma_f32_16x16x32_bf16 v[18:21], v[98:101], v[114:117], v[18:21]
	v_mfma_f32_16x16x32_bf16 v[14:17], v[90:93], v[122:125], v[14:17]
	v_mfma_f32_16x16x32_bf16 v[10:13], v[98:101], v[122:125], v[10:13]
	v_mfma_f32_16x16x32_bf16 v[6:9], v[90:93], v[130:133], v[6:9]
	v_mfma_f32_16x16x32_bf16 v[2:5], v[98:101], v[130:133], v[2:5]
	s_setprio 0
	s_barrier
	s_add_i32 s60, s60, 2
	s_add_u32 s58, s58, 0x100
	s_addc_u32 s59, s59, 0
	s_add_u32 s38, s38, 0x100
	s_addc_u32 s39, s39, 0
	s_cmp_gt_u32 s60, 5
	s_cbranch_scc0 .LBB0_287
	s_and_b64 vcc, exec, s[14:15]
	s_cbranch_vccz .LBB0_290
	s_barrier

; #define FG_STAGE(bufoff, gbase, v0, v1) do { \
;         __builtin_amdgcn_global_load_lds((const unsigned*)((const char*)(gbase) + (v0)), (LAS unsigned*)(lds + (bufoff) + ldsw), 16, 0, 0); \
;         __builtin_amdgcn_global_load_lds((const unsigned*)((const char*)(gbase) + (v1)), (LAS unsigned*)(lds + (bufoff) + ldsw + 8192), 16, 0, 0); } while (0)
; #define FG_LDA(dst, b, h) do { _Pragma("unroll") for (int m = 0; m < 4; ++m) _Pragma("unroll") for (int k = 0; k < 2; ++k) dst[m][k] = *(const LAS bf16x8*)(lds + FG_SA(b, h) + aoff + m * 2048 + k * 1024); } while (0)
; #define FG_LDB(dst, b, h) do { _Pragma("unroll") for (int n = 0; n < 2; ++n) _Pragma("unroll") for (int k = 0; k < 2; ++k) dst[n][k] = *(const LAS bf16x8*)(lds + FG_SB(b, h) + boff + n * 2048 + k * 1024); } while (0)
; #define FG_MMA(ai, bj, At, Bt) do { __builtin_amdgcn_s_setprio(1); _Pragma("unroll") for (int m = 0; m < 4; ++m) _Pragma("unroll") for (int n = 0; n < 2; ++n) _Pragma("unroll") for (int k = 0; k < 2; ++k) \
;         acc[ai][bj][m][n] = __builtin_amdgcn_mfma_f32_16x16x32_bf16(Bt[n][k], At[m][k], acc[ai][bj][m][n], 0, 0, 0); __builtin_amdgcn_s_setprio(0); } while (0)
; #define FG_WAIT_V(n) asm volatile("s_waitcnt vmcnt(" #n ")" ::: "memory")
; #define FG_BAR __builtin_amdgcn_s_barrier()
; template <bool GATHER, class Unit, class Epi, class Sched>
; __device__ __forceinline__ void gemm_phase(LAS unsigned char* lds, const int K, const Sched& S, const Epi& E) {
;     ...
;         for (int t = 0; t < nt; t += 2) {
;             const bool last = (t == nt - 2);
;             const char* a1 = cA + (size_t)(t + 1) * kstep;
;             const char* a2 = last ? nA : cA + (size_t)(t + 2) * kstep; const char* b2 = last ? nB : cB + (size_t)(t + 2) * kstep;
;             const char* a3 = a2 + kstep; const char* b3 = b2 + kstep;
;             const unsigned x00 = (GATHER && last) ? vN00 : vA00, x01 = (GATHER && last) ? vN01 : vA01, x10 = (GATHER && last) ? vN10 : vA10, x11 = (GATHER && last) ? vN11 : vA11;
;             FG_LDB(B0, 0, 0); FG_LDB(B1, 0, 1); FG_SCHED; FG_LDA(At, 0, 0); FG_STAGE(FG_SA(1, 1), a1, vA10, vA11);
;             FG_WAIT_V(8); FG_WAIT_L(0); FG_BAR; FG_MMA(0, 0, At, B0); FG_MMA(0, 1, At, B1); FG_BAR; FG_SCHED;
;             FG_LDA(At, 0, 1); FG_STAGE(FG_SB(0, 0), b2, voffB0, voffB1); FG_STAGE(FG_SB(0, 1), b2 + hstepB, voffB0, voffB1); FG_STAGE(FG_SA(0, 0), a2, x00, x01);
.LBB0_446:
	ds_read_b128 v[130:133], v161
	ds_read_b128 v[134:137], v161 offset:1024
	ds_read_b128 v[172:175], v161 offset:2048
	ds_read_b128 v[176:179], v161 offset:3072
	ds_read_b128 v[180:183], v165
	ds_read_b128 v[184:187], v165 offset:1024
	ds_read_b128 v[188:191], v165 offset:2048
	ds_read_b128 v[192:195], v165 offset:3072
	s_add_u32 s48, s4, 0x100
	s_addc_u32 s49, s5, 0
	s_cmp_eq_u32 s76, 4
	s_cselect_b32 s53, s41, s49
	s_cselect_b32 s52, s72, s48
	s_cselect_b32 s51, s39, s75
	s_cselect_b32 s50, s73, s74
	v_lshl_add_u64 v[162:163], s[4:5], 0, v[154:155]
	s_add_i32 m0, s30, 0xc000
	ds_read_b128 v[196:199], v167
	ds_read_b128 v[200:203], v167 offset:1024
	ds_read_b128 v[204:207], v167 offset:2048
	ds_read_b128 v[208:211], v167 offset:3072
	ds_read_b128 v[212:215], v167 offset:4096
	ds_read_b128 v[216:219], v167 offset:5120
	ds_read_b128 v[220:223], v167 offset:6144
	ds_read_b128 v[224:227], v167 offset:7168
	global_load_lds_dwordx4 v[162:163], off
	v_lshl_add_u64 v[162:163], s[4:5], 0, v[152:153]
	s_add_i32 m0, s30, 0xe000
	s_nop 0
	global_load_lds_dwordx4 v[162:163], off
	s_waitcnt vmcnt(8)
	s_waitcnt lgkmcnt(0)
	s_barrier
	s_setprio 1
	s_waitcnt lgkmcnt(0)
	v_mfma_f32_16x16x32_bf16 v[126:129], v[130:133], v[196:199], v[126:129]
	v_mfma_f32_16x16x32_bf16 v[122:125], v[172:175], v[196:199], v[122:125]
	v_mfma_f32_16x16x32_bf16 v[118:121], v[130:133], v[204:207], v[118:121]
	v_mfma_f32_16x16x32_bf16 v[110:113], v[172:175], v[204:207], v[110:113]
	v_mfma_f32_16x16x32_bf16 v[102:105], v[130:133], v[212:215], v[102:105]
	v_mfma_f32_16x16x32_bf16 v[94:97], v[172:175], v[212:215], v[94:97]
	v_mfma_f32_16x16x32_bf16 v[86:89], v[130:133], v[220:223], v[86:89]
	v_mfma_f32_16x16x32_bf16 v[78:81], v[172:175], v[220:223], v[78:81]
	v_mfma_f32_16x16x32_bf16 v[126:129], v[134:137], v[200:203], v[126:129]
	v_mfma_f32_16x16x32_bf16 v[122:125], v[176:179], v[200:203], v[122:125]
	v_mfma_f32_16x16x32_bf16 v[118:121], v[134:137], v[208:211], v[118:121]
	v_mfma_f32_16x16x32_bf16 v[110:113], v[176:179], v[208:211], v[110:113]
	v_mfma_f32_16x16x32_bf16 v[102:105], v[134:137], v[216:219], v[102:105]
	v_mfma_f32_16x16x32_bf16 v[94:97], v[176:179], v[216:219], v[94:97]
	v_mfma_f32_16x16x32_bf16 v[86:89], v[134:137], v[224:227], v[86:89]
	v_mfma_f32_16x16x32_bf16 v[78:81], v[176:179], v[224:227], v[78:81]
	v_mfma_f32_16x16x32_bf16 v[114:117], v[180:183], v[196:199], v[114:117]
	v_mfma_f32_16x16x32_bf16 v[106:109], v[188:191], v[196:199], v[106:109]
	v_mfma_f32_16x16x32_bf16 v[98:101], v[180:183], v[204:207], v[98:101]
	v_mfma_f32_16x16x32_bf16 v[90:93], v[188:191], v[204:207], v[90:93]
	v_mfma_f32_16x16x32_bf16 v[82:85], v[180:183], v[212:215], v[82:85]
	v_mfma_f32_16x16x32_bf16 v[74:77], v[188:191], v[212:215], v[74:77]
	v_mfma_f32_16x16x32_bf16 v[70:73], v[180:183], v[220:223], v[70:73]
	v_mfma_f32_16x16x32_bf16 v[66:69], v[188:191], v[220:223], v[66:69]
	v_mfma_f32_16x16x32_bf16 v[114:117], v[184:187], v[200:203], v[114:117]
	v_mfma_f32_16x16x32_bf16 v[106:109], v[192:195], v[200:203], v[106:109]
	v_mfma_f32_16x16x32_bf16 v[98:101], v[184:187], v[208:211], v[98:101]
	v_mfma_f32_16x16x32_bf16 v[90:93], v[192:195], v[208:211], v[90:93]
	v_mfma_f32_16x16x32_bf16 v[82:85], v[184:187], v[216:219], v[82:85]
	v_mfma_f32_16x16x32_bf16 v[74:77], v[192:195], v[216:219], v[74:77]
	v_mfma_f32_16x16x32_bf16 v[70:73], v[184:187], v[224:227], v[70:73]
	v_mfma_f32_16x16x32_bf16 v[66:69], v[192:195], v[224:227], v[66:69]
	s_setprio 0
	s_barrier
	s_add_i32 s4, s61, s29
	v_lshl_add_u64 v[162:163], s[50:51], 0, v[138:139]
	s_mov_b32 m0, s4
	ds_read_b128 v[196:199], v167 offset:16384
	ds_read_b128 v[200:203], v167 offset:17408
	ds_read_b128 v[204:207], v167 offset:18432
	ds_read_b128 v[208:211], v167 offset:19456
	ds_read_b128 v[212:215], v167 offset:20480
	ds_read_b128 v[216:219], v167 offset:21504
	ds_read_b128 v[220:223], v167 offset:22528
	ds_read_b128 v[224:227], v167 offset:23552
	global_load_lds_dwordx4 v[162:163], off
	s_add_i32 m0, s4, 0x2000
	s_add_u32 s4, s50, 0x20000
	v_lshl_add_u64 v[228:229], s[50:51], 0, v[140:141]
	s_addc_u32 s5, s51, 0
	s_add_i32 s77, s62, s29
	global_load_lds_dwordx4 v[228:229], off
	v_lshl_add_u64 v[230:231], s[4:5], 0, v[138:139]
	s_mov_b32 m0, s77
	v_lshl_add_u64 v[232:233], s[52:53], 0, v[144:145]
	global_load_lds_dwordx4 v[230:231], off
	v_lshl_add_u64 v[230:231], s[4:5], 0, v[140:141]
	s_add_i32 m0, s77, 0x2000
	s_nop 0
	global_load_lds_dwordx4 v[230:231], off
	v_lshl_add_u64 v[230:231], s[52:53], 0, v[142:143]
	s_mov_b32 m0, s30
	s_nop 0
	global_load_lds_dwordx4 v[230:231], off
	s_mov_b32 m0, s31
	s_nop 0
	global_load_lds_dwordx4 v[232:233], off
	s_waitcnt vmcnt(8)
	s_waitcnt lgkmcnt(0)
	s_barrier
; #define FG_STAGE(bufoff, gbase, v0, v1) do { \
;         __builtin_amdgcn_global_load_lds((const unsigned*)((const char*)(gbase) + (v0)), (LAS unsigned*)(lds + (bufoff) + ldsw), 16, 0, 0); \
;         __builtin_amdgcn_global_load_lds((const unsigned*)((const char*)(gbase) + (v1)), (LAS unsigned*)(lds + (bufoff) + ldsw + 8192), 16, 0, 0); } while (0)
; #define FG_LDA(dst, b, h) do { _Pragma("unroll") for (int m = 0; m < 4; ++m) _Pragma("unroll") for (int k = 0; k < 2; ++k) dst[m][k] = *(const LAS bf16x8*)(lds + FG_SA(b, h) + aoff + m * 2048 + k * 1024); } while (0)
; #define FG_LDB(dst, b, h) do { _Pragma("unroll") for (int n = 0; n < 2; ++n) _Pragma("unroll") for (int k = 0; k < 2; ++k) dst[n][k] = *(const LAS bf16x8*)(lds + FG_SB(b, h) + boff + n * 2048 + k * 1024); } while (0)
; #define FG_MMA(ai, bj, At, Bt) do { __builtin_amdgcn_s_setprio(1); _Pragma("unroll") for (int m = 0; m < 4; ++m) _Pragma("unroll") for (int n = 0; n < 2; ++n) _Pragma("unroll") for (int k = 0; k < 2; ++k) \
;         acc[ai][bj][m][n] = __builtin_amdgcn_mfma_f32_16x16x32_bf16(Bt[n][k], At[m][k], acc[ai][bj][m][n], 0, 0, 0); __builtin_amdgcn_s_setprio(0); } while (0)
; #define FG_WAIT_V(n) asm volatile("s_waitcnt vmcnt(" #n ")" ::: "memory")
; #define FG_WAIT_L(n) asm volatile("s_waitcnt lgkmcnt(" #n ")" ::: "memory")
; #define FG_BAR __builtin_amdgcn_s_barrier()
; #define FG_SCHED __builtin_amdgcn_sched_barrier(0)
; template <bool GATHER, class Unit, class Epi, class Sched>
; __device__ __forceinline__ void gemm_phase(LAS unsigned char* lds, const int K, const Sched& S, const Epi& E) {
;     ...
;             FG_LDA(At, 0, 1); FG_STAGE(FG_SB(0, 0), b2, voffB0, voffB1); FG_STAGE(FG_SB(0, 1), b2 + hstepB, voffB0, voffB1); FG_STAGE(FG_SA(0, 0), a2, x00, x01);
;             FG_WAIT_V(8); FG_WAIT_L(0); FG_BAR; if (hi_on) { FG_MMA(1, 0, At, B0); FG_MMA(1, 1, At, B1); } FG_BAR; FG_SCHED;
;             FG_LDB(B0, 1, 0); FG_LDB(B1, 1, 1); FG_SCHED; FG_LDA(At, 1, 0); FG_STAGE(FG_SA(0, 1), a2, x10, x11);
;             FG_WAIT_V(8); FG_WAIT_L(0); FG_BAR; FG_MMA(0, 0, At, B0); FG_MMA(0, 1, At, B1); FG_BAR; FG_SCHED;
;             FG_LDA(At, 1, 1); FG_STAGE(FG_SB(1, 0), b3, voffB0, voffB1); FG_STAGE(FG_SB(1, 1), b3 + hstepB, voffB0, voffB1); FG_STAGE(FG_SA(1, 0), a3, x00, x01);
	s_setprio 1
	s_waitcnt lgkmcnt(0)
	v_mfma_f32_16x16x32_bf16 v[62:65], v[130:133], v[196:199], v[62:65]
	v_mfma_f32_16x16x32_bf16 v[58:61], v[172:175], v[196:199], v[58:61]
	v_mfma_f32_16x16x32_bf16 v[54:57], v[130:133], v[204:207], v[54:57]
	v_mfma_f32_16x16x32_bf16 v[46:49], v[172:175], v[204:207], v[46:49]
	v_mfma_f32_16x16x32_bf16 v[38:41], v[130:133], v[212:215], v[38:41]
	v_mfma_f32_16x16x32_bf16 v[30:33], v[172:175], v[212:215], v[30:33]
	v_mfma_f32_16x16x32_bf16 v[22:25], v[130:133], v[220:223], v[22:25]
	v_mfma_f32_16x16x32_bf16 v[14:17], v[172:175], v[220:223], v[14:17]
	v_mfma_f32_16x16x32_bf16 v[62:65], v[134:137], v[200:203], v[62:65]
	v_mfma_f32_16x16x32_bf16 v[58:61], v[176:179], v[200:203], v[58:61]
	v_mfma_f32_16x16x32_bf16 v[54:57], v[134:137], v[208:211], v[54:57]
	v_mfma_f32_16x16x32_bf16 v[46:49], v[176:179], v[208:211], v[46:49]
	v_mfma_f32_16x16x32_bf16 v[38:41], v[134:137], v[216:219], v[38:41]
	v_mfma_f32_16x16x32_bf16 v[30:33], v[176:179], v[216:219], v[30:33]
	v_mfma_f32_16x16x32_bf16 v[22:25], v[134:137], v[224:227], v[22:25]
	v_mfma_f32_16x16x32_bf16 v[14:17], v[176:179], v[224:227], v[14:17]
	v_mfma_f32_16x16x32_bf16 v[50:53], v[180:183], v[196:199], v[50:53]
	v_mfma_f32_16x16x32_bf16 v[42:45], v[188:191], v[196:199], v[42:45]
	v_mfma_f32_16x16x32_bf16 v[34:37], v[180:183], v[204:207], v[34:37]
	v_mfma_f32_16x16x32_bf16 v[26:29], v[188:191], v[204:207], v[26:29]
	v_mfma_f32_16x16x32_bf16 v[18:21], v[180:183], v[212:215], v[18:21]
	v_mfma_f32_16x16x32_bf16 v[10:13], v[188:191], v[212:215], v[10:13]
	v_mfma_f32_16x16x32_bf16 v[6:9], v[180:183], v[220:223], v[6:9]
	v_mfma_f32_16x16x32_bf16 v[2:5], v[188:191], v[220:223], v[2:5]
	v_mfma_f32_16x16x32_bf16 v[50:53], v[184:187], v[200:203], v[50:53]
	v_mfma_f32_16x16x32_bf16 v[42:45], v[192:195], v[200:203], v[42:45]
	v_mfma_f32_16x16x32_bf16 v[34:37], v[184:187], v[208:211], v[34:37]
	v_mfma_f32_16x16x32_bf16 v[26:29], v[192:195], v[208:211], v[26:29]
	v_mfma_f32_16x16x32_bf16 v[18:21], v[184:187], v[216:219], v[18:21]
	v_mfma_f32_16x16x32_bf16 v[10:13], v[192:195], v[216:219], v[10:13]
	v_mfma_f32_16x16x32_bf16 v[6:9], v[184:187], v[224:227], v[6:9]
	v_mfma_f32_16x16x32_bf16 v[2:5], v[192:195], v[224:227], v[2:5]
	s_setprio 0
	s_barrier
	s_add_i32 s4, 0, 0x18000
	v_add_u32_e32 v150, s4, v1
	s_add_i32 s77, 0, 0x1c000
	ds_read_b128 v[130:133], v150
	ds_read_b128 v[134:137], v150 offset:1024
	ds_read_b128 v[172:175], v150 offset:2048
	ds_read_b128 v[176:179], v150 offset:3072
	v_add_u32_e32 v150, s77, v1
	ds_read_b128 v[180:183], v150
	ds_read_b128 v[184:187], v150 offset:1024
	ds_read_b128 v[188:191], v150 offset:2048
	ds_read_b128 v[192:195], v150 offset:3072
	s_mov_b32 m0, s33
	v_lshl_add_u64 v[234:235], s[52:53], 0, v[146:147]
	ds_read_b128 v[196:199], v167 offset:32768
	ds_read_b128 v[200:203], v167 offset:33792
	ds_read_b128 v[204:207], v167 offset:34816
	ds_read_b128 v[208:211], v167 offset:35840
	ds_read_b128 v[212:215], v167 offset:36864
	ds_read_b128 v[216:219], v167 offset:37888
	ds_read_b128 v[220:223], v167 offset:38912
	ds_read_b128 v[224:227], v167 offset:39936
	global_load_lds_dwordx4 v[234:235], off
	v_lshl_add_u64 v[234:235], s[52:53], 0, v[148:149]
	s_mov_b32 m0, s35
	s_nop 0
	global_load_lds_dwordx4 v[234:235], off
	s_waitcnt vmcnt(8)
	s_waitcnt lgkmcnt(0)
	s_barrier
	s_setprio 1
	s_waitcnt lgkmcnt(0)
	v_mfma_f32_16x16x32_bf16 v[126:129], v[130:133], v[196:199], v[126:129]
	v_mfma_f32_16x16x32_bf16 v[122:125], v[172:175], v[196:199], v[122:125]
	v_mfma_f32_16x16x32_bf16 v[118:121], v[130:133], v[204:207], v[118:121]
	v_mfma_f32_16x16x32_bf16 v[110:113], v[172:175], v[204:207], v[110:113]
	v_mfma_f32_16x16x32_bf16 v[102:105], v[130:133], v[212:215], v[102:105]
	v_mfma_f32_16x16x32_bf16 v[94:97], v[172:175], v[212:215], v[94:97]
	v_mfma_f32_16x16x32_bf16 v[86:89], v[130:133], v[220:223], v[86:89]
	v_mfma_f32_16x16x32_bf16 v[78:81], v[172:175], v[220:223], v[78:81]
	v_mfma_f32_16x16x32_bf16 v[126:129], v[134:137], v[200:203], v[126:129]
	v_mfma_f32_16x16x32_bf16 v[122:125], v[176:179], v[200:203], v[122:125]
	v_mfma_f32_16x16x32_bf16 v[118:121], v[134:137], v[208:211], v[118:121]
	v_mfma_f32_16x16x32_bf16 v[110:113], v[176:179], v[208:211], v[110:113]
	v_mfma_f32_16x16x32_bf16 v[102:105], v[134:137], v[216:219], v[102:105]
	v_mfma_f32_16x16x32_bf16 v[94:97], v[176:179], v[216:219], v[94:97]
	v_mfma_f32_16x16x32_bf16 v[86:89], v[134:137], v[224:227], v[86:89]
	v_mfma_f32_16x16x32_bf16 v[78:81], v[176:179], v[224:227], v[78:81]
	v_mfma_f32_16x16x32_bf16 v[114:117], v[180:183], v[196:199], v[114:117]
	v_mfma_f32_16x16x32_bf16 v[106:109], v[188:191], v[196:199], v[106:109]
	v_mfma_f32_16x16x32_bf16 v[98:101], v[180:183], v[204:207], v[98:101]
	v_mfma_f32_16x16x32_bf16 v[90:93], v[188:191], v[204:207], v[90:93]
	v_mfma_f32_16x16x32_bf16 v[82:85], v[180:183], v[212:215], v[82:85]
	v_mfma_f32_16x16x32_bf16 v[74:77], v[188:191], v[212:215], v[74:77]
	v_mfma_f32_16x16x32_bf16 v[70:73], v[180:183], v[220:223], v[70:73]
	v_mfma_f32_16x16x32_bf16 v[66:69], v[188:191], v[220:223], v[66:69]
	v_mfma_f32_16x16x32_bf16 v[114:117], v[184:187], v[200:203], v[114:117]
	v_mfma_f32_16x16x32_bf16 v[106:109], v[192:195], v[200:203], v[106:109]
	v_mfma_f32_16x16x32_bf16 v[98:101], v[184:187], v[208:211], v[98:101]
	v_mfma_f32_16x16x32_bf16 v[90:93], v[192:195], v[208:211], v[90:93]
	v_mfma_f32_16x16x32_bf16 v[82:85], v[184:187], v[216:219], v[82:85]
	v_mfma_f32_16x16x32_bf16 v[74:77], v[192:195], v[216:219], v[74:77]
	v_mfma_f32_16x16x32_bf16 v[70:73], v[184:187], v[224:227], v[70:73]
	v_mfma_f32_16x16x32_bf16 v[66:69], v[192:195], v[224:227], v[66:69]
	s_setprio 0
	s_barrier
; #define FG_STAGE(bufoff, gbase, v0, v1) do { \
;         __builtin_amdgcn_global_load_lds((const unsigned*)((const char*)(gbase) + (v0)), (LAS unsigned*)(lds + (bufoff) + ldsw), 16, 0, 0); \
;         __builtin_amdgcn_global_load_lds((const unsigned*)((const char*)(gbase) + (v1)), (LAS unsigned*)(lds + (bufoff) + ldsw + 8192), 16, 0, 0); } while (0)
; #define FG_LDA(dst, b, h) do { _Pragma("unroll") for (int m = 0; m < 4; ++m) _Pragma("unroll") for (int k = 0; k < 2; ++k) dst[m][k] = *(const LAS bf16x8*)(lds + FG_SA(b, h) + aoff + m * 2048 + k * 1024); } while (0)
; #define FG_MMA(ai, bj, At, Bt) do { __builtin_amdgcn_s_setprio(1); _Pragma("unroll") for (int m = 0; m < 4; ++m) _Pragma("unroll") for (int n = 0; n < 2; ++n) _Pragma("unroll") for (int k = 0; k < 2; ++k) \
;         acc[ai][bj][m][n] = __builtin_amdgcn_mfma_f32_16x16x32_bf16(Bt[n][k], At[m][k], acc[ai][bj][m][n], 0, 0, 0); __builtin_amdgcn_s_setprio(0); } while (0)
; #define FG_WAIT_V(n) asm volatile("s_waitcnt vmcnt(" #n ")" ::: "memory")
; #define FG_WAIT_L(n) asm volatile("s_waitcnt lgkmcnt(" #n ")" ::: "memory")
; #define FG_BAR __builtin_amdgcn_s_barrier()
; #define FG_SCHED __builtin_amdgcn_sched_barrier(0)
; template <bool GATHER, class Unit, class Epi, class Sched>
; __device__ __forceinline__ void gemm_phase(LAS unsigned char* lds, const int K, const Sched& S, const Epi& E) {
;     ...
;             FG_LDA(At, 1, 1); FG_STAGE(FG_SB(1, 0), b3, voffB0, voffB1); FG_STAGE(FG_SB(1, 1), b3 + hstepB, voffB0, voffB1); FG_STAGE(FG_SA(1, 0), a3, x00, x01);
;             FG_WAIT_V(8); FG_WAIT_L(0); FG_BAR; if (hi_on) { FG_MMA(1, 0, At, B0); FG_MMA(1, 1, At, B1); } FG_BAR; FG_SCHED;
;         }
;         if (wr == 0) FG_BAR;
	s_add_i32 s4, s4, s29
	v_lshl_add_u64 v[162:163], v[162:163], 0, s[12:13]
	s_mov_b32 m0, s4
	ds_read_b128 v[196:199], v167 offset:49152
	ds_read_b128 v[200:203], v167 offset:50176
	ds_read_b128 v[204:207], v167 offset:51200
	ds_read_b128 v[208:211], v167 offset:52224
	ds_read_b128 v[212:215], v167 offset:53248
	ds_read_b128 v[216:219], v167 offset:54272
	ds_read_b128 v[220:223], v167 offset:55296
	ds_read_b128 v[224:227], v167 offset:56320
	global_load_lds_dwordx4 v[162:163], off
	s_add_i32 m0, s4, 0x2000
	s_add_u32 s4, s50, 0x20080
	v_lshl_add_u64 v[162:163], v[228:229], 0, s[12:13]
	s_addc_u32 s5, s51, 0
	s_add_i32 s50, s77, s29
	global_load_lds_dwordx4 v[162:163], off
	v_lshl_add_u64 v[162:163], s[4:5], 0, v[138:139]
	s_mov_b32 m0, s50
	s_nop 0
	global_load_lds_dwordx4 v[162:163], off
	v_lshl_add_u64 v[162:163], s[4:5], 0, v[140:141]
	s_add_i32 m0, s50, 0x2000
	s_nop 0
	global_load_lds_dwordx4 v[162:163], off
	v_lshl_add_u64 v[162:163], v[230:231], 0, s[12:13]
	s_mov_b32 m0, s58
	s_nop 0
	global_load_lds_dwordx4 v[162:163], off
	v_lshl_add_u64 v[162:163], v[232:233], 0, s[12:13]
	s_mov_b32 m0, s59
	s_nop 0
	global_load_lds_dwordx4 v[162:163], off
	s_waitcnt vmcnt(8)
	s_waitcnt lgkmcnt(0)
	s_barrier
	s_setprio 1
	s_waitcnt lgkmcnt(0)
	v_mfma_f32_16x16x32_bf16 v[62:65], v[130:133], v[196:199], v[62:65]
	v_mfma_f32_16x16x32_bf16 v[58:61], v[172:175], v[196:199], v[58:61]
	v_mfma_f32_16x16x32_bf16 v[54:57], v[130:133], v[204:207], v[54:57]
	v_mfma_f32_16x16x32_bf16 v[46:49], v[172:175], v[204:207], v[46:49]
	v_mfma_f32_16x16x32_bf16 v[38:41], v[130:133], v[212:215], v[38:41]
	v_mfma_f32_16x16x32_bf16 v[30:33], v[172:175], v[212:215], v[30:33]
	v_mfma_f32_16x16x32_bf16 v[22:25], v[130:133], v[220:223], v[22:25]
	v_mfma_f32_16x16x32_bf16 v[14:17], v[172:175], v[220:223], v[14:17]
	v_mfma_f32_16x16x32_bf16 v[62:65], v[134:137], v[200:203], v[62:65]
	v_mfma_f32_16x16x32_bf16 v[58:61], v[176:179], v[200:203], v[58:61]
	v_mfma_f32_16x16x32_bf16 v[54:57], v[134:137], v[208:211], v[54:57]
	v_mfma_f32_16x16x32_bf16 v[46:49], v[176:179], v[208:211], v[46:49]
	v_mfma_f32_16x16x32_bf16 v[38:41], v[134:137], v[216:219], v[38:41]
	v_mfma_f32_16x16x32_bf16 v[30:33], v[176:179], v[216:219], v[30:33]
	v_mfma_f32_16x16x32_bf16 v[22:25], v[134:137], v[224:227], v[22:25]
	v_mfma_f32_16x16x32_bf16 v[14:17], v[176:179], v[224:227], v[14:17]
	v_mfma_f32_16x16x32_bf16 v[50:53], v[180:183], v[196:199], v[50:53]
	v_mfma_f32_16x16x32_bf16 v[42:45], v[188:191], v[196:199], v[42:45]
	v_mfma_f32_16x16x32_bf16 v[34:37], v[180:183], v[204:207], v[34:37]
	v_mfma_f32_16x16x32_bf16 v[26:29], v[188:191], v[204:207], v[26:29]
	v_mfma_f32_16x16x32_bf16 v[18:21], v[180:183], v[212:215], v[18:21]
	v_mfma_f32_16x16x32_bf16 v[10:13], v[188:191], v[212:215], v[10:13]
	v_mfma_f32_16x16x32_bf16 v[6:9], v[180:183], v[220:223], v[6:9]
	v_mfma_f32_16x16x32_bf16 v[2:5], v[188:191], v[220:223], v[2:5]
	v_mfma_f32_16x16x32_bf16 v[50:53], v[184:187], v[200:203], v[50:53]
	v_mfma_f32_16x16x32_bf16 v[42:45], v[192:195], v[200:203], v[42:45]
	v_mfma_f32_16x16x32_bf16 v[34:37], v[184:187], v[208:211], v[34:37]
	v_mfma_f32_16x16x32_bf16 v[26:29], v[192:195], v[208:211], v[26:29]
	v_mfma_f32_16x16x32_bf16 v[18:21], v[184:187], v[216:219], v[18:21]
	v_mfma_f32_16x16x32_bf16 v[10:13], v[192:195], v[216:219], v[10:13]
	v_mfma_f32_16x16x32_bf16 v[6:9], v[184:187], v[224:227], v[6:9]
	v_mfma_f32_16x16x32_bf16 v[2:5], v[192:195], v[224:227], v[2:5]
	s_setprio 0
	s_barrier
	s_add_i32 s76, s76, 2
	s_add_u32 s74, s74, 0x100
	s_addc_u32 s75, s75, 0
	s_cmp_gt_u32 s76, 5
	s_mov_b64 s[4:5], s[48:49]
	s_cbranch_scc0 .LBB0_446
	s_and_b64 vcc, exec, s[14:15]
	s_cbranch_vccz .LBB0_449
	s_barrier

; #define FG_STAGE(bufoff, gbase, v0, v1) do { \
;         __builtin_amdgcn_global_load_lds((const unsigned*)((const char*)(gbase) + (v0)), (LAS unsigned*)(lds + (bufoff) + ldsw), 16, 0, 0); \
;         __builtin_amdgcn_global_load_lds((const unsigned*)((const char*)(gbase) + (v1)), (LAS unsigned*)(lds + (bufoff) + ldsw + 8192), 16, 0, 0); } while (0)
; #define FG_LDA(dst, b, h) do { _Pragma("unroll") for (int m = 0; m < 4; ++m) _Pragma("unroll") for (int k = 0; k < 2; ++k) dst[m][k] = *(const LAS bf16x8*)(lds + FG_SA(b, h) + aoff + m * 2048 + k * 1024); } while (0)
; #define FG_LDB(dst, b, h) do { _Pragma("unroll") for (int n = 0; n < 2; ++n) _Pragma("unroll") for (int k = 0; k < 2; ++k) dst[n][k] = *(const LAS bf16x8*)(lds + FG_SB(b, h) + boff + n * 2048 + k * 1024); } while (0)
; #define FG_MMA(ai, bj, At, Bt) do { __builtin_amdgcn_s_setprio(1); _Pragma("unroll") for (int m = 0; m < 4; ++m) _Pragma("unroll") for (int n = 0; n < 2; ++n) _Pragma("unroll") for (int k = 0; k < 2; ++k) \
;         acc[ai][bj][m][n] = __builtin_amdgcn_mfma_f32_16x16x32_bf16(Bt[n][k], At[m][k], acc[ai][bj][m][n], 0, 0, 0); __builtin_amdgcn_s_setprio(0); } while (0)
; #define FG_WAIT_V(n) asm volatile("s_waitcnt vmcnt(" #n ")" ::: "memory")
; #define FG_BAR __builtin_amdgcn_s_barrier()
; template <bool GATHER, class Unit, class Epi, class Sched>
; __device__ __forceinline__ void gemm_phase(LAS unsigned char* lds, const int K, const Sched& S, const Epi& E) {
;     ...
;         for (int t = 0; t < nt; t += 2) {
;             const bool last = (t == nt - 2);
;             const char* a1 = cA + (size_t)(t + 1) * kstep;
;             const char* a2 = last ? nA : cA + (size_t)(t + 2) * kstep; const char* b2 = last ? nB : cB + (size_t)(t + 2) * kstep;
;             const char* a3 = a2 + kstep; const char* b3 = b2 + kstep;
;             const unsigned x00 = (GATHER && last) ? vN00 : vA00, x01 = (GATHER && last) ? vN01 : vA01, x10 = (GATHER && last) ? vN10 : vA10, x11 = (GATHER && last) ? vN11 : vA11;
;             FG_LDB(B0, 0, 0); FG_LDB(B1, 0, 1); FG_SCHED; FG_LDA(At, 0, 0); FG_STAGE(FG_SA(1, 1), a1, vA10, vA11);
;             FG_WAIT_V(8); FG_WAIT_L(0); FG_BAR; FG_MMA(0, 0, At, B0); FG_MMA(0, 1, At, B1); FG_BAR; FG_SCHED;
;             FG_LDA(At, 0, 1); FG_STAGE(FG_SB(0, 0), b2, voffB0, voffB1); FG_STAGE(FG_SB(0, 1), b2 + hstepB, voffB0, voffB1); FG_STAGE(FG_SA(0, 0), a2, x00, x01);
.LBB0_652:
	ds_read_b128 v[66:69], v237
	ds_read_b128 v[70:73], v237 offset:1024
	ds_read_b128 v[74:77], v237 offset:2048
	ds_read_b128 v[78:81], v237 offset:3072
	ds_read_b128 v[138:141], v238
	ds_read_b128 v[142:145], v238 offset:1024
	ds_read_b128 v[154:157], v238 offset:2048
	ds_read_b128 v[158:161], v238 offset:3072
	s_add_u32 s44, s40, 0x100
	s_addc_u32 s45, s41, 0
	s_cmp_eq_u32 s60, 28
	s_cselect_b32 s49, s7, s45
	s_cselect_b32 s48, s35, s44
	s_cselect_b32 s47, s25, s59
	s_cselect_b32 s46, s43, s58
	v_lshl_add_u64 v[194:195], s[40:41], 0, v[218:219]
	s_add_i32 m0, s28, 0xc000
	ds_read_b128 v[162:165], v239
	ds_read_b128 v[166:169], v239 offset:1024
	ds_read_b128 v[170:173], v239 offset:2048
	ds_read_b128 v[174:177], v239 offset:3072
	ds_read_b128 v[178:181], v239 offset:4096
	ds_read_b128 v[182:185], v239 offset:5120
	ds_read_b128 v[186:189], v239 offset:6144
	ds_read_b128 v[190:193], v239 offset:7168
	global_load_lds_dwordx4 v[194:195], off
	v_lshl_add_u64 v[194:195], s[40:41], 0, v[216:217]
	s_add_i32 m0, s28, 0xe000
	s_nop 0
	global_load_lds_dwordx4 v[194:195], off
	s_waitcnt vmcnt(8)
	s_waitcnt lgkmcnt(0)
	s_barrier
	s_setprio 1
	s_waitcnt lgkmcnt(0)
	v_mfma_f32_16x16x32_bf16 v[150:153], v[66:69], v[162:165], v[150:153]
	v_mfma_f32_16x16x32_bf16 v[146:149], v[74:77], v[162:165], v[146:149]
	v_mfma_f32_16x16x32_bf16 v[126:129], v[66:69], v[170:173], v[126:129]
	v_mfma_f32_16x16x32_bf16 v[122:125], v[74:77], v[170:173], v[122:125]
	v_mfma_f32_16x16x32_bf16 v[110:113], v[66:69], v[178:181], v[110:113]
	v_mfma_f32_16x16x32_bf16 v[106:109], v[74:77], v[178:181], v[106:109]
	v_mfma_f32_16x16x32_bf16 v[94:97], v[66:69], v[186:189], v[94:97]
	v_mfma_f32_16x16x32_bf16 v[90:93], v[74:77], v[186:189], v[90:93]
	v_mfma_f32_16x16x32_bf16 v[150:153], v[70:73], v[166:169], v[150:153]
	v_mfma_f32_16x16x32_bf16 v[146:149], v[78:81], v[166:169], v[146:149]
	v_mfma_f32_16x16x32_bf16 v[126:129], v[70:73], v[174:177], v[126:129]
	v_mfma_f32_16x16x32_bf16 v[122:125], v[78:81], v[174:177], v[122:125]
	v_mfma_f32_16x16x32_bf16 v[110:113], v[70:73], v[182:185], v[110:113]
	v_mfma_f32_16x16x32_bf16 v[106:109], v[78:81], v[182:185], v[106:109]
	v_mfma_f32_16x16x32_bf16 v[94:97], v[70:73], v[190:193], v[94:97]
	v_mfma_f32_16x16x32_bf16 v[90:93], v[78:81], v[190:193], v[90:93]
	v_mfma_f32_16x16x32_bf16 v[134:137], v[138:141], v[162:165], v[134:137]
	v_mfma_f32_16x16x32_bf16 v[130:133], v[154:157], v[162:165], v[130:133]
	v_mfma_f32_16x16x32_bf16 v[118:121], v[138:141], v[170:173], v[118:121]
	v_mfma_f32_16x16x32_bf16 v[114:117], v[154:157], v[170:173], v[114:117]
	v_mfma_f32_16x16x32_bf16 v[102:105], v[138:141], v[178:181], v[102:105]
	v_mfma_f32_16x16x32_bf16 v[98:101], v[154:157], v[178:181], v[98:101]
	v_mfma_f32_16x16x32_bf16 v[86:89], v[138:141], v[186:189], v[86:89]
	v_mfma_f32_16x16x32_bf16 v[82:85], v[154:157], v[186:189], v[82:85]
	v_mfma_f32_16x16x32_bf16 v[134:137], v[142:145], v[166:169], v[134:137]
	v_mfma_f32_16x16x32_bf16 v[130:133], v[158:161], v[166:169], v[130:133]
	v_mfma_f32_16x16x32_bf16 v[118:121], v[142:145], v[174:177], v[118:121]
	v_mfma_f32_16x16x32_bf16 v[114:117], v[158:161], v[174:177], v[114:117]
	v_mfma_f32_16x16x32_bf16 v[102:105], v[142:145], v[182:185], v[102:105]
	v_mfma_f32_16x16x32_bf16 v[98:101], v[158:161], v[182:185], v[98:101]
	v_mfma_f32_16x16x32_bf16 v[86:89], v[142:145], v[190:193], v[86:89]
	v_mfma_f32_16x16x32_bf16 v[82:85], v[158:161], v[190:193], v[82:85]
	s_setprio 0
	s_barrier
	s_add_i32 s40, s56, s27
	v_lshl_add_u64 v[194:195], s[46:47], 0, v[202:203]
	s_mov_b32 m0, s40
	ds_read_b128 v[162:165], v239 offset:16384
	ds_read_b128 v[166:169], v239 offset:17408
	ds_read_b128 v[170:173], v239 offset:18432
	ds_read_b128 v[174:177], v239 offset:19456
	ds_read_b128 v[178:181], v239 offset:20480
	ds_read_b128 v[182:185], v239 offset:21504
	ds_read_b128 v[186:189], v239 offset:22528
	ds_read_b128 v[190:193], v239 offset:23552
	global_load_lds_dwordx4 v[194:195], off
	s_add_i32 m0, s40, 0x2000
	s_add_u32 s40, s46, 0x80000
	v_lshl_add_u64 v[196:197], s[46:47], 0, v[204:205]
	s_addc_u32 s41, s47, 0
	s_add_i32 s61, s57, s27
	global_load_lds_dwordx4 v[196:197], off
	v_lshl_add_u64 v[198:199], s[40:41], 0, v[202:203]
	s_mov_b32 m0, s61
	v_lshl_add_u64 v[200:201], s[48:49], 0, v[208:209]
	global_load_lds_dwordx4 v[198:199], off
	v_lshl_add_u64 v[198:199], s[40:41], 0, v[204:205]
	s_add_i32 m0, s61, 0x2000
	s_nop 0
	global_load_lds_dwordx4 v[198:199], off
	v_lshl_add_u64 v[198:199], s[48:49], 0, v[206:207]
	s_mov_b32 m0, s28
	s_nop 0
	global_load_lds_dwordx4 v[198:199], off
	s_mov_b32 m0, s29
	s_nop 0
	global_load_lds_dwordx4 v[200:201], off
	s_waitcnt vmcnt(8)
	s_waitcnt lgkmcnt(0)
	s_barrier
; #define FG_STAGE(bufoff, gbase, v0, v1) do { \
;         __builtin_amdgcn_global_load_lds((const unsigned*)((const char*)(gbase) + (v0)), (LAS unsigned*)(lds + (bufoff) + ldsw), 16, 0, 0); \
;         __builtin_amdgcn_global_load_lds((const unsigned*)((const char*)(gbase) + (v1)), (LAS unsigned*)(lds + (bufoff) + ldsw + 8192), 16, 0, 0); } while (0)
; #define FG_LDA(dst, b, h) do { _Pragma("unroll") for (int m = 0; m < 4; ++m) _Pragma("unroll") for (int k = 0; k < 2; ++k) dst[m][k] = *(const LAS bf16x8*)(lds + FG_SA(b, h) + aoff + m * 2048 + k * 1024); } while (0)
; #define FG_LDB(dst, b, h) do { _Pragma("unroll") for (int n = 0; n < 2; ++n) _Pragma("unroll") for (int k = 0; k < 2; ++k) dst[n][k] = *(const LAS bf16x8*)(lds + FG_SB(b, h) + boff + n * 2048 + k * 1024); } while (0)
; #define FG_MMA(ai, bj, At, Bt) do { __builtin_amdgcn_s_setprio(1); _Pragma("unroll") for (int m = 0; m < 4; ++m) _Pragma("unroll") for (int n = 0; n < 2; ++n) _Pragma("unroll") for (int k = 0; k < 2; ++k) \
;         acc[ai][bj][m][n] = __builtin_amdgcn_mfma_f32_16x16x32_bf16(Bt[n][k], At[m][k], acc[ai][bj][m][n], 0, 0, 0); __builtin_amdgcn_s_setprio(0); } while (0)
; #define FG_WAIT_V(n) asm volatile("s_waitcnt vmcnt(" #n ")" ::: "memory")
; #define FG_WAIT_L(n) asm volatile("s_waitcnt lgkmcnt(" #n ")" ::: "memory")
; #define FG_BAR __builtin_amdgcn_s_barrier()
; #define FG_SCHED __builtin_amdgcn_sched_barrier(0)
; template <bool GATHER, class Unit, class Epi, class Sched>
; __device__ __forceinline__ void gemm_phase(LAS unsigned char* lds, const int K, const Sched& S, const Epi& E) {
;     ...
;             FG_LDA(At, 0, 1); FG_STAGE(FG_SB(0, 0), b2, voffB0, voffB1); FG_STAGE(FG_SB(0, 1), b2 + hstepB, voffB0, voffB1); FG_STAGE(FG_SA(0, 0), a2, x00, x01);
;             FG_WAIT_V(8); FG_WAIT_L(0); FG_BAR; if (hi_on) { FG_MMA(1, 0, At, B0); FG_MMA(1, 1, At, B1); } FG_BAR; FG_SCHED;
;             FG_LDB(B0, 1, 0); FG_LDB(B1, 1, 1); FG_SCHED; FG_LDA(At, 1, 0); FG_STAGE(FG_SA(0, 1), a2, x10, x11);
;             FG_WAIT_V(8); FG_WAIT_L(0); FG_BAR; FG_MMA(0, 0, At, B0); FG_MMA(0, 1, At, B1); FG_BAR; FG_SCHED;
;             FG_LDA(At, 1, 1); FG_STAGE(FG_SB(1, 0), b3, voffB0, voffB1); FG_STAGE(FG_SB(1, 1), b3 + hstepB, voffB0, voffB1); FG_STAGE(FG_SA(1, 0), a3, x00, x01);
	s_setprio 1
	s_waitcnt lgkmcnt(0)
	v_mfma_f32_16x16x32_bf16 v[62:65], v[66:69], v[162:165], v[62:65]
	v_mfma_f32_16x16x32_bf16 v[58:61], v[74:77], v[162:165], v[58:61]
	v_mfma_f32_16x16x32_bf16 v[46:49], v[66:69], v[170:173], v[46:49]
	v_mfma_f32_16x16x32_bf16 v[42:45], v[74:77], v[170:173], v[42:45]
	v_mfma_f32_16x16x32_bf16 v[30:33], v[66:69], v[178:181], v[30:33]
	v_mfma_f32_16x16x32_bf16 v[26:29], v[74:77], v[178:181], v[26:29]
	v_mfma_f32_16x16x32_bf16 v[14:17], v[66:69], v[186:189], v[14:17]
	v_mfma_f32_16x16x32_bf16 v[10:13], v[74:77], v[186:189], v[10:13]
	v_mfma_f32_16x16x32_bf16 v[62:65], v[70:73], v[166:169], v[62:65]
	v_mfma_f32_16x16x32_bf16 v[58:61], v[78:81], v[166:169], v[58:61]
	v_mfma_f32_16x16x32_bf16 v[46:49], v[70:73], v[174:177], v[46:49]
	v_mfma_f32_16x16x32_bf16 v[42:45], v[78:81], v[174:177], v[42:45]
	v_mfma_f32_16x16x32_bf16 v[30:33], v[70:73], v[182:185], v[30:33]
	v_mfma_f32_16x16x32_bf16 v[26:29], v[78:81], v[182:185], v[26:29]
	v_mfma_f32_16x16x32_bf16 v[14:17], v[70:73], v[190:193], v[14:17]
	v_mfma_f32_16x16x32_bf16 v[10:13], v[78:81], v[190:193], v[10:13]
	v_mfma_f32_16x16x32_bf16 v[54:57], v[138:141], v[162:165], v[54:57]
	v_mfma_f32_16x16x32_bf16 v[50:53], v[154:157], v[162:165], v[50:53]
	v_mfma_f32_16x16x32_bf16 v[38:41], v[138:141], v[170:173], v[38:41]
	v_mfma_f32_16x16x32_bf16 v[34:37], v[154:157], v[170:173], v[34:37]
	v_mfma_f32_16x16x32_bf16 v[22:25], v[138:141], v[178:181], v[22:25]
	v_mfma_f32_16x16x32_bf16 v[18:21], v[154:157], v[178:181], v[18:21]
	v_mfma_f32_16x16x32_bf16 v[6:9], v[138:141], v[186:189], v[6:9]
	v_mfma_f32_16x16x32_bf16 v[2:5], v[154:157], v[186:189], v[2:5]
	v_mfma_f32_16x16x32_bf16 v[54:57], v[142:145], v[166:169], v[54:57]
	v_mfma_f32_16x16x32_bf16 v[50:53], v[158:161], v[166:169], v[50:53]
	v_mfma_f32_16x16x32_bf16 v[38:41], v[142:145], v[174:177], v[38:41]
	v_mfma_f32_16x16x32_bf16 v[34:37], v[158:161], v[174:177], v[34:37]
	v_mfma_f32_16x16x32_bf16 v[22:25], v[142:145], v[182:185], v[22:25]
	v_mfma_f32_16x16x32_bf16 v[18:21], v[158:161], v[182:185], v[18:21]
	v_mfma_f32_16x16x32_bf16 v[6:9], v[142:145], v[190:193], v[6:9]
	v_mfma_f32_16x16x32_bf16 v[2:5], v[158:161], v[190:193], v[2:5]
	s_setprio 0
	s_barrier
	s_add_i32 s40, 0, 0x18000
	s_add_i32 s61, 0, 0x1c000
	v_add_u32_e32 v78, s40, v1
	v_add_u32_e32 v158, s61, v1
	ds_read_b128 v[66:69], v78
	ds_read_b128 v[70:73], v78 offset:1024
	ds_read_b128 v[74:77], v78 offset:2048
	ds_read_b128 v[78:81], v78 offset:3072
	ds_read_b128 v[138:141], v158
	ds_read_b128 v[142:145], v158 offset:1024
	ds_read_b128 v[154:157], v158 offset:2048
	ds_read_b128 v[158:161], v158 offset:3072
	s_mov_b32 m0, s30
	v_lshl_add_u64 v[224:225], s[48:49], 0, v[210:211]
	ds_read_b128 v[162:165], v239 offset:32768
	ds_read_b128 v[166:169], v239 offset:33792
	ds_read_b128 v[170:173], v239 offset:34816
	ds_read_b128 v[174:177], v239 offset:35840
	ds_read_b128 v[178:181], v239 offset:36864
	ds_read_b128 v[182:185], v239 offset:37888
	ds_read_b128 v[186:189], v239 offset:38912
	ds_read_b128 v[190:193], v239 offset:39936
	global_load_lds_dwordx4 v[224:225], off
	v_lshl_add_u64 v[224:225], s[48:49], 0, v[212:213]
	s_mov_b32 m0, s31
	s_nop 0
	global_load_lds_dwordx4 v[224:225], off
	s_waitcnt vmcnt(8)
	s_waitcnt lgkmcnt(0)
	s_barrier
	s_setprio 1
	s_waitcnt lgkmcnt(0)
	v_mfma_f32_16x16x32_bf16 v[150:153], v[66:69], v[162:165], v[150:153]
	v_mfma_f32_16x16x32_bf16 v[146:149], v[74:77], v[162:165], v[146:149]
	v_mfma_f32_16x16x32_bf16 v[126:129], v[66:69], v[170:173], v[126:129]
	v_mfma_f32_16x16x32_bf16 v[122:125], v[74:77], v[170:173], v[122:125]
	v_mfma_f32_16x16x32_bf16 v[110:113], v[66:69], v[178:181], v[110:113]
	v_mfma_f32_16x16x32_bf16 v[106:109], v[74:77], v[178:181], v[106:109]
	v_mfma_f32_16x16x32_bf16 v[94:97], v[66:69], v[186:189], v[94:97]
	v_mfma_f32_16x16x32_bf16 v[90:93], v[74:77], v[186:189], v[90:93]
	v_mfma_f32_16x16x32_bf16 v[150:153], v[70:73], v[166:169], v[150:153]
	v_mfma_f32_16x16x32_bf16 v[146:149], v[78:81], v[166:169], v[146:149]
	v_mfma_f32_16x16x32_bf16 v[126:129], v[70:73], v[174:177], v[126:129]
	v_mfma_f32_16x16x32_bf16 v[122:125], v[78:81], v[174:177], v[122:125]
	v_mfma_f32_16x16x32_bf16 v[110:113], v[70:73], v[182:185], v[110:113]
	v_mfma_f32_16x16x32_bf16 v[106:109], v[78:81], v[182:185], v[106:109]
	v_mfma_f32_16x16x32_bf16 v[94:97], v[70:73], v[190:193], v[94:97]
	v_mfma_f32_16x16x32_bf16 v[90:93], v[78:81], v[190:193], v[90:93]
	v_mfma_f32_16x16x32_bf16 v[134:137], v[138:141], v[162:165], v[134:137]
	v_mfma_f32_16x16x32_bf16 v[130:133], v[154:157], v[162:165], v[130:133]
	v_mfma_f32_16x16x32_bf16 v[118:121], v[138:141], v[170:173], v[118:121]
	v_mfma_f32_16x16x32_bf16 v[114:117], v[154:157], v[170:173], v[114:117]
	v_mfma_f32_16x16x32_bf16 v[102:105], v[138:141], v[178:181], v[102:105]
	v_mfma_f32_16x16x32_bf16 v[98:101], v[154:157], v[178:181], v[98:101]
	v_mfma_f32_16x16x32_bf16 v[86:89], v[138:141], v[186:189], v[86:89]
	v_mfma_f32_16x16x32_bf16 v[82:85], v[154:157], v[186:189], v[82:85]
	v_mfma_f32_16x16x32_bf16 v[134:137], v[142:145], v[166:169], v[134:137]
	v_mfma_f32_16x16x32_bf16 v[130:133], v[158:161], v[166:169], v[130:133]
	v_mfma_f32_16x16x32_bf16 v[118:121], v[142:145], v[174:177], v[118:121]
	v_mfma_f32_16x16x32_bf16 v[114:117], v[158:161], v[174:177], v[114:117]
	v_mfma_f32_16x16x32_bf16 v[102:105], v[142:145], v[182:185], v[102:105]
	v_mfma_f32_16x16x32_bf16 v[98:101], v[158:161], v[182:185], v[98:101]
	v_mfma_f32_16x16x32_bf16 v[86:89], v[142:145], v[190:193], v[86:89]
	v_mfma_f32_16x16x32_bf16 v[82:85], v[158:161], v[190:193], v[82:85]
	s_setprio 0
	s_barrier
; #define FG_STAGE(bufoff, gbase, v0, v1) do { \
;         __builtin_amdgcn_global_load_lds((const unsigned*)((const char*)(gbase) + (v0)), (LAS unsigned*)(lds + (bufoff) + ldsw), 16, 0, 0); \
;         __builtin_amdgcn_global_load_lds((const unsigned*)((const char*)(gbase) + (v1)), (LAS unsigned*)(lds + (bufoff) + ldsw + 8192), 16, 0, 0); } while (0)
; #define FG_LDA(dst, b, h) do { _Pragma("unroll") for (int m = 0; m < 4; ++m) _Pragma("unroll") for (int k = 0; k < 2; ++k) dst[m][k] = *(const LAS bf16x8*)(lds + FG_SA(b, h) + aoff + m * 2048 + k * 1024); } while (0)
; #define FG_MMA(ai, bj, At, Bt) do { __builtin_amdgcn_s_setprio(1); _Pragma("unroll") for (int m = 0; m < 4; ++m) _Pragma("unroll") for (int n = 0; n < 2; ++n) _Pragma("unroll") for (int k = 0; k < 2; ++k) \
;         acc[ai][bj][m][n] = __builtin_amdgcn_mfma_f32_16x16x32_bf16(Bt[n][k], At[m][k], acc[ai][bj][m][n], 0, 0, 0); __builtin_amdgcn_s_setprio(0); } while (0)
; #define FG_WAIT_V(n) asm volatile("s_waitcnt vmcnt(" #n ")" ::: "memory")
; #define FG_WAIT_L(n) asm volatile("s_waitcnt lgkmcnt(" #n ")" ::: "memory")
; #define FG_BAR __builtin_amdgcn_s_barrier()
; #define FG_SCHED __builtin_amdgcn_sched_barrier(0)
; template <bool GATHER, class Unit, class Epi, class Sched>
; __device__ __forceinline__ void gemm_phase(LAS unsigned char* lds, const int K, const Sched& S, const Epi& E) {
;     ...
;             FG_LDA(At, 1, 1); FG_STAGE(FG_SB(1, 0), b3, voffB0, voffB1); FG_STAGE(FG_SB(1, 1), b3 + hstepB, voffB0, voffB1); FG_STAGE(FG_SA(1, 0), a3, x00, x01);
;             FG_WAIT_V(8); FG_WAIT_L(0); FG_BAR; if (hi_on) { FG_MMA(1, 0, At, B0); FG_MMA(1, 1, At, B1); } FG_BAR; FG_SCHED;
;         }
;         if (wr == 0) FG_BAR;
	s_add_i32 s40, s40, s27
	v_lshl_add_u64 v[194:195], v[194:195], 0, s[18:19]
	s_mov_b32 m0, s40
	ds_read_b128 v[162:165], v239 offset:49152
	ds_read_b128 v[166:169], v239 offset:50176
	ds_read_b128 v[170:173], v239 offset:51200
	ds_read_b128 v[174:177], v239 offset:52224
	ds_read_b128 v[178:181], v239 offset:53248
	ds_read_b128 v[182:185], v239 offset:54272
	ds_read_b128 v[186:189], v239 offset:55296
	ds_read_b128 v[190:193], v239 offset:56320
	global_load_lds_dwordx4 v[194:195], off
	s_add_i32 m0, s40, 0x2000
	s_add_u32 s40, s46, 0x80080
	v_lshl_add_u64 v[194:195], v[196:197], 0, s[18:19]
	s_addc_u32 s41, s47, 0
	s_add_i32 s46, s61, s27
	global_load_lds_dwordx4 v[194:195], off
	v_lshl_add_u64 v[194:195], s[40:41], 0, v[202:203]
	s_mov_b32 m0, s46
	s_nop 0
	global_load_lds_dwordx4 v[194:195], off
	v_lshl_add_u64 v[194:195], s[40:41], 0, v[204:205]
	s_add_i32 m0, s46, 0x2000
	s_nop 0
	global_load_lds_dwordx4 v[194:195], off
	v_lshl_add_u64 v[194:195], v[198:199], 0, s[18:19]
	s_mov_b32 m0, s52
	s_nop 0
	global_load_lds_dwordx4 v[194:195], off
	v_lshl_add_u64 v[194:195], v[200:201], 0, s[18:19]
	s_mov_b32 m0, s53
	s_nop 0
	global_load_lds_dwordx4 v[194:195], off
	s_waitcnt vmcnt(8)
	s_waitcnt lgkmcnt(0)
	s_barrier
	s_setprio 1
	s_waitcnt lgkmcnt(0)
	v_mfma_f32_16x16x32_bf16 v[62:65], v[66:69], v[162:165], v[62:65]
	v_mfma_f32_16x16x32_bf16 v[58:61], v[74:77], v[162:165], v[58:61]
	v_mfma_f32_16x16x32_bf16 v[46:49], v[66:69], v[170:173], v[46:49]
	v_mfma_f32_16x16x32_bf16 v[42:45], v[74:77], v[170:173], v[42:45]
	v_mfma_f32_16x16x32_bf16 v[30:33], v[66:69], v[178:181], v[30:33]
	v_mfma_f32_16x16x32_bf16 v[26:29], v[74:77], v[178:181], v[26:29]
	v_mfma_f32_16x16x32_bf16 v[14:17], v[66:69], v[186:189], v[14:17]
	v_mfma_f32_16x16x32_bf16 v[10:13], v[74:77], v[186:189], v[10:13]
	v_mfma_f32_16x16x32_bf16 v[62:65], v[70:73], v[166:169], v[62:65]
	v_mfma_f32_16x16x32_bf16 v[58:61], v[78:81], v[166:169], v[58:61]
	v_mfma_f32_16x16x32_bf16 v[46:49], v[70:73], v[174:177], v[46:49]
	v_mfma_f32_16x16x32_bf16 v[42:45], v[78:81], v[174:177], v[42:45]
	v_mfma_f32_16x16x32_bf16 v[30:33], v[70:73], v[182:185], v[30:33]
	v_mfma_f32_16x16x32_bf16 v[26:29], v[78:81], v[182:185], v[26:29]
	v_mfma_f32_16x16x32_bf16 v[14:17], v[70:73], v[190:193], v[14:17]
	v_mfma_f32_16x16x32_bf16 v[10:13], v[78:81], v[190:193], v[10:13]
	v_mfma_f32_16x16x32_bf16 v[54:57], v[138:141], v[162:165], v[54:57]
	v_mfma_f32_16x16x32_bf16 v[50:53], v[154:157], v[162:165], v[50:53]
	v_mfma_f32_16x16x32_bf16 v[38:41], v[138:141], v[170:173], v[38:41]
	v_mfma_f32_16x16x32_bf16 v[34:37], v[154:157], v[170:173], v[34:37]
	v_mfma_f32_16x16x32_bf16 v[22:25], v[138:141], v[178:181], v[22:25]
	v_mfma_f32_16x16x32_bf16 v[18:21], v[154:157], v[178:181], v[18:21]
	v_mfma_f32_16x16x32_bf16 v[6:9], v[138:141], v[186:189], v[6:9]
	v_mfma_f32_16x16x32_bf16 v[2:5], v[154:157], v[186:189], v[2:5]
	v_mfma_f32_16x16x32_bf16 v[54:57], v[142:145], v[166:169], v[54:57]
	v_mfma_f32_16x16x32_bf16 v[50:53], v[158:161], v[166:169], v[50:53]
	v_mfma_f32_16x16x32_bf16 v[38:41], v[142:145], v[174:177], v[38:41]
	v_mfma_f32_16x16x32_bf16 v[34:37], v[158:161], v[174:177], v[34:37]
	v_mfma_f32_16x16x32_bf16 v[22:25], v[142:145], v[182:185], v[22:25]
	v_mfma_f32_16x16x32_bf16 v[18:21], v[158:161], v[182:185], v[18:21]
	v_mfma_f32_16x16x32_bf16 v[6:9], v[142:145], v[190:193], v[6:9]
	v_mfma_f32_16x16x32_bf16 v[2:5], v[158:161], v[190:193], v[2:5]
	s_setprio 0
	s_barrier
	s_add_i32 s60, s60, 2
	s_add_u32 s58, s58, 0x100
	s_addc_u32 s59, s59, 0
	s_cmp_gt_u32 s60, 29
	s_mov_b64 s[40:41], s[44:45]
	s_cbranch_scc0 .LBB0_652
	s_and_b64 vcc, exec, s[20:21]
	s_cbranch_vccz .LBB0_655
	s_barrier

; #define FG_STAGE(bufoff, gbase, v0, v1) do { \
;         __builtin_amdgcn_global_load_lds((const unsigned*)((const char*)(gbase) + (v0)), (LAS unsigned*)(lds + (bufoff) + ldsw), 16, 0, 0); \
;         __builtin_amdgcn_global_load_lds((const unsigned*)((const char*)(gbase) + (v1)), (LAS unsigned*)(lds + (bufoff) + ldsw + 8192), 16, 0, 0); } while (0)
; #define FG_LDA(dst, b, h) do { _Pragma("unroll") for (int m = 0; m < 4; ++m) _Pragma("unroll") for (int k = 0; k < 2; ++k) dst[m][k] = *(const LAS bf16x8*)(lds + FG_SA(b, h) + aoff + m * 2048 + k * 1024); } while (0)
; #define FG_LDB(dst, b, h) do { _Pragma("unroll") for (int n = 0; n < 2; ++n) _Pragma("unroll") for (int k = 0; k < 2; ++k) dst[n][k] = *(const LAS bf16x8*)(lds + FG_SB(b, h) + boff + n * 2048 + k * 1024); } while (0)
; #define FG_WAIT_V(n) asm volatile("s_waitcnt vmcnt(" #n ")" ::: "memory")
; #define FG_WAIT_L(n) asm volatile("s_waitcnt lgkmcnt(" #n ")" ::: "memory")
; #define FG_BAR __builtin_amdgcn_s_barrier()
; #define FG_SCHED __builtin_amdgcn_sched_barrier(0)
; template <bool GATHER, class Unit, class Epi, class Sched>
; __device__ __forceinline__ void gemm_phase(LAS unsigned char* lds, const int K, const Sched& S, const Epi& E) {
;     ...
;         for (int t = 0; t < nt; t += 2) {
;             const bool last = (t == nt - 2);
;             const char* a1 = cA + (size_t)(t + 1) * kstep;
;             const char* a2 = last ? nA : cA + (size_t)(t + 2) * kstep; const char* b2 = last ? nB : cB + (size_t)(t + 2) * kstep;
;             const char* a3 = a2 + kstep; const char* b3 = b2 + kstep;
;             const unsigned x00 = (GATHER && last) ? vN00 : vA00, x01 = (GATHER && last) ? vN01 : vA01, x10 = (GATHER && last) ? vN10 : vA10, x11 = (GATHER && last) ? vN11 : vA11;
;             FG_LDB(B0, 0, 0); FG_LDB(B1, 0, 1); FG_SCHED; FG_LDA(At, 0, 0); FG_STAGE(FG_SA(1, 1), a1, vA10, vA11);
;             FG_WAIT_V(8); FG_WAIT_L(0); FG_BAR; FG_MMA(0, 0, At, B0); FG_MMA(0, 1, At, B1); FG_BAR; FG_SCHED;
;             FG_LDA(At, 0, 1); FG_STAGE(FG_SB(0, 0), b2, voffB0, voffB1); FG_STAGE(FG_SB(0, 1), b2 + hstepB, voffB0, voffB1); FG_STAGE(FG_SA(0, 0), a2, x00, x01);
;             FG_WAIT_V(8); FG_WAIT_L(0); FG_BAR; if (hi_on) { FG_MMA(1, 0, At, B0); FG_MMA(1, 1, At, B1); } FG_BAR; FG_SCHED;
;             FG_LDB(B0, 1, 0); FG_LDB(B1, 1, 1); FG_SCHED; FG_LDA(At, 1, 0); FG_STAGE(FG_SA(0, 1), a2, x10, x11);
.LBB0_734:
	ds_read_b128 v[86:89], v84
	ds_read_b128 v[90:93], v84 offset:1024
	ds_read_b128 v[94:97], v84 offset:2048
	ds_read_b128 v[98:101], v84 offset:3072
	s_add_u32 s20, s18, 0x80
	s_addc_u32 s21, s19, 0
	s_cmp_eq_u32 s53, 4
	s_cselect_b32 s25, s47, s21
	s_cselect_b32 s24, s48, s20
	s_cselect_b32 s21, s49, s52
	s_cselect_b32 s20, s50, s51
	v_lshl_add_u64 v[134:135], s[18:19], 0, v[82:83]
	s_add_i32 m0, s5, 0xc000
	ds_read_b128 v[102:105], v85
	ds_read_b128 v[106:109], v85 offset:1024
	ds_read_b128 v[110:113], v85 offset:2048
	ds_read_b128 v[114:117], v85 offset:3072
	ds_read_b128 v[118:121], v85 offset:4096
	ds_read_b128 v[122:125], v85 offset:5120
	ds_read_b128 v[126:129], v85 offset:6144
	ds_read_b128 v[130:133], v85 offset:7168
	global_load_lds_dwordx4 v[134:135], off
	v_lshl_add_u64 v[134:135], s[18:19], 0, v[80:81]
	s_add_i32 m0, s5, 0xe000
	s_nop 0
	global_load_lds_dwordx4 v[134:135], off
	s_waitcnt vmcnt(8)
	s_waitcnt lgkmcnt(0)
	s_barrier
	s_setprio 1
	s_waitcnt lgkmcnt(0)
	v_mfma_f32_16x16x32_bf16 v[62:65], v[86:89], v[102:105], v[62:65]
	v_mfma_f32_16x16x32_bf16 v[58:61], v[94:97], v[102:105], v[58:61]
	v_mfma_f32_16x16x32_bf16 v[54:57], v[86:89], v[110:113], v[54:57]
	v_mfma_f32_16x16x32_bf16 v[50:53], v[94:97], v[110:113], v[50:53]
	v_mfma_f32_16x16x32_bf16 v[46:49], v[86:89], v[118:121], v[46:49]
	v_mfma_f32_16x16x32_bf16 v[42:45], v[94:97], v[118:121], v[42:45]
	v_mfma_f32_16x16x32_bf16 v[38:41], v[86:89], v[126:129], v[38:41]
	v_mfma_f32_16x16x32_bf16 v[34:37], v[94:97], v[126:129], v[34:37]
	v_mfma_f32_16x16x32_bf16 v[62:65], v[90:93], v[106:109], v[62:65]
	v_mfma_f32_16x16x32_bf16 v[58:61], v[98:101], v[106:109], v[58:61]
	v_mfma_f32_16x16x32_bf16 v[54:57], v[90:93], v[114:117], v[54:57]
	v_mfma_f32_16x16x32_bf16 v[50:53], v[98:101], v[114:117], v[50:53]
	v_mfma_f32_16x16x32_bf16 v[46:49], v[90:93], v[122:125], v[46:49]
	v_mfma_f32_16x16x32_bf16 v[42:45], v[98:101], v[122:125], v[42:45]
	v_mfma_f32_16x16x32_bf16 v[38:41], v[90:93], v[130:133], v[38:41]
	v_mfma_f32_16x16x32_bf16 v[34:37], v[98:101], v[130:133], v[34:37]
	s_setprio 0
	s_barrier
	s_add_i32 s54, s41, s26
	v_lshl_add_u64 v[134:135], s[20:21], 0, v[68:69]
	s_mov_b32 m0, s54
	ds_read_b128 v[102:105], v85 offset:16384
	ds_read_b128 v[106:109], v85 offset:17408
	ds_read_b128 v[110:113], v85 offset:18432
	ds_read_b128 v[114:117], v85 offset:19456
	ds_read_b128 v[118:121], v85 offset:20480
	ds_read_b128 v[122:125], v85 offset:21504
	ds_read_b128 v[126:129], v85 offset:22528
	ds_read_b128 v[130:133], v85 offset:23552
	global_load_lds_dwordx4 v[134:135], off
	s_add_i32 m0, s54, 0x2000
	s_add_u32 s54, s20, 0x20000
	v_lshl_add_u64 v[136:137], s[20:21], 0, v[66:67]
	s_addc_u32 s55, s21, 0
	global_load_lds_dwordx4 v[136:137], off
	v_lshl_add_u64 v[138:139], s[54:55], 0, v[68:69]
	s_mov_b32 m0, s28
	v_lshl_add_u64 v[140:141], s[24:25], 0, v[72:73]
	global_load_lds_dwordx4 v[138:139], off
	v_lshl_add_u64 v[138:139], s[54:55], 0, v[66:67]
	s_mov_b32 m0, s29
	s_nop 0
	global_load_lds_dwordx4 v[138:139], off
	v_lshl_add_u64 v[138:139], s[24:25], 0, v[70:71]
	s_mov_b32 m0, s5
	s_nop 0
	global_load_lds_dwordx4 v[138:139], off
	s_mov_b32 m0, s30
	s_nop 0
	global_load_lds_dwordx4 v[140:141], off
	s_waitcnt vmcnt(8)
	s_waitcnt lgkmcnt(0)
	s_barrier
	s_setprio 1
	s_waitcnt lgkmcnt(0)
	v_mfma_f32_16x16x32_bf16 v[30:33], v[86:89], v[102:105], v[30:33]
	v_mfma_f32_16x16x32_bf16 v[26:29], v[94:97], v[102:105], v[26:29]
	v_mfma_f32_16x16x32_bf16 v[22:25], v[86:89], v[110:113], v[22:25]
	v_mfma_f32_16x16x32_bf16 v[18:21], v[94:97], v[110:113], v[18:21]
	v_mfma_f32_16x16x32_bf16 v[14:17], v[86:89], v[118:121], v[14:17]
	v_mfma_f32_16x16x32_bf16 v[10:13], v[94:97], v[118:121], v[10:13]
	v_mfma_f32_16x16x32_bf16 v[6:9], v[86:89], v[126:129], v[6:9]
	v_mfma_f32_16x16x32_bf16 v[2:5], v[94:97], v[126:129], v[2:5]
	v_mfma_f32_16x16x32_bf16 v[30:33], v[90:93], v[106:109], v[30:33]
	v_mfma_f32_16x16x32_bf16 v[26:29], v[98:101], v[106:109], v[26:29]
	v_mfma_f32_16x16x32_bf16 v[22:25], v[90:93], v[114:117], v[22:25]
	v_mfma_f32_16x16x32_bf16 v[18:21], v[98:101], v[114:117], v[18:21]
	v_mfma_f32_16x16x32_bf16 v[14:17], v[90:93], v[122:125], v[14:17]
	v_mfma_f32_16x16x32_bf16 v[10:13], v[98:101], v[122:125], v[10:13]
	v_mfma_f32_16x16x32_bf16 v[6:9], v[90:93], v[130:133], v[6:9]
	v_mfma_f32_16x16x32_bf16 v[2:5], v[98:101], v[130:133], v[2:5]
	s_setprio 0
	s_barrier
; #define FG_STAGE(bufoff, gbase, v0, v1) do { \
;         __builtin_amdgcn_global_load_lds((const unsigned*)((const char*)(gbase) + (v0)), (LAS unsigned*)(lds + (bufoff) + ldsw), 16, 0, 0); \
;         __builtin_amdgcn_global_load_lds((const unsigned*)((const char*)(gbase) + (v1)), (LAS unsigned*)(lds + (bufoff) + ldsw + 8192), 16, 0, 0); } while (0)
; #define FG_LDA(dst, b, h) do { _Pragma("unroll") for (int m = 0; m < 4; ++m) _Pragma("unroll") for (int k = 0; k < 2; ++k) dst[m][k] = *(const LAS bf16x8*)(lds + FG_SA(b, h) + aoff + m * 2048 + k * 1024); } while (0)
; #define FG_LDB(dst, b, h) do { _Pragma("unroll") for (int n = 0; n < 2; ++n) _Pragma("unroll") for (int k = 0; k < 2; ++k) dst[n][k] = *(const LAS bf16x8*)(lds + FG_SB(b, h) + boff + n * 2048 + k * 1024); } while (0)
; #define FG_MMA(ai, bj, At, Bt) do { __builtin_amdgcn_s_setprio(1); _Pragma("unroll") for (int m = 0; m < 4; ++m) _Pragma("unroll") for (int n = 0; n < 2; ++n) _Pragma("unroll") for (int k = 0; k < 2; ++k) \
;         acc[ai][bj][m][n] = __builtin_amdgcn_mfma_f32_16x16x32_bf16(Bt[n][k], At[m][k], acc[ai][bj][m][n], 0, 0, 0); __builtin_amdgcn_s_setprio(0); } while (0)
; #define FG_WAIT_V(n) asm volatile("s_waitcnt vmcnt(" #n ")" ::: "memory")
; #define FG_WAIT_L(n) asm volatile("s_waitcnt lgkmcnt(" #n ")" ::: "memory")
; #define FG_BAR __builtin_amdgcn_s_barrier()
; #define FG_SCHED __builtin_amdgcn_sched_barrier(0)
; template <bool GATHER, class Unit, class Epi, class Sched>
; __device__ __forceinline__ void gemm_phase(LAS unsigned char* lds, const int K, const Sched& S, const Epi& E) {
;     ...
;             FG_LDB(B0, 1, 0); FG_LDB(B1, 1, 1); FG_SCHED; FG_LDA(At, 1, 0); FG_STAGE(FG_SA(0, 1), a2, x10, x11);
;             FG_WAIT_V(8); FG_WAIT_L(0); FG_BAR; FG_MMA(0, 0, At, B0); FG_MMA(0, 1, At, B1); FG_BAR; FG_SCHED;
;             FG_LDA(At, 1, 1); FG_STAGE(FG_SB(1, 0), b3, voffB0, voffB1); FG_STAGE(FG_SB(1, 1), b3 + hstepB, voffB0, voffB1); FG_STAGE(FG_SA(1, 0), a3, x00, x01);
;             FG_WAIT_V(8); FG_WAIT_L(0); FG_BAR; if (hi_on) { FG_MMA(1, 0, At, B0); FG_MMA(1, 1, At, B1); } FG_BAR; FG_SCHED;
;         }
;         if (wr == 0) FG_BAR;
	s_add_i32 s54, 0, 0x18000
	v_add_u32_e32 v78, s54, v1
	ds_read_b128 v[86:89], v78
	ds_read_b128 v[90:93], v78 offset:1024
	ds_read_b128 v[94:97], v78 offset:2048
	ds_read_b128 v[98:101], v78 offset:3072
	s_mov_b32 m0, s31
	v_lshl_add_u64 v[142:143], s[24:25], 0, v[74:75]
	ds_read_b128 v[102:105], v85 offset:32768
	ds_read_b128 v[106:109], v85 offset:33792
	ds_read_b128 v[110:113], v85 offset:34816
	ds_read_b128 v[114:117], v85 offset:35840
	ds_read_b128 v[118:121], v85 offset:36864
	ds_read_b128 v[122:125], v85 offset:37888
	ds_read_b128 v[126:129], v85 offset:38912
	ds_read_b128 v[130:133], v85 offset:39936
	global_load_lds_dwordx4 v[142:143], off
	v_lshl_add_u64 v[142:143], s[24:25], 0, v[76:77]
	s_mov_b32 m0, s33
	s_nop 0
	global_load_lds_dwordx4 v[142:143], off
	s_waitcnt vmcnt(8)
	s_waitcnt lgkmcnt(0)
	s_barrier
	s_setprio 1
	s_waitcnt lgkmcnt(0)
	v_mfma_f32_16x16x32_bf16 v[62:65], v[86:89], v[102:105], v[62:65]
	v_mfma_f32_16x16x32_bf16 v[58:61], v[94:97], v[102:105], v[58:61]
	v_mfma_f32_16x16x32_bf16 v[54:57], v[86:89], v[110:113], v[54:57]
	v_mfma_f32_16x16x32_bf16 v[50:53], v[94:97], v[110:113], v[50:53]
	v_mfma_f32_16x16x32_bf16 v[46:49], v[86:89], v[118:121], v[46:49]
	v_mfma_f32_16x16x32_bf16 v[42:45], v[94:97], v[118:121], v[42:45]
	v_mfma_f32_16x16x32_bf16 v[38:41], v[86:89], v[126:129], v[38:41]
	v_mfma_f32_16x16x32_bf16 v[34:37], v[94:97], v[126:129], v[34:37]
	v_mfma_f32_16x16x32_bf16 v[62:65], v[90:93], v[106:109], v[62:65]
	v_mfma_f32_16x16x32_bf16 v[58:61], v[98:101], v[106:109], v[58:61]
	v_mfma_f32_16x16x32_bf16 v[54:57], v[90:93], v[114:117], v[54:57]
	v_mfma_f32_16x16x32_bf16 v[50:53], v[98:101], v[114:117], v[50:53]
	v_mfma_f32_16x16x32_bf16 v[46:49], v[90:93], v[122:125], v[46:49]
	v_mfma_f32_16x16x32_bf16 v[42:45], v[98:101], v[122:125], v[42:45]
	v_mfma_f32_16x16x32_bf16 v[38:41], v[90:93], v[130:133], v[38:41]
	v_mfma_f32_16x16x32_bf16 v[34:37], v[98:101], v[130:133], v[34:37]
	s_setprio 0
	s_barrier
	s_add_i32 s24, s54, s26
	v_lshl_add_u64 v[134:135], v[134:135], 0, s[12:13]
	s_mov_b32 m0, s24
	ds_read_b128 v[102:105], v85 offset:49152
	ds_read_b128 v[106:109], v85 offset:50176
	ds_read_b128 v[110:113], v85 offset:51200
	ds_read_b128 v[114:117], v85 offset:52224
	ds_read_b128 v[118:121], v85 offset:53248
	ds_read_b128 v[122:125], v85 offset:54272
	ds_read_b128 v[126:129], v85 offset:55296
	ds_read_b128 v[130:133], v85 offset:56320
	global_load_lds_dwordx4 v[134:135], off
	s_add_i32 m0, s24, 0x2000
	s_add_u32 s20, s20, 0x20080
	v_lshl_add_u64 v[134:135], v[136:137], 0, s[12:13]
	s_addc_u32 s21, s21, 0
	global_load_lds_dwordx4 v[134:135], off
	v_lshl_add_u64 v[134:135], s[20:21], 0, v[68:69]
	s_mov_b32 m0, s39
	s_nop 0
	global_load_lds_dwordx4 v[134:135], off
	v_lshl_add_u64 v[134:135], s[20:21], 0, v[66:67]
	s_mov_b32 m0, s40
	s_nop 0
	global_load_lds_dwordx4 v[134:135], off
	v_lshl_add_u64 v[134:135], v[138:139], 0, s[12:13]
	s_mov_b32 m0, s37
	s_nop 0
	global_load_lds_dwordx4 v[134:135], off
	v_lshl_add_u64 v[134:135], v[140:141], 0, s[12:13]
	s_mov_b32 m0, s38
	s_nop 0
	global_load_lds_dwordx4 v[134:135], off
	s_waitcnt vmcnt(8)
	s_waitcnt lgkmcnt(0)
	s_barrier
	s_setprio 1
	s_waitcnt lgkmcnt(0)
	v_mfma_f32_16x16x32_bf16 v[30:33], v[86:89], v[102:105], v[30:33]
	v_mfma_f32_16x16x32_bf16 v[26:29], v[94:97], v[102:105], v[26:29]
	v_mfma_f32_16x16x32_bf16 v[22:25], v[86:89], v[110:113], v[22:25]
	v_mfma_f32_16x16x32_bf16 v[18:21], v[94:97], v[110:113], v[18:21]
	v_mfma_f32_16x16x32_bf16 v[14:17], v[86:89], v[118:121], v[14:17]
	v_mfma_f32_16x16x32_bf16 v[10:13], v[94:97], v[118:121], v[10:13]
	v_mfma_f32_16x16x32_bf16 v[6:9], v[86:89], v[126:129], v[6:9]
	v_mfma_f32_16x16x32_bf16 v[2:5], v[94:97], v[126:129], v[2:5]
	v_mfma_f32_16x16x32_bf16 v[30:33], v[90:93], v[106:109], v[30:33]
	v_mfma_f32_16x16x32_bf16 v[26:29], v[98:101], v[106:109], v[26:29]
	v_mfma_f32_16x16x32_bf16 v[22:25], v[90:93], v[114:117], v[22:25]
	v_mfma_f32_16x16x32_bf16 v[18:21], v[98:101], v[114:117], v[18:21]
	v_mfma_f32_16x16x32_bf16 v[14:17], v[90:93], v[122:125], v[14:17]
	v_mfma_f32_16x16x32_bf16 v[10:13], v[98:101], v[122:125], v[10:13]
	v_mfma_f32_16x16x32_bf16 v[6:9], v[90:93], v[130:133], v[6:9]
	v_mfma_f32_16x16x32_bf16 v[2:5], v[98:101], v[130:133], v[2:5]
	s_setprio 0
	s_barrier
	s_add_i32 s53, s53, 2
	s_add_u32 s51, s51, 0x100
	s_addc_u32 s52, s52, 0
	s_add_u32 s18, s18, 0x100
	s_addc_u32 s19, s19, 0
	s_cmp_gt_u32 s53, 5
	s_cbranch_scc0 .LBB0_734
	s_and_b64 vcc, exec, s[14:15]
	s_cbranch_vccz .LBB0_737
	s_barrier

; #define FG_STAGE(bufoff, gbase, v0, v1) do { \
;         __builtin_amdgcn_global_load_lds((const unsigned*)((const char*)(gbase) + (v0)), (LAS unsigned*)(lds + (bufoff) + ldsw), 16, 0, 0); \
;         __builtin_amdgcn_global_load_lds((const unsigned*)((const char*)(gbase) + (v1)), (LAS unsigned*)(lds + (bufoff) + ldsw + 8192), 16, 0, 0); } while (0)
; #define FG_LDA(dst, b, h) do { _Pragma("unroll") for (int m = 0; m < 4; ++m) _Pragma("unroll") for (int k = 0; k < 2; ++k) dst[m][k] = *(const LAS bf16x8*)(lds + FG_SA(b, h) + aoff + m * 2048 + k * 1024); } while (0)
; #define FG_WAIT_V(n) asm volatile("s_waitcnt vmcnt(" #n ")" ::: "memory")
; template <bool GATHER, class Unit, class Epi, class Sched>
; __device__ __forceinline__ void gemm_phase(LAS unsigned char* lds, const int K, const Sched& S, const Epi& E) {
;     ...
;         if (GATHER) { if (has_next) { vN00 = S.a_voff(nxt, R0, C0); vN01 = S.a_voff(nxt, R1, C1); vN10 = S.a_voff(nxt, HALF + R0, C0); vN11 = S.a_voff(nxt, HALF + R1, C1); }
;                       else { vN00 = vA00; vN01 = vA01; vN10 = vA10; vN11 = vA11; } }
;         for (int t = 0; t < nt; t += 2) {
;             const bool last = (t == nt - 2);
;             const char* a1 = cA + (size_t)(t + 1) * kstep;
;             const char* a2 = last ? nA : cA + (size_t)(t + 2) * kstep; const char* b2 = last ? nB : cB + (size_t)(t + 2) * kstep;
;             const char* a3 = a2 + kstep; const char* b3 = b2 + kstep;
;             const unsigned x00 = (GATHER && last) ? vN00 : vA00, x01 = (GATHER && last) ? vN01 : vA01, x10 = (GATHER && last) ? vN10 : vA10, x11 = (GATHER && last) ? vN11 : vA11;
;             FG_LDB(B0, 0, 0); FG_LDB(B1, 0, 1); FG_SCHED; FG_LDA(At, 0, 0); FG_STAGE(FG_SA(1, 1), a1, vA10, vA11);
;             FG_WAIT_V(8); FG_WAIT_L(0); FG_BAR; FG_MMA(0, 0, At, B0); FG_MMA(0, 1, At, B1); FG_BAR; FG_SCHED;
;             FG_LDA(At, 0, 1); FG_STAGE(FG_SB(0, 0), b2, voffB0, voffB1); FG_STAGE(FG_SB(0, 1), b2 + hstepB, voffB0, voffB1); FG_STAGE(FG_SA(0, 0), a2, x00, x01);
;             FG_WAIT_V(8); FG_WAIT_L(0); FG_BAR; if (hi_on) { FG_MMA(1, 0, At, B0); FG_MMA(1, 1, At, B1); } FG_BAR; FG_SCHED;
;             FG_LDB(B0, 1, 0); FG_LDB(B1, 1, 1); FG_SCHED; FG_LDA(At, 1, 0); FG_STAGE(FG_SA(0, 1), a2, x10, x11);
;             FG_WAIT_V(8); FG_WAIT_L(0); FG_BAR; FG_MMA(0, 0, At, B0); FG_MMA(0, 1, At, B1); FG_BAR; FG_SCHED;
.LBB0_916:
	v_add_u32_e32 v5, s57, v209
	ds_read_b128 v[150:153], v5
	ds_read_b128 v[154:157], v5 offset:1024
	ds_read_b128 v[158:161], v5 offset:2048
	ds_read_b128 v[162:165], v5 offset:3072
	v_add_u32_e32 v5, s58, v209
	ds_read_b128 v[134:137], v5
	ds_read_b128 v[138:141], v5 offset:1024
	ds_read_b128 v[142:145], v5 offset:2048
	ds_read_b128 v[146:149], v5 offset:3072
	s_add_u32 s48, s12, s44
	s_addc_u32 s49, s13, s45
	s_add_u32 s48, s48, 0x1be00100
	s_addc_u32 s49, s49, 0
	s_and_b64 s[10:11], exec, s[10:11]
	s_cselect_b32 s49, s15, s49
	s_cselect_b32 s48, s14, s48
	v_lshl_add_u64 v[214:215], v[212:213], 0, s[44:45]
	s_add_i32 m0, s27, 0xc000
	ds_read_b128 v[166:169], v223
	ds_read_b128 v[170:173], v223 offset:1024
	ds_read_b128 v[174:177], v223 offset:2048
	ds_read_b128 v[178:181], v223 offset:3072
	ds_read_b128 v[182:185], v223 offset:4096
	ds_read_b128 v[186:189], v223 offset:5120
	ds_read_b128 v[190:193], v223 offset:6144
	ds_read_b128 v[194:197], v223 offset:7168
	global_load_lds_dwordx4 v[214:215], off
	v_lshl_add_u64 v[214:215], v[210:211], 0, s[44:45]
	s_add_i32 m0, s27, 0xe000
	s_nop 0
	global_load_lds_dwordx4 v[214:215], off
	s_waitcnt vmcnt(8)
	s_waitcnt lgkmcnt(0)
	s_barrier
	s_setprio 1
	s_waitcnt lgkmcnt(0)
	v_mfma_f32_16x16x32_bf16 v[130:133], v[150:153], v[166:169], v[130:133]
	v_mfma_f32_16x16x32_bf16 v[126:129], v[158:161], v[166:169], v[126:129]
	v_mfma_f32_16x16x32_bf16 v[114:117], v[150:153], v[174:177], v[114:117]
	v_mfma_f32_16x16x32_bf16 v[110:113], v[158:161], v[174:177], v[110:113]
	v_mfma_f32_16x16x32_bf16 v[98:101], v[150:153], v[182:185], v[98:101]
	v_mfma_f32_16x16x32_bf16 v[94:97], v[158:161], v[182:185], v[94:97]
	v_mfma_f32_16x16x32_bf16 v[82:85], v[150:153], v[190:193], v[82:85]
	v_mfma_f32_16x16x32_bf16 v[78:81], v[158:161], v[190:193], v[78:81]
	v_mfma_f32_16x16x32_bf16 v[130:133], v[154:157], v[170:173], v[130:133]
	v_mfma_f32_16x16x32_bf16 v[126:129], v[162:165], v[170:173], v[126:129]
	v_mfma_f32_16x16x32_bf16 v[114:117], v[154:157], v[178:181], v[114:117]
	v_mfma_f32_16x16x32_bf16 v[110:113], v[162:165], v[178:181], v[110:113]
	v_mfma_f32_16x16x32_bf16 v[98:101], v[154:157], v[186:189], v[98:101]
	v_mfma_f32_16x16x32_bf16 v[94:97], v[162:165], v[186:189], v[94:97]
	v_mfma_f32_16x16x32_bf16 v[82:85], v[154:157], v[194:197], v[82:85]
	v_mfma_f32_16x16x32_bf16 v[78:81], v[162:165], v[194:197], v[78:81]
	v_mfma_f32_16x16x32_bf16 v[122:125], v[134:137], v[166:169], v[122:125]
	v_mfma_f32_16x16x32_bf16 v[118:121], v[142:145], v[166:169], v[118:121]
	v_mfma_f32_16x16x32_bf16 v[106:109], v[134:137], v[174:177], v[106:109]
	v_mfma_f32_16x16x32_bf16 v[102:105], v[142:145], v[174:177], v[102:105]
	v_mfma_f32_16x16x32_bf16 v[90:93], v[134:137], v[182:185], v[90:93]
	v_mfma_f32_16x16x32_bf16 v[86:89], v[142:145], v[182:185], v[86:89]
	v_mfma_f32_16x16x32_bf16 v[74:77], v[134:137], v[190:193], v[74:77]
	v_mfma_f32_16x16x32_bf16 v[70:73], v[142:145], v[190:193], v[70:73]
	v_mfma_f32_16x16x32_bf16 v[122:125], v[138:141], v[170:173], v[122:125]
	v_mfma_f32_16x16x32_bf16 v[118:121], v[146:149], v[170:173], v[118:121]
	v_mfma_f32_16x16x32_bf16 v[106:109], v[138:141], v[178:181], v[106:109]
	v_mfma_f32_16x16x32_bf16 v[102:105], v[146:149], v[178:181], v[102:105]
	v_mfma_f32_16x16x32_bf16 v[90:93], v[138:141], v[186:189], v[90:93]
	v_mfma_f32_16x16x32_bf16 v[86:89], v[146:149], v[186:189], v[86:89]
	v_mfma_f32_16x16x32_bf16 v[74:77], v[138:141], v[194:197], v[74:77]
	v_mfma_f32_16x16x32_bf16 v[70:73], v[146:149], v[194:197], v[70:73]
	s_setprio 0
	s_barrier
	s_add_i32 s10, s57, s26
	v_lshl_add_u64 v[214:215], s[46:47], 0, v[198:199]
	s_mov_b32 m0, s10
	ds_read_b128 v[190:193], v223 offset:16384
	ds_read_b128 v[194:197], v223 offset:17408
	ds_read_b128 v[182:185], v223 offset:18432
	ds_read_b128 v[186:189], v223 offset:19456
	ds_read_b128 v[174:177], v223 offset:20480
	ds_read_b128 v[178:181], v223 offset:21504
	ds_read_b128 v[166:169], v223 offset:22528
	ds_read_b128 v[170:173], v223 offset:23552
	global_load_lds_dwordx4 v[214:215], off
	s_add_i32 m0, s10, 0x2000
	s_add_u32 s10, s46, 0x80000
	v_lshl_add_u64 v[216:217], s[46:47], 0, v[200:201]
	s_addc_u32 s11, s47, 0
	s_add_i32 s66, s58, s26
	global_load_lds_dwordx4 v[216:217], off
	v_lshl_add_u64 v[232:233], s[10:11], 0, v[198:199]
	s_mov_b32 m0, s66
	v_cndmask_b32_e64 v5, 0, 1, s[8:9]
	global_load_lds_dwordx4 v[232:233], off
	v_lshl_add_u64 v[232:233], s[10:11], 0, v[200:201]
	s_add_i32 m0, s66, 0x2000
	v_cmp_ne_u32_e64 s[10:11], 1, v5
	global_load_lds_dwordx4 v[232:233], off
	s_mov_b32 m0, s27
	s_andn2_b64 vcc, exec, s[8:9]
	global_load_lds_dwordx4 v2, s[48:49]
	s_mov_b32 m0, s28
	s_nop 0
	global_load_lds_dwordx4 v4, s[48:49]
	s_waitcnt vmcnt(8)
	s_waitcnt lgkmcnt(0)
	s_barrier
	s_cbranch_vccnz .LBB0_918
	s_setprio 1
	s_waitcnt lgkmcnt(0)
	v_mfma_f32_16x16x32_bf16 v[62:65], v[150:153], v[190:193], v[62:65]
	v_mfma_f32_16x16x32_bf16 v[66:69], v[158:161], v[190:193], v[66:69]
	v_mfma_f32_16x16x32_bf16 v[46:49], v[150:153], v[182:185], v[46:49]
	v_mfma_f32_16x16x32_bf16 v[50:53], v[158:161], v[182:185], v[50:53]
	v_mfma_f32_16x16x32_bf16 v[30:33], v[150:153], v[174:177], v[30:33]
	v_mfma_f32_16x16x32_bf16 v[34:37], v[158:161], v[174:177], v[34:37]
	v_mfma_f32_16x16x32_bf16 v[14:17], v[150:153], v[166:169], v[14:17]
	v_mfma_f32_16x16x32_bf16 v[18:21], v[158:161], v[166:169], v[18:21]
	v_mfma_f32_16x16x32_bf16 v[62:65], v[154:157], v[194:197], v[62:65]
	v_mfma_f32_16x16x32_bf16 v[66:69], v[162:165], v[194:197], v[66:69]
	v_mfma_f32_16x16x32_bf16 v[46:49], v[154:157], v[186:189], v[46:49]
	v_mfma_f32_16x16x32_bf16 v[50:53], v[162:165], v[186:189], v[50:53]
	v_mfma_f32_16x16x32_bf16 v[30:33], v[154:157], v[178:181], v[30:33]
	v_mfma_f32_16x16x32_bf16 v[34:37], v[162:165], v[178:181], v[34:37]
	v_mfma_f32_16x16x32_bf16 v[14:17], v[154:157], v[170:173], v[14:17]
	v_mfma_f32_16x16x32_bf16 v[18:21], v[162:165], v[170:173], v[18:21]
	v_mfma_f32_16x16x32_bf16 v[54:57], v[134:137], v[190:193], v[54:57]
	v_mfma_f32_16x16x32_bf16 v[58:61], v[142:145], v[190:193], v[58:61]
	v_mfma_f32_16x16x32_bf16 v[38:41], v[134:137], v[182:185], v[38:41]
	v_mfma_f32_16x16x32_bf16 v[42:45], v[142:145], v[182:185], v[42:45]
	v_mfma_f32_16x16x32_bf16 v[22:25], v[134:137], v[174:177], v[22:25]
	v_mfma_f32_16x16x32_bf16 v[26:29], v[142:145], v[174:177], v[26:29]
	v_mfma_f32_16x16x32_bf16 v[6:9], v[134:137], v[166:169], v[6:9]
	v_mfma_f32_16x16x32_bf16 v[10:13], v[142:145], v[166:169], v[10:13]
	v_mfma_f32_16x16x32_bf16 v[54:57], v[138:141], v[194:197], v[54:57]
	v_mfma_f32_16x16x32_bf16 v[58:61], v[146:149], v[194:197], v[58:61]
	v_mfma_f32_16x16x32_bf16 v[38:41], v[138:141], v[186:189], v[38:41]
	v_mfma_f32_16x16x32_bf16 v[42:45], v[146:149], v[186:189], v[42:45]
	v_mfma_f32_16x16x32_bf16 v[22:25], v[138:141], v[178:181], v[22:25]
	v_mfma_f32_16x16x32_bf16 v[26:29], v[146:149], v[178:181], v[26:29]
	v_mfma_f32_16x16x32_bf16 v[6:9], v[138:141], v[170:173], v[6:9]
	v_mfma_f32_16x16x32_bf16 v[10:13], v[146:149], v[170:173], v[10:13]
	s_setprio 0
; #define FG_STAGE(bufoff, gbase, v0, v1) do { \
;         __builtin_amdgcn_global_load_lds((const unsigned*)((const char*)(gbase) + (v0)), (LAS unsigned*)(lds + (bufoff) + ldsw), 16, 0, 0); \
;         __builtin_amdgcn_global_load_lds((const unsigned*)((const char*)(gbase) + (v1)), (LAS unsigned*)(lds + (bufoff) + ldsw + 8192), 16, 0, 0); } while (0)
; #define FG_LDA(dst, b, h) do { _Pragma("unroll") for (int m = 0; m < 4; ++m) _Pragma("unroll") for (int k = 0; k < 2; ++k) dst[m][k] = *(const LAS bf16x8*)(lds + FG_SA(b, h) + aoff + m * 2048 + k * 1024); } while (0)
; #define FG_LDB(dst, b, h) do { _Pragma("unroll") for (int n = 0; n < 2; ++n) _Pragma("unroll") for (int k = 0; k < 2; ++k) dst[n][k] = *(const LAS bf16x8*)(lds + FG_SB(b, h) + boff + n * 2048 + k * 1024); } while (0)
; #define FG_MMA(ai, bj, At, Bt) do { __builtin_amdgcn_s_setprio(1); _Pragma("unroll") for (int m = 0; m < 4; ++m) _Pragma("unroll") for (int n = 0; n < 2; ++n) _Pragma("unroll") for (int k = 0; k < 2; ++k) \
;         acc[ai][bj][m][n] = __builtin_amdgcn_mfma_f32_16x16x32_bf16(Bt[n][k], At[m][k], acc[ai][bj][m][n], 0, 0, 0); __builtin_amdgcn_s_setprio(0); } while (0)
; #define FG_WAIT_V(n) asm volatile("s_waitcnt vmcnt(" #n ")" ::: "memory")
; #define FG_WAIT_L(n) asm volatile("s_waitcnt lgkmcnt(" #n ")" ::: "memory")
; #define FG_BAR __builtin_amdgcn_s_barrier()
; #define FG_SCHED __builtin_amdgcn_sched_barrier(0)
; template <bool GATHER, class Unit, class Epi, class Sched>
; __device__ __forceinline__ void gemm_phase(LAS unsigned char* lds, const int K, const Sched& S, const Epi& E) {
;     ...
;             FG_LDB(B0, 1, 0); FG_LDB(B1, 1, 1); FG_SCHED; FG_LDA(At, 1, 0); FG_STAGE(FG_SA(0, 1), a2, x10, x11);
;             FG_WAIT_V(8); FG_WAIT_L(0); FG_BAR; FG_MMA(0, 0, At, B0); FG_MMA(0, 1, At, B1); FG_BAR; FG_SCHED;
;             FG_LDA(At, 1, 1); FG_STAGE(FG_SB(1, 0), b3, voffB0, voffB1); FG_STAGE(FG_SB(1, 1), b3 + hstepB, voffB0, voffB1); FG_STAGE(FG_SA(1, 0), a3, x00, x01);
;             FG_WAIT_V(8); FG_WAIT_L(0); FG_BAR; if (hi_on) { FG_MMA(1, 0, At, B0); FG_MMA(1, 1, At, B1); } FG_BAR; FG_SCHED;
;         }
;         if (wr == 0) FG_BAR;
.LBB0_918:
	v_mov_b32_e32 v5, v3
	v_lshl_add_u64 v[232:233], s[48:49], 0, v[2:3]
	v_lshl_add_u64 v[4:5], s[48:49], 0, v[4:5]
	s_barrier
	s_add_i32 s66, 0, 0x18000
	v_add_u32_e32 v2, s66, v209
	s_add_i32 s67, 0, 0x1c000
	ds_read_b128 v[150:153], v2
	ds_read_b128 v[154:157], v2 offset:1024
	ds_read_b128 v[158:161], v2 offset:2048
	ds_read_b128 v[162:165], v2 offset:3072
	v_add_u32_e32 v2, s67, v209
	ds_read_b128 v[134:137], v2
	ds_read_b128 v[138:141], v2 offset:1024
	ds_read_b128 v[142:145], v2 offset:2048
	ds_read_b128 v[146:149], v2 offset:3072
	s_mov_b32 m0, s29
	ds_read_b128 v[166:169], v223 offset:32768
	ds_read_b128 v[170:173], v223 offset:33792
	ds_read_b128 v[174:177], v223 offset:34816
	ds_read_b128 v[178:181], v223 offset:35840
	ds_read_b128 v[182:185], v223 offset:36864
	ds_read_b128 v[186:189], v223 offset:37888
	ds_read_b128 v[190:193], v223 offset:38912
	ds_read_b128 v[194:197], v223 offset:39936
	global_load_lds_dwordx4 v207, s[48:49]
	s_mov_b32 m0, s30
	s_nop 0
	global_load_lds_dwordx4 v205, s[48:49]
	s_waitcnt vmcnt(8)
	s_waitcnt lgkmcnt(0)
	s_barrier
	s_setprio 1
	s_waitcnt lgkmcnt(0)
	v_mfma_f32_16x16x32_bf16 v[130:133], v[150:153], v[166:169], v[130:133]
	v_mfma_f32_16x16x32_bf16 v[126:129], v[158:161], v[166:169], v[126:129]
	v_mfma_f32_16x16x32_bf16 v[114:117], v[150:153], v[174:177], v[114:117]
	v_mfma_f32_16x16x32_bf16 v[110:113], v[158:161], v[174:177], v[110:113]
	v_mfma_f32_16x16x32_bf16 v[98:101], v[150:153], v[182:185], v[98:101]
	v_mfma_f32_16x16x32_bf16 v[94:97], v[158:161], v[182:185], v[94:97]
	v_mfma_f32_16x16x32_bf16 v[82:85], v[150:153], v[190:193], v[82:85]
	v_mfma_f32_16x16x32_bf16 v[78:81], v[158:161], v[190:193], v[78:81]
	v_mfma_f32_16x16x32_bf16 v[130:133], v[154:157], v[170:173], v[130:133]
	v_mfma_f32_16x16x32_bf16 v[126:129], v[162:165], v[170:173], v[126:129]
	v_mfma_f32_16x16x32_bf16 v[114:117], v[154:157], v[178:181], v[114:117]
	v_mfma_f32_16x16x32_bf16 v[110:113], v[162:165], v[178:181], v[110:113]
	v_mfma_f32_16x16x32_bf16 v[98:101], v[154:157], v[186:189], v[98:101]
	v_mfma_f32_16x16x32_bf16 v[94:97], v[162:165], v[186:189], v[94:97]
	v_mfma_f32_16x16x32_bf16 v[82:85], v[154:157], v[194:197], v[82:85]
	v_mfma_f32_16x16x32_bf16 v[78:81], v[162:165], v[194:197], v[78:81]
	v_mfma_f32_16x16x32_bf16 v[122:125], v[134:137], v[166:169], v[122:125]
	v_mfma_f32_16x16x32_bf16 v[118:121], v[142:145], v[166:169], v[118:121]
	v_mfma_f32_16x16x32_bf16 v[106:109], v[134:137], v[174:177], v[106:109]
	v_mfma_f32_16x16x32_bf16 v[102:105], v[142:145], v[174:177], v[102:105]
	v_mfma_f32_16x16x32_bf16 v[90:93], v[134:137], v[182:185], v[90:93]
	v_mfma_f32_16x16x32_bf16 v[86:89], v[142:145], v[182:185], v[86:89]
	v_mfma_f32_16x16x32_bf16 v[74:77], v[134:137], v[190:193], v[74:77]
	v_mfma_f32_16x16x32_bf16 v[70:73], v[142:145], v[190:193], v[70:73]
	v_mfma_f32_16x16x32_bf16 v[122:125], v[138:141], v[170:173], v[122:125]
	v_mfma_f32_16x16x32_bf16 v[118:121], v[146:149], v[170:173], v[118:121]
	v_mfma_f32_16x16x32_bf16 v[106:109], v[138:141], v[178:181], v[106:109]
	v_mfma_f32_16x16x32_bf16 v[102:105], v[146:149], v[178:181], v[102:105]
	v_mfma_f32_16x16x32_bf16 v[90:93], v[138:141], v[186:189], v[90:93]
	v_mfma_f32_16x16x32_bf16 v[86:89], v[146:149], v[186:189], v[86:89]
	v_mfma_f32_16x16x32_bf16 v[74:77], v[138:141], v[194:197], v[74:77]
	v_mfma_f32_16x16x32_bf16 v[70:73], v[146:149], v[194:197], v[70:73]
	s_setprio 0
	s_barrier
	s_add_i32 s48, s66, s26
	v_lshl_add_u64 v[214:215], v[214:215], 0, s[20:21]
	s_mov_b32 m0, s48
	ds_read_b128 v[190:193], v223 offset:49152
	ds_read_b128 v[194:197], v223 offset:50176
	ds_read_b128 v[182:185], v223 offset:51200
	ds_read_b128 v[186:189], v223 offset:52224
	ds_read_b128 v[174:177], v223 offset:53248
	ds_read_b128 v[178:181], v223 offset:54272
	ds_read_b128 v[166:169], v223 offset:55296
	ds_read_b128 v[170:173], v223 offset:56320
	global_load_lds_dwordx4 v[214:215], off
	s_add_i32 m0, s48, 0x2000
	s_add_u32 s46, s46, 0x80080
	v_lshl_add_u64 v[214:215], v[216:217], 0, s[20:21]
	s_addc_u32 s47, s47, 0
	s_add_i32 s48, s67, s26
	global_load_lds_dwordx4 v[214:215], off
	v_lshl_add_u64 v[214:215], s[46:47], 0, v[198:199]
	s_mov_b32 m0, s48
	v_lshl_add_u64 v[4:5], v[4:5], 0, s[20:21]
	global_load_lds_dwordx4 v[214:215], off
	v_lshl_add_u64 v[214:215], s[46:47], 0, v[200:201]
	s_add_i32 m0, s48, 0x2000
	s_and_b64 vcc, exec, s[10:11]
	global_load_lds_dwordx4 v[214:215], off
	v_lshl_add_u64 v[214:215], v[232:233], 0, s[20:21]
	s_mov_b32 m0, s52
	s_nop 0
	global_load_lds_dwordx4 v[214:215], off
	s_mov_b32 m0, s53
	s_nop 0
	global_load_lds_dwordx4 v[4:5], off
	s_waitcnt vmcnt(8)
	s_waitcnt lgkmcnt(0)
	s_barrier
	s_cbranch_vccnz .LBB0_913
	s_setprio 1
	s_waitcnt lgkmcnt(0)
	v_mfma_f32_16x16x32_bf16 v[62:65], v[150:153], v[190:193], v[62:65]
	v_mfma_f32_16x16x32_bf16 v[66:69], v[158:161], v[190:193], v[66:69]
	v_mfma_f32_16x16x32_bf16 v[46:49], v[150:153], v[182:185], v[46:49]
	v_mfma_f32_16x16x32_bf16 v[50:53], v[158:161], v[182:185], v[50:53]
	v_mfma_f32_16x16x32_bf16 v[30:33], v[150:153], v[174:177], v[30:33]
	v_mfma_f32_16x16x32_bf16 v[34:37], v[158:161], v[174:177], v[34:37]
	v_mfma_f32_16x16x32_bf16 v[14:17], v[150:153], v[166:169], v[14:17]
	v_mfma_f32_16x16x32_bf16 v[18:21], v[158:161], v[166:169], v[18:21]
	v_mfma_f32_16x16x32_bf16 v[62:65], v[154:157], v[194:197], v[62:65]
	v_mfma_f32_16x16x32_bf16 v[66:69], v[162:165], v[194:197], v[66:69]
	v_mfma_f32_16x16x32_bf16 v[46:49], v[154:157], v[186:189], v[46:49]
	v_mfma_f32_16x16x32_bf16 v[50:53], v[162:165], v[186:189], v[50:53]
	v_mfma_f32_16x16x32_bf16 v[30:33], v[154:157], v[178:181], v[30:33]
	v_mfma_f32_16x16x32_bf16 v[34:37], v[162:165], v[178:181], v[34:37]
	v_mfma_f32_16x16x32_bf16 v[14:17], v[154:157], v[170:173], v[14:17]
	v_mfma_f32_16x16x32_bf16 v[18:21], v[162:165], v[170:173], v[18:21]
	v_mfma_f32_16x16x32_bf16 v[54:57], v[134:137], v[190:193], v[54:57]
	v_mfma_f32_16x16x32_bf16 v[58:61], v[142:145], v[190:193], v[58:61]
	v_mfma_f32_16x16x32_bf16 v[38:41], v[134:137], v[182:185], v[38:41]
	v_mfma_f32_16x16x32_bf16 v[42:45], v[142:145], v[182:185], v[42:45]
	v_mfma_f32_16x16x32_bf16 v[22:25], v[134:137], v[174:177], v[22:25]
	v_mfma_f32_16x16x32_bf16 v[26:29], v[142:145], v[174:177], v[26:29]
	v_mfma_f32_16x16x32_bf16 v[4:7], v[134:137], v[166:169], v[6:9]
	v_mfma_f32_16x16x32_bf16 v[10:13], v[142:145], v[166:169], v[10:13]
	v_mfma_f32_16x16x32_bf16 v[54:57], v[138:141], v[194:197], v[54:57]
	v_mfma_f32_16x16x32_bf16 v[58:61], v[146:149], v[194:197], v[58:61]
	v_mfma_f32_16x16x32_bf16 v[38:41], v[138:141], v[186:189], v[38:41]
	v_mfma_f32_16x16x32_bf16 v[42:45], v[146:149], v[186:189], v[42:45]
	v_mfma_f32_16x16x32_bf16 v[22:25], v[138:141], v[178:181], v[22:25]
	v_mfma_f32_16x16x32_bf16 v[26:29], v[146:149], v[178:181], v[26:29]
	v_mfma_f32_16x16x32_bf16 v[6:9], v[138:141], v[170:173], v[4:7]
	v_mfma_f32_16x16x32_bf16 v[10:13], v[146:149], v[170:173], v[10:13]
	s_setprio 0
	s_branch .LBB0_913

; #define FG_STAGE(bufoff, gbase, v0, v1) do { \
;         __builtin_amdgcn_global_load_lds((const unsigned*)((const char*)(gbase) + (v0)), (LAS unsigned*)(lds + (bufoff) + ldsw), 16, 0, 0); \
;         __builtin_amdgcn_global_load_lds((const unsigned*)((const char*)(gbase) + (v1)), (LAS unsigned*)(lds + (bufoff) + ldsw + 8192), 16, 0, 0); } while (0)
; #define FG_LDA(dst, b, h) do { _Pragma("unroll") for (int m = 0; m < 4; ++m) _Pragma("unroll") for (int k = 0; k < 2; ++k) dst[m][k] = *(const LAS bf16x8*)(lds + FG_SA(b, h) + aoff + m * 2048 + k * 1024); } while (0)
; #define FG_LDB(dst, b, h) do { _Pragma("unroll") for (int n = 0; n < 2; ++n) _Pragma("unroll") for (int k = 0; k < 2; ++k) dst[n][k] = *(const LAS bf16x8*)(lds + FG_SB(b, h) + boff + n * 2048 + k * 1024); } while (0)
; #define FG_MMA(ai, bj, At, Bt) do { __builtin_amdgcn_s_setprio(1); _Pragma("unroll") for (int m = 0; m < 4; ++m) _Pragma("unroll") for (int n = 0; n < 2; ++n) _Pragma("unroll") for (int k = 0; k < 2; ++k) \
;         acc[ai][bj][m][n] = __builtin_amdgcn_mfma_f32_16x16x32_bf16(Bt[n][k], At[m][k], acc[ai][bj][m][n], 0, 0, 0); __builtin_amdgcn_s_setprio(0); } while (0)
; template <bool GATHER, class Unit, class Epi, class Sched>
; __device__ __forceinline__ void gemm_phase(LAS unsigned char* lds, const int K, const Sched& S, const Epi& E) {
;     ...
;         for (int t = 0; t < nt; t += 2) {
;             const bool last = (t == nt - 2);
;             const char* a1 = cA + (size_t)(t + 1) * kstep;
;             const char* a2 = last ? nA : cA + (size_t)(t + 2) * kstep; const char* b2 = last ? nB : cB + (size_t)(t + 2) * kstep;
;             const char* a3 = a2 + kstep; const char* b3 = b2 + kstep;
;             const unsigned x00 = (GATHER && last) ? vN00 : vA00, x01 = (GATHER && last) ? vN01 : vA01, x10 = (GATHER && last) ? vN10 : vA10, x11 = (GATHER && last) ? vN11 : vA11;
;             FG_LDB(B0, 0, 0); FG_LDB(B1, 0, 1); FG_SCHED; FG_LDA(At, 0, 0); FG_STAGE(FG_SA(1, 1), a1, vA10, vA11);
;             FG_WAIT_V(8); FG_WAIT_L(0); FG_BAR; FG_MMA(0, 0, At, B0); FG_MMA(0, 1, At, B1); FG_BAR; FG_SCHED;
;             FG_LDA(At, 0, 1); FG_STAGE(FG_SB(0, 0), b2, voffB0, voffB1); FG_STAGE(FG_SB(0, 1), b2 + hstepB, voffB0, voffB1); FG_STAGE(FG_SA(0, 0), a2, x00, x01);
;             FG_WAIT_V(8); FG_WAIT_L(0); FG_BAR; if (hi_on) { FG_MMA(1, 0, At, B0); FG_MMA(1, 1, At, B1); } FG_BAR; FG_SCHED;
.LBB0_1046:
	ds_read_b128 v[150:153], v220
	ds_read_b128 v[154:157], v220 offset:1024
	ds_read_b128 v[158:161], v220 offset:2048
	ds_read_b128 v[162:165], v220 offset:3072
	ds_read_b128 v[134:137], v221
	ds_read_b128 v[138:141], v221 offset:1024
	ds_read_b128 v[142:145], v221 offset:2048
	ds_read_b128 v[146:149], v221 offset:3072
	s_add_u32 s8, s12, 0x80
	s_addc_u32 s9, s13, 0
	s_cmp_eq_u32 s49, 4
	s_cselect_b32 s17, s11, s9
	s_cselect_b32 s16, s19, s8
	s_cselect_b32 s15, s37, s48
	s_cselect_b32 s14, s39, s47
	v_lshl_add_u64 v[4:5], s[12:13], 0, v[212:213]
	s_add_i32 m0, s27, 0xc000
	ds_read_b128 v[166:169], v222
	ds_read_b128 v[170:173], v222 offset:1024
	ds_read_b128 v[174:177], v222 offset:2048
	ds_read_b128 v[178:181], v222 offset:3072
	ds_read_b128 v[182:185], v222 offset:4096
	ds_read_b128 v[186:189], v222 offset:5120
	ds_read_b128 v[190:193], v222 offset:6144
	ds_read_b128 v[194:197], v222 offset:7168
	global_load_lds_dwordx4 v[4:5], off
	v_lshl_add_u64 v[4:5], s[12:13], 0, v[210:211]
	s_add_i32 m0, s27, 0xe000
	s_nop 0
	global_load_lds_dwordx4 v[4:5], off
	s_waitcnt vmcnt(8)
	s_waitcnt lgkmcnt(0)
	s_barrier
	s_setprio 1
	s_waitcnt lgkmcnt(0)
	v_mfma_f32_16x16x32_bf16 v[130:133], v[150:153], v[166:169], v[130:133]
	v_mfma_f32_16x16x32_bf16 v[126:129], v[158:161], v[166:169], v[126:129]
	v_mfma_f32_16x16x32_bf16 v[114:117], v[150:153], v[174:177], v[114:117]
	v_mfma_f32_16x16x32_bf16 v[110:113], v[158:161], v[174:177], v[110:113]
	v_mfma_f32_16x16x32_bf16 v[98:101], v[150:153], v[182:185], v[98:101]
	v_mfma_f32_16x16x32_bf16 v[94:97], v[158:161], v[182:185], v[94:97]
	v_mfma_f32_16x16x32_bf16 v[82:85], v[150:153], v[190:193], v[82:85]
	v_mfma_f32_16x16x32_bf16 v[78:81], v[158:161], v[190:193], v[78:81]
	v_mfma_f32_16x16x32_bf16 v[130:133], v[154:157], v[170:173], v[130:133]
	v_mfma_f32_16x16x32_bf16 v[126:129], v[162:165], v[170:173], v[126:129]
	v_mfma_f32_16x16x32_bf16 v[114:117], v[154:157], v[178:181], v[114:117]
	v_mfma_f32_16x16x32_bf16 v[110:113], v[162:165], v[178:181], v[110:113]
	v_mfma_f32_16x16x32_bf16 v[98:101], v[154:157], v[186:189], v[98:101]
	v_mfma_f32_16x16x32_bf16 v[94:97], v[162:165], v[186:189], v[94:97]
	v_mfma_f32_16x16x32_bf16 v[82:85], v[154:157], v[194:197], v[82:85]
	v_mfma_f32_16x16x32_bf16 v[78:81], v[162:165], v[194:197], v[78:81]
	v_mfma_f32_16x16x32_bf16 v[122:125], v[134:137], v[166:169], v[122:125]
	v_mfma_f32_16x16x32_bf16 v[118:121], v[142:145], v[166:169], v[118:121]
	v_mfma_f32_16x16x32_bf16 v[106:109], v[134:137], v[174:177], v[106:109]
	v_mfma_f32_16x16x32_bf16 v[102:105], v[142:145], v[174:177], v[102:105]
	v_mfma_f32_16x16x32_bf16 v[90:93], v[134:137], v[182:185], v[90:93]
	v_mfma_f32_16x16x32_bf16 v[86:89], v[142:145], v[182:185], v[86:89]
	v_mfma_f32_16x16x32_bf16 v[74:77], v[134:137], v[190:193], v[74:77]
	v_mfma_f32_16x16x32_bf16 v[70:73], v[142:145], v[190:193], v[70:73]
	v_mfma_f32_16x16x32_bf16 v[122:125], v[138:141], v[170:173], v[122:125]
	v_mfma_f32_16x16x32_bf16 v[118:121], v[146:149], v[170:173], v[118:121]
	v_mfma_f32_16x16x32_bf16 v[106:109], v[138:141], v[178:181], v[106:109]
	v_mfma_f32_16x16x32_bf16 v[102:105], v[146:149], v[178:181], v[102:105]
	v_mfma_f32_16x16x32_bf16 v[90:93], v[138:141], v[186:189], v[90:93]
	v_mfma_f32_16x16x32_bf16 v[86:89], v[146:149], v[186:189], v[86:89]
	v_mfma_f32_16x16x32_bf16 v[74:77], v[138:141], v[194:197], v[74:77]
	v_mfma_f32_16x16x32_bf16 v[70:73], v[146:149], v[194:197], v[70:73]
	s_setprio 0
	s_barrier
	s_add_i32 s8, s61, s26
	v_lshl_add_u64 v[4:5], s[14:15], 0, v[198:199]
	s_mov_b32 m0, s8
	ds_read_b128 v[190:193], v222 offset:16384
	ds_read_b128 v[194:197], v222 offset:17408
	ds_read_b128 v[182:185], v222 offset:18432
	ds_read_b128 v[186:189], v222 offset:19456
	ds_read_b128 v[174:177], v222 offset:20480
	ds_read_b128 v[178:181], v222 offset:21504
	ds_read_b128 v[166:169], v222 offset:22528
	ds_read_b128 v[170:173], v222 offset:23552
	global_load_lds_dwordx4 v[4:5], off
	s_add_i32 m0, s8, 0x2000
	s_add_u32 s8, s14, 0x20000
	v_lshl_add_u64 v[214:215], s[14:15], 0, v[200:201]
	s_addc_u32 s9, s15, 0
	s_add_i32 s50, s62, s26
	global_load_lds_dwordx4 v[214:215], off
	v_lshl_add_u64 v[216:217], s[8:9], 0, v[198:199]
	s_mov_b32 m0, s50
	v_lshl_add_u64 v[218:219], s[16:17], 0, v[204:205]
	global_load_lds_dwordx4 v[216:217], off
	v_lshl_add_u64 v[216:217], s[8:9], 0, v[200:201]
	s_add_i32 m0, s50, 0x2000
	v_cmp_ne_u32_e64 s[8:9], 1, v225
	global_load_lds_dwordx4 v[216:217], off
	v_lshl_add_u64 v[216:217], s[16:17], 0, v[202:203]
	s_mov_b32 m0, s27
	s_andn2_b64 vcc, exec, s[6:7]
	global_load_lds_dwordx4 v[216:217], off
	s_mov_b32 m0, s28
	s_nop 0
	global_load_lds_dwordx4 v[218:219], off
	s_waitcnt vmcnt(8)
	s_waitcnt lgkmcnt(0)
	s_barrier
	s_cbranch_vccnz .LBB0_1048
	s_setprio 1
	s_waitcnt lgkmcnt(0)
	v_mfma_f32_16x16x32_bf16 v[66:69], v[150:153], v[190:193], v[66:69]
	v_mfma_f32_16x16x32_bf16 v[62:65], v[158:161], v[190:193], v[62:65]
	v_mfma_f32_16x16x32_bf16 v[50:53], v[150:153], v[182:185], v[50:53]
	v_mfma_f32_16x16x32_bf16 v[46:49], v[158:161], v[182:185], v[46:49]
	v_mfma_f32_16x16x32_bf16 v[34:37], v[150:153], v[174:177], v[34:37]
	v_mfma_f32_16x16x32_bf16 v[30:33], v[158:161], v[174:177], v[30:33]
	v_mfma_f32_16x16x32_bf16 v[18:21], v[150:153], v[166:169], v[18:21]
	v_mfma_f32_16x16x32_bf16 v[14:17], v[158:161], v[166:169], v[14:17]
	v_mfma_f32_16x16x32_bf16 v[66:69], v[154:157], v[194:197], v[66:69]
	v_mfma_f32_16x16x32_bf16 v[62:65], v[162:165], v[194:197], v[62:65]
	v_mfma_f32_16x16x32_bf16 v[50:53], v[154:157], v[186:189], v[50:53]
	v_mfma_f32_16x16x32_bf16 v[46:49], v[162:165], v[186:189], v[46:49]
	v_mfma_f32_16x16x32_bf16 v[34:37], v[154:157], v[178:181], v[34:37]
	v_mfma_f32_16x16x32_bf16 v[30:33], v[162:165], v[178:181], v[30:33]
	v_mfma_f32_16x16x32_bf16 v[18:21], v[154:157], v[170:173], v[18:21]
	v_mfma_f32_16x16x32_bf16 v[14:17], v[162:165], v[170:173], v[14:17]
	v_mfma_f32_16x16x32_bf16 v[58:61], v[134:137], v[190:193], v[58:61]
	v_mfma_f32_16x16x32_bf16 v[54:57], v[142:145], v[190:193], v[54:57]
	v_mfma_f32_16x16x32_bf16 v[42:45], v[134:137], v[182:185], v[42:45]
	v_mfma_f32_16x16x32_bf16 v[38:41], v[142:145], v[182:185], v[38:41]
	v_mfma_f32_16x16x32_bf16 v[26:29], v[134:137], v[174:177], v[26:29]
	v_mfma_f32_16x16x32_bf16 v[22:25], v[142:145], v[174:177], v[22:25]
	v_mfma_f32_16x16x32_bf16 v[10:13], v[134:137], v[166:169], v[10:13]
	v_mfma_f32_16x16x32_bf16 v[6:9], v[142:145], v[166:169], v[6:9]
	v_mfma_f32_16x16x32_bf16 v[58:61], v[138:141], v[194:197], v[58:61]
	v_mfma_f32_16x16x32_bf16 v[54:57], v[146:149], v[194:197], v[54:57]
	v_mfma_f32_16x16x32_bf16 v[42:45], v[138:141], v[186:189], v[42:45]
	v_mfma_f32_16x16x32_bf16 v[38:41], v[146:149], v[186:189], v[38:41]
	v_mfma_f32_16x16x32_bf16 v[26:29], v[138:141], v[178:181], v[26:29]
	v_mfma_f32_16x16x32_bf16 v[22:25], v[146:149], v[178:181], v[22:25]
	v_mfma_f32_16x16x32_bf16 v[10:13], v[138:141], v[170:173], v[10:13]
	v_mfma_f32_16x16x32_bf16 v[6:9], v[146:149], v[170:173], v[6:9]
	s_setprio 0
; #define FG_STAGE(bufoff, gbase, v0, v1) do { \
;         __builtin_amdgcn_global_load_lds((const unsigned*)((const char*)(gbase) + (v0)), (LAS unsigned*)(lds + (bufoff) + ldsw), 16, 0, 0); \
;         __builtin_amdgcn_global_load_lds((const unsigned*)((const char*)(gbase) + (v1)), (LAS unsigned*)(lds + (bufoff) + ldsw + 8192), 16, 0, 0); } while (0)
; #define FG_LDA(dst, b, h) do { _Pragma("unroll") for (int m = 0; m < 4; ++m) _Pragma("unroll") for (int k = 0; k < 2; ++k) dst[m][k] = *(const LAS bf16x8*)(lds + FG_SA(b, h) + aoff + m * 2048 + k * 1024); } while (0)
; #define FG_LDB(dst, b, h) do { _Pragma("unroll") for (int n = 0; n < 2; ++n) _Pragma("unroll") for (int k = 0; k < 2; ++k) dst[n][k] = *(const LAS bf16x8*)(lds + FG_SB(b, h) + boff + n * 2048 + k * 1024); } while (0)
; #define FG_MMA(ai, bj, At, Bt) do { __builtin_amdgcn_s_setprio(1); _Pragma("unroll") for (int m = 0; m < 4; ++m) _Pragma("unroll") for (int n = 0; n < 2; ++n) _Pragma("unroll") for (int k = 0; k < 2; ++k) \
;         acc[ai][bj][m][n] = __builtin_amdgcn_mfma_f32_16x16x32_bf16(Bt[n][k], At[m][k], acc[ai][bj][m][n], 0, 0, 0); __builtin_amdgcn_s_setprio(0); } while (0)
; #define FG_WAIT_V(n) asm volatile("s_waitcnt vmcnt(" #n ")" ::: "memory")
; #define FG_WAIT_L(n) asm volatile("s_waitcnt lgkmcnt(" #n ")" ::: "memory")
; #define FG_BAR __builtin_amdgcn_s_barrier()
; #define FG_SCHED __builtin_amdgcn_sched_barrier(0)
; template <bool GATHER, class Unit, class Epi, class Sched>
; __device__ __forceinline__ void gemm_phase(LAS unsigned char* lds, const int K, const Sched& S, const Epi& E) {
;     ...
;             FG_WAIT_V(8); FG_WAIT_L(0); FG_BAR; if (hi_on) { FG_MMA(1, 0, At, B0); FG_MMA(1, 1, At, B1); } FG_BAR; FG_SCHED;
;             FG_LDB(B0, 1, 0); FG_LDB(B1, 1, 1); FG_SCHED; FG_LDA(At, 1, 0); FG_STAGE(FG_SA(0, 1), a2, x10, x11);
;             FG_WAIT_V(8); FG_WAIT_L(0); FG_BAR; FG_MMA(0, 0, At, B0); FG_MMA(0, 1, At, B1); FG_BAR; FG_SCHED;
;             FG_LDA(At, 1, 1); FG_STAGE(FG_SB(1, 0), b3, voffB0, voffB1); FG_STAGE(FG_SB(1, 1), b3 + hstepB, voffB0, voffB1); FG_STAGE(FG_SA(1, 0), a3, x00, x01);
;             FG_WAIT_V(8); FG_WAIT_L(0); FG_BAR; if (hi_on) { FG_MMA(1, 0, At, B0); FG_MMA(1, 1, At, B1); } FG_BAR; FG_SCHED;
;         }
.LBB0_1048:
	s_barrier
	s_add_i32 s50, 0, 0x18000
	v_add_u32_e32 v2, s50, v1
	s_add_i32 s51, 0, 0x1c000
	ds_read_b128 v[150:153], v2
	ds_read_b128 v[154:157], v2 offset:1024
	ds_read_b128 v[158:161], v2 offset:2048
	ds_read_b128 v[162:165], v2 offset:3072
	v_add_u32_e32 v2, s51, v1
	ds_read_b128 v[134:137], v2
	ds_read_b128 v[138:141], v2 offset:1024
	ds_read_b128 v[142:145], v2 offset:2048
	ds_read_b128 v[146:149], v2 offset:3072
	s_mov_b32 m0, s29
	v_lshl_add_u64 v[226:227], s[16:17], 0, v[206:207]
	ds_read_b128 v[166:169], v222 offset:32768
	ds_read_b128 v[170:173], v222 offset:33792
	ds_read_b128 v[174:177], v222 offset:34816
	ds_read_b128 v[178:181], v222 offset:35840
	ds_read_b128 v[182:185], v222 offset:36864
	ds_read_b128 v[186:189], v222 offset:37888
	ds_read_b128 v[190:193], v222 offset:38912
	ds_read_b128 v[194:197], v222 offset:39936
	global_load_lds_dwordx4 v[226:227], off
	v_lshl_add_u64 v[226:227], s[16:17], 0, v[208:209]
	s_mov_b32 m0, s30
	s_nop 0
	global_load_lds_dwordx4 v[226:227], off
	s_waitcnt vmcnt(8)
	s_waitcnt lgkmcnt(0)
	s_barrier
	s_setprio 1
	s_waitcnt lgkmcnt(0)
	v_mfma_f32_16x16x32_bf16 v[130:133], v[150:153], v[166:169], v[130:133]
	v_mfma_f32_16x16x32_bf16 v[126:129], v[158:161], v[166:169], v[126:129]
	v_mfma_f32_16x16x32_bf16 v[114:117], v[150:153], v[174:177], v[114:117]
	v_mfma_f32_16x16x32_bf16 v[110:113], v[158:161], v[174:177], v[110:113]
	v_mfma_f32_16x16x32_bf16 v[98:101], v[150:153], v[182:185], v[98:101]
	v_mfma_f32_16x16x32_bf16 v[94:97], v[158:161], v[182:185], v[94:97]
	v_mfma_f32_16x16x32_bf16 v[82:85], v[150:153], v[190:193], v[82:85]
	v_mfma_f32_16x16x32_bf16 v[78:81], v[158:161], v[190:193], v[78:81]
	v_mfma_f32_16x16x32_bf16 v[130:133], v[154:157], v[170:173], v[130:133]
	v_mfma_f32_16x16x32_bf16 v[126:129], v[162:165], v[170:173], v[126:129]
	v_mfma_f32_16x16x32_bf16 v[114:117], v[154:157], v[178:181], v[114:117]
	v_mfma_f32_16x16x32_bf16 v[110:113], v[162:165], v[178:181], v[110:113]
	v_mfma_f32_16x16x32_bf16 v[98:101], v[154:157], v[186:189], v[98:101]
	v_mfma_f32_16x16x32_bf16 v[94:97], v[162:165], v[186:189], v[94:97]
	v_mfma_f32_16x16x32_bf16 v[82:85], v[154:157], v[194:197], v[82:85]
	v_mfma_f32_16x16x32_bf16 v[78:81], v[162:165], v[194:197], v[78:81]
	v_mfma_f32_16x16x32_bf16 v[122:125], v[134:137], v[166:169], v[122:125]
	v_mfma_f32_16x16x32_bf16 v[118:121], v[142:145], v[166:169], v[118:121]
	v_mfma_f32_16x16x32_bf16 v[106:109], v[134:137], v[174:177], v[106:109]
	v_mfma_f32_16x16x32_bf16 v[102:105], v[142:145], v[174:177], v[102:105]
	v_mfma_f32_16x16x32_bf16 v[90:93], v[134:137], v[182:185], v[90:93]
	v_mfma_f32_16x16x32_bf16 v[86:89], v[142:145], v[182:185], v[86:89]
	v_mfma_f32_16x16x32_bf16 v[74:77], v[134:137], v[190:193], v[74:77]
	v_mfma_f32_16x16x32_bf16 v[70:73], v[142:145], v[190:193], v[70:73]
	v_mfma_f32_16x16x32_bf16 v[122:125], v[138:141], v[170:173], v[122:125]
	v_mfma_f32_16x16x32_bf16 v[118:121], v[146:149], v[170:173], v[118:121]
	v_mfma_f32_16x16x32_bf16 v[106:109], v[138:141], v[178:181], v[106:109]
	v_mfma_f32_16x16x32_bf16 v[102:105], v[146:149], v[178:181], v[102:105]
	v_mfma_f32_16x16x32_bf16 v[90:93], v[138:141], v[186:189], v[90:93]
	v_mfma_f32_16x16x32_bf16 v[86:89], v[146:149], v[186:189], v[86:89]
	v_mfma_f32_16x16x32_bf16 v[74:77], v[138:141], v[194:197], v[74:77]
	v_mfma_f32_16x16x32_bf16 v[70:73], v[146:149], v[194:197], v[70:73]
	s_setprio 0
	s_barrier
	s_add_i32 s16, s50, s26
	v_lshl_add_u64 v[4:5], v[4:5], 0, s[24:25]
	s_mov_b32 m0, s16
	ds_read_b128 v[190:193], v222 offset:49152
	ds_read_b128 v[194:197], v222 offset:50176
	ds_read_b128 v[182:185], v222 offset:51200
	ds_read_b128 v[186:189], v222 offset:52224
	ds_read_b128 v[174:177], v222 offset:53248
	ds_read_b128 v[178:181], v222 offset:54272
	ds_read_b128 v[166:169], v222 offset:55296
	ds_read_b128 v[170:173], v222 offset:56320
	global_load_lds_dwordx4 v[4:5], off
	s_add_i32 m0, s16, 0x2000
	s_add_u32 s14, s14, 0x20080
	v_lshl_add_u64 v[4:5], v[214:215], 0, s[24:25]
	s_addc_u32 s15, s15, 0
	s_add_i32 s16, s51, s26
	global_load_lds_dwordx4 v[4:5], off
	v_lshl_add_u64 v[4:5], s[14:15], 0, v[198:199]
	s_mov_b32 m0, s16
	s_and_b64 vcc, exec, s[8:9]
	global_load_lds_dwordx4 v[4:5], off
	v_lshl_add_u64 v[4:5], s[14:15], 0, v[200:201]
	s_add_i32 m0, s16, 0x2000
	s_nop 0
	global_load_lds_dwordx4 v[4:5], off
	v_lshl_add_u64 v[4:5], v[216:217], 0, s[24:25]
	s_mov_b32 m0, s55
	s_nop 0
	global_load_lds_dwordx4 v[4:5], off
	v_lshl_add_u64 v[4:5], v[218:219], 0, s[24:25]
	s_mov_b32 m0, s56
	s_nop 0
	global_load_lds_dwordx4 v[4:5], off
	s_waitcnt vmcnt(8)
	s_waitcnt lgkmcnt(0)
	s_barrier
	s_cbranch_vccnz .LBB0_1045
	s_setprio 1
	s_waitcnt lgkmcnt(0)
	v_mfma_f32_16x16x32_bf16 v[66:69], v[150:153], v[190:193], v[66:69]
	v_mfma_f32_16x16x32_bf16 v[62:65], v[158:161], v[190:193], v[62:65]
	v_mfma_f32_16x16x32_bf16 v[50:53], v[150:153], v[182:185], v[50:53]
	v_mfma_f32_16x16x32_bf16 v[46:49], v[158:161], v[182:185], v[46:49]
	v_mfma_f32_16x16x32_bf16 v[34:37], v[150:153], v[174:177], v[34:37]
	v_mfma_f32_16x16x32_bf16 v[30:33], v[158:161], v[174:177], v[30:33]
	v_mfma_f32_16x16x32_bf16 v[18:21], v[150:153], v[166:169], v[18:21]
	v_mfma_f32_16x16x32_bf16 v[14:17], v[158:161], v[166:169], v[14:17]
	v_mfma_f32_16x16x32_bf16 v[66:69], v[154:157], v[194:197], v[66:69]
	v_mfma_f32_16x16x32_bf16 v[62:65], v[162:165], v[194:197], v[62:65]
	v_mfma_f32_16x16x32_bf16 v[50:53], v[154:157], v[186:189], v[50:53]
	v_mfma_f32_16x16x32_bf16 v[46:49], v[162:165], v[186:189], v[46:49]
	v_mfma_f32_16x16x32_bf16 v[34:37], v[154:157], v[178:181], v[34:37]
	v_mfma_f32_16x16x32_bf16 v[30:33], v[162:165], v[178:181], v[30:33]
	v_mfma_f32_16x16x32_bf16 v[18:21], v[154:157], v[170:173], v[18:21]
	v_mfma_f32_16x16x32_bf16 v[14:17], v[162:165], v[170:173], v[14:17]
	v_mfma_f32_16x16x32_bf16 v[58:61], v[134:137], v[190:193], v[58:61]
	v_mfma_f32_16x16x32_bf16 v[54:57], v[142:145], v[190:193], v[54:57]
	v_mfma_f32_16x16x32_bf16 v[42:45], v[134:137], v[182:185], v[42:45]
	v_mfma_f32_16x16x32_bf16 v[38:41], v[142:145], v[182:185], v[38:41]
	v_mfma_f32_16x16x32_bf16 v[26:29], v[134:137], v[174:177], v[26:29]
	v_mfma_f32_16x16x32_bf16 v[22:25], v[142:145], v[174:177], v[22:25]
	v_mfma_f32_16x16x32_bf16 v[10:13], v[134:137], v[166:169], v[10:13]
	v_mfma_f32_16x16x32_bf16 v[4:7], v[142:145], v[166:169], v[6:9]
	v_mfma_f32_16x16x32_bf16 v[58:61], v[138:141], v[194:197], v[58:61]
	v_mfma_f32_16x16x32_bf16 v[54:57], v[146:149], v[194:197], v[54:57]
	v_mfma_f32_16x16x32_bf16 v[42:45], v[138:141], v[186:189], v[42:45]
	v_mfma_f32_16x16x32_bf16 v[38:41], v[146:149], v[186:189], v[38:41]
	v_mfma_f32_16x16x32_bf16 v[26:29], v[138:141], v[178:181], v[26:29]
	v_mfma_f32_16x16x32_bf16 v[22:25], v[146:149], v[178:181], v[22:25]
	v_mfma_f32_16x16x32_bf16 v[10:13], v[138:141], v[170:173], v[10:13]
	v_mfma_f32_16x16x32_bf16 v[6:9], v[146:149], v[170:173], v[4:7]
	s_setprio 0
	s_branch .LBB0_1045

; #define FG_STAGE(bufoff, gbase, v0, v1) do { \
;         __builtin_amdgcn_global_load_lds((const unsigned*)((const char*)(gbase) + (v0)), (LAS unsigned*)(lds + (bufoff) + ldsw), 16, 0, 0); \
;         __builtin_amdgcn_global_load_lds((const unsigned*)((const char*)(gbase) + (v1)), (LAS unsigned*)(lds + (bufoff) + ldsw + 8192), 16, 0, 0); } while (0)
; #define FG_LDA(dst, b, h) do { _Pragma("unroll") for (int m = 0; m < 4; ++m) _Pragma("unroll") for (int k = 0; k < 2; ++k) dst[m][k] = *(const LAS bf16x8*)(lds + FG_SA(b, h) + aoff + m * 2048 + k * 1024); } while (0)
; #define FG_LDB(dst, b, h) do { _Pragma("unroll") for (int n = 0; n < 2; ++n) _Pragma("unroll") for (int k = 0; k < 2; ++k) dst[n][k] = *(const LAS bf16x8*)(lds + FG_SB(b, h) + boff + n * 2048 + k * 1024); } while (0)
; #define FG_MMA(ai, bj, At, Bt) do { __builtin_amdgcn_s_setprio(1); _Pragma("unroll") for (int m = 0; m < 4; ++m) _Pragma("unroll") for (int n = 0; n < 2; ++n) _Pragma("unroll") for (int k = 0; k < 2; ++k) \
;         acc[ai][bj][m][n] = __builtin_amdgcn_mfma_f32_16x16x32_bf16(Bt[n][k], At[m][k], acc[ai][bj][m][n], 0, 0, 0); __builtin_amdgcn_s_setprio(0); } while (0)
; template <bool GATHER, class Unit, class Epi, class Sched>
; __device__ __forceinline__ void gemm_phase(LAS unsigned char* lds, const int K, const Sched& S, const Epi& E) {
;     ...
;         for (int t = 0; t < nt; t += 2) {
;             const bool last = (t == nt - 2);
;             const char* a1 = cA + (size_t)(t + 1) * kstep;
;             const char* a2 = last ? nA : cA + (size_t)(t + 2) * kstep; const char* b2 = last ? nB : cB + (size_t)(t + 2) * kstep;
;             const char* a3 = a2 + kstep; const char* b3 = b2 + kstep;
;             const unsigned x00 = (GATHER && last) ? vN00 : vA00, x01 = (GATHER && last) ? vN01 : vA01, x10 = (GATHER && last) ? vN10 : vA10, x11 = (GATHER && last) ? vN11 : vA11;
;             FG_LDB(B0, 0, 0); FG_LDB(B1, 0, 1); FG_SCHED; FG_LDA(At, 0, 0); FG_STAGE(FG_SA(1, 1), a1, vA10, vA11);
;             FG_WAIT_V(8); FG_WAIT_L(0); FG_BAR; FG_MMA(0, 0, At, B0); FG_MMA(0, 1, At, B1); FG_BAR; FG_SCHED;
;             FG_LDA(At, 0, 1); FG_STAGE(FG_SB(0, 0), b2, voffB0, voffB1); FG_STAGE(FG_SB(0, 1), b2 + hstepB, voffB0, voffB1); FG_STAGE(FG_SA(0, 0), a2, x00, x01);
;             FG_WAIT_V(8); FG_WAIT_L(0); FG_BAR; if (hi_on) { FG_MMA(1, 0, At, B0); FG_MMA(1, 1, At, B1); } FG_BAR; FG_SCHED;
.LBB0_1239:
	ds_read_b128 v[130:133], v161
	ds_read_b128 v[134:137], v161 offset:1024
	ds_read_b128 v[172:175], v161 offset:2048
	ds_read_b128 v[176:179], v161 offset:3072
	ds_read_b128 v[180:183], v163
	ds_read_b128 v[184:187], v163 offset:1024
	ds_read_b128 v[188:191], v163 offset:2048
	ds_read_b128 v[192:195], v163 offset:3072
	s_add_u32 s48, s46, 0x100
	s_addc_u32 s49, s47, 0
	s_cmp_eq_u32 s69, 28
	s_cselect_b32 s53, s37, s49
	s_cselect_b32 s52, s43, s48
	s_cselect_b32 s51, s35, s68
	s_cselect_b32 s50, s45, s67
	v_lshl_add_u64 v[164:165], s[46:47], 0, v[154:155]
	s_add_i32 m0, s28, 0xc000
	ds_read_b128 v[196:199], v167
	ds_read_b128 v[200:203], v167 offset:1024
	ds_read_b128 v[204:207], v167 offset:2048
	ds_read_b128 v[208:211], v167 offset:3072
	ds_read_b128 v[212:215], v167 offset:4096
	ds_read_b128 v[216:219], v167 offset:5120
	ds_read_b128 v[220:223], v167 offset:6144
	ds_read_b128 v[224:227], v167 offset:7168
	global_load_lds_dwordx4 v[164:165], off
	v_lshl_add_u64 v[164:165], s[46:47], 0, v[152:153]
	s_add_i32 m0, s28, 0xe000
	s_nop 0
	global_load_lds_dwordx4 v[164:165], off
	s_waitcnt vmcnt(8)
	s_waitcnt lgkmcnt(0)
	s_barrier
	s_setprio 1
	s_waitcnt lgkmcnt(0)
	v_mfma_f32_16x16x32_bf16 v[126:129], v[130:133], v[196:199], v[126:129]
	v_mfma_f32_16x16x32_bf16 v[122:125], v[172:175], v[196:199], v[122:125]
	v_mfma_f32_16x16x32_bf16 v[118:121], v[130:133], v[204:207], v[118:121]
	v_mfma_f32_16x16x32_bf16 v[110:113], v[172:175], v[204:207], v[110:113]
	v_mfma_f32_16x16x32_bf16 v[102:105], v[130:133], v[212:215], v[102:105]
	v_mfma_f32_16x16x32_bf16 v[94:97], v[172:175], v[212:215], v[94:97]
	v_mfma_f32_16x16x32_bf16 v[86:89], v[130:133], v[220:223], v[86:89]
	v_mfma_f32_16x16x32_bf16 v[78:81], v[172:175], v[220:223], v[78:81]
	v_mfma_f32_16x16x32_bf16 v[126:129], v[134:137], v[200:203], v[126:129]
	v_mfma_f32_16x16x32_bf16 v[122:125], v[176:179], v[200:203], v[122:125]
	v_mfma_f32_16x16x32_bf16 v[118:121], v[134:137], v[208:211], v[118:121]
	v_mfma_f32_16x16x32_bf16 v[110:113], v[176:179], v[208:211], v[110:113]
	v_mfma_f32_16x16x32_bf16 v[102:105], v[134:137], v[216:219], v[102:105]
	v_mfma_f32_16x16x32_bf16 v[94:97], v[176:179], v[216:219], v[94:97]
	v_mfma_f32_16x16x32_bf16 v[86:89], v[134:137], v[224:227], v[86:89]
	v_mfma_f32_16x16x32_bf16 v[78:81], v[176:179], v[224:227], v[78:81]
	v_mfma_f32_16x16x32_bf16 v[114:117], v[180:183], v[196:199], v[114:117]
	v_mfma_f32_16x16x32_bf16 v[106:109], v[188:191], v[196:199], v[106:109]
	v_mfma_f32_16x16x32_bf16 v[98:101], v[180:183], v[204:207], v[98:101]
	v_mfma_f32_16x16x32_bf16 v[90:93], v[188:191], v[204:207], v[90:93]
	v_mfma_f32_16x16x32_bf16 v[82:85], v[180:183], v[212:215], v[82:85]
	v_mfma_f32_16x16x32_bf16 v[74:77], v[188:191], v[212:215], v[74:77]
	v_mfma_f32_16x16x32_bf16 v[70:73], v[180:183], v[220:223], v[70:73]
	v_mfma_f32_16x16x32_bf16 v[66:69], v[188:191], v[220:223], v[66:69]
	v_mfma_f32_16x16x32_bf16 v[114:117], v[184:187], v[200:203], v[114:117]
	v_mfma_f32_16x16x32_bf16 v[106:109], v[192:195], v[200:203], v[106:109]
	v_mfma_f32_16x16x32_bf16 v[98:101], v[184:187], v[208:211], v[98:101]
	v_mfma_f32_16x16x32_bf16 v[90:93], v[192:195], v[208:211], v[90:93]
	v_mfma_f32_16x16x32_bf16 v[82:85], v[184:187], v[216:219], v[82:85]
	v_mfma_f32_16x16x32_bf16 v[74:77], v[192:195], v[216:219], v[74:77]
	v_mfma_f32_16x16x32_bf16 v[70:73], v[184:187], v[224:227], v[70:73]
	v_mfma_f32_16x16x32_bf16 v[66:69], v[192:195], v[224:227], v[66:69]
	s_setprio 0
	s_barrier
	s_add_i32 s46, s58, s27
	v_lshl_add_u64 v[164:165], s[50:51], 0, v[138:139]
	s_mov_b32 m0, s46
	ds_read_b128 v[196:199], v167 offset:16384
	ds_read_b128 v[200:203], v167 offset:17408
	ds_read_b128 v[204:207], v167 offset:18432
	ds_read_b128 v[208:211], v167 offset:19456
	ds_read_b128 v[212:215], v167 offset:20480
	ds_read_b128 v[216:219], v167 offset:21504
	ds_read_b128 v[220:223], v167 offset:22528
	ds_read_b128 v[224:227], v167 offset:23552
	global_load_lds_dwordx4 v[164:165], off
	s_add_i32 m0, s46, 0x2000
	s_add_u32 s46, s50, 0x80000
	v_lshl_add_u64 v[228:229], s[50:51], 0, v[140:141]
	s_addc_u32 s47, s51, 0
	s_add_i32 s70, s59, s27
	global_load_lds_dwordx4 v[228:229], off
	v_lshl_add_u64 v[230:231], s[46:47], 0, v[138:139]
	s_mov_b32 m0, s70
	v_lshl_add_u64 v[232:233], s[52:53], 0, v[144:145]
	global_load_lds_dwordx4 v[230:231], off
	v_lshl_add_u64 v[230:231], s[46:47], 0, v[140:141]
	s_add_i32 m0, s70, 0x2000
	s_nop 0
	global_load_lds_dwordx4 v[230:231], off
	v_lshl_add_u64 v[230:231], s[52:53], 0, v[142:143]
	s_mov_b32 m0, s28
	s_nop 0
	global_load_lds_dwordx4 v[230:231], off
	s_mov_b32 m0, s29
	s_nop 0
	global_load_lds_dwordx4 v[232:233], off
	s_waitcnt vmcnt(8)
	s_waitcnt lgkmcnt(0)
	s_barrier
; #define FG_STAGE(bufoff, gbase, v0, v1) do { \
;         __builtin_amdgcn_global_load_lds((const unsigned*)((const char*)(gbase) + (v0)), (LAS unsigned*)(lds + (bufoff) + ldsw), 16, 0, 0); \
;         __builtin_amdgcn_global_load_lds((const unsigned*)((const char*)(gbase) + (v1)), (LAS unsigned*)(lds + (bufoff) + ldsw + 8192), 16, 0, 0); } while (0)
; #define FG_LDA(dst, b, h) do { _Pragma("unroll") for (int m = 0; m < 4; ++m) _Pragma("unroll") for (int k = 0; k < 2; ++k) dst[m][k] = *(const LAS bf16x8*)(lds + FG_SA(b, h) + aoff + m * 2048 + k * 1024); } while (0)
; #define FG_LDB(dst, b, h) do { _Pragma("unroll") for (int n = 0; n < 2; ++n) _Pragma("unroll") for (int k = 0; k < 2; ++k) dst[n][k] = *(const LAS bf16x8*)(lds + FG_SB(b, h) + boff + n * 2048 + k * 1024); } while (0)
; #define FG_MMA(ai, bj, At, Bt) do { __builtin_amdgcn_s_setprio(1); _Pragma("unroll") for (int m = 0; m < 4; ++m) _Pragma("unroll") for (int n = 0; n < 2; ++n) _Pragma("unroll") for (int k = 0; k < 2; ++k) \
;         acc[ai][bj][m][n] = __builtin_amdgcn_mfma_f32_16x16x32_bf16(Bt[n][k], At[m][k], acc[ai][bj][m][n], 0, 0, 0); __builtin_amdgcn_s_setprio(0); } while (0)
; #define FG_WAIT_V(n) asm volatile("s_waitcnt vmcnt(" #n ")" ::: "memory")
; #define FG_WAIT_L(n) asm volatile("s_waitcnt lgkmcnt(" #n ")" ::: "memory")
; #define FG_BAR __builtin_amdgcn_s_barrier()
; #define FG_SCHED __builtin_amdgcn_sched_barrier(0)
; template <bool GATHER, class Unit, class Epi, class Sched>
; __device__ __forceinline__ void gemm_phase(LAS unsigned char* lds, const int K, const Sched& S, const Epi& E) {
;     ...
;             FG_WAIT_V(8); FG_WAIT_L(0); FG_BAR; if (hi_on) { FG_MMA(1, 0, At, B0); FG_MMA(1, 1, At, B1); } FG_BAR; FG_SCHED;
;             FG_LDB(B0, 1, 0); FG_LDB(B1, 1, 1); FG_SCHED; FG_LDA(At, 1, 0); FG_STAGE(FG_SA(0, 1), a2, x10, x11);
;             FG_WAIT_V(8); FG_WAIT_L(0); FG_BAR; FG_MMA(0, 0, At, B0); FG_MMA(0, 1, At, B1); FG_BAR; FG_SCHED;
	s_setprio 1
	s_waitcnt lgkmcnt(0)
	v_mfma_f32_16x16x32_bf16 v[62:65], v[130:133], v[196:199], v[62:65]
	v_mfma_f32_16x16x32_bf16 v[58:61], v[172:175], v[196:199], v[58:61]
	v_mfma_f32_16x16x32_bf16 v[54:57], v[130:133], v[204:207], v[54:57]
	v_mfma_f32_16x16x32_bf16 v[46:49], v[172:175], v[204:207], v[46:49]
	v_mfma_f32_16x16x32_bf16 v[38:41], v[130:133], v[212:215], v[38:41]
	v_mfma_f32_16x16x32_bf16 v[30:33], v[172:175], v[212:215], v[30:33]
	v_mfma_f32_16x16x32_bf16 v[22:25], v[130:133], v[220:223], v[22:25]
	v_mfma_f32_16x16x32_bf16 v[14:17], v[172:175], v[220:223], v[14:17]
	v_mfma_f32_16x16x32_bf16 v[62:65], v[134:137], v[200:203], v[62:65]
	v_mfma_f32_16x16x32_bf16 v[58:61], v[176:179], v[200:203], v[58:61]
	v_mfma_f32_16x16x32_bf16 v[54:57], v[134:137], v[208:211], v[54:57]
	v_mfma_f32_16x16x32_bf16 v[46:49], v[176:179], v[208:211], v[46:49]
	v_mfma_f32_16x16x32_bf16 v[38:41], v[134:137], v[216:219], v[38:41]
	v_mfma_f32_16x16x32_bf16 v[30:33], v[176:179], v[216:219], v[30:33]
	v_mfma_f32_16x16x32_bf16 v[22:25], v[134:137], v[224:227], v[22:25]
	v_mfma_f32_16x16x32_bf16 v[14:17], v[176:179], v[224:227], v[14:17]
	v_mfma_f32_16x16x32_bf16 v[50:53], v[180:183], v[196:199], v[50:53]
	v_mfma_f32_16x16x32_bf16 v[42:45], v[188:191], v[196:199], v[42:45]
	v_mfma_f32_16x16x32_bf16 v[34:37], v[180:183], v[204:207], v[34:37]
	v_mfma_f32_16x16x32_bf16 v[26:29], v[188:191], v[204:207], v[26:29]
	v_mfma_f32_16x16x32_bf16 v[18:21], v[180:183], v[212:215], v[18:21]
	v_mfma_f32_16x16x32_bf16 v[10:13], v[188:191], v[212:215], v[10:13]
	v_mfma_f32_16x16x32_bf16 v[6:9], v[180:183], v[220:223], v[6:9]
	v_mfma_f32_16x16x32_bf16 v[2:5], v[188:191], v[220:223], v[2:5]
	v_mfma_f32_16x16x32_bf16 v[50:53], v[184:187], v[200:203], v[50:53]
	v_mfma_f32_16x16x32_bf16 v[42:45], v[192:195], v[200:203], v[42:45]
	v_mfma_f32_16x16x32_bf16 v[34:37], v[184:187], v[208:211], v[34:37]
	v_mfma_f32_16x16x32_bf16 v[26:29], v[192:195], v[208:211], v[26:29]
	v_mfma_f32_16x16x32_bf16 v[18:21], v[184:187], v[216:219], v[18:21]
	v_mfma_f32_16x16x32_bf16 v[10:13], v[192:195], v[216:219], v[10:13]
	v_mfma_f32_16x16x32_bf16 v[6:9], v[184:187], v[224:227], v[6:9]
	v_mfma_f32_16x16x32_bf16 v[2:5], v[192:195], v[224:227], v[2:5]
	s_setprio 0
	s_barrier
	s_add_i32 s46, 0, 0x18000
	v_add_u32_e32 v150, s46, v1
	s_add_i32 s70, 0, 0x1c000
	ds_read_b128 v[130:133], v150
	ds_read_b128 v[134:137], v150 offset:1024
	ds_read_b128 v[172:175], v150 offset:2048
	ds_read_b128 v[176:179], v150 offset:3072
	v_add_u32_e32 v150, s70, v1
	ds_read_b128 v[180:183], v150
	ds_read_b128 v[184:187], v150 offset:1024
	ds_read_b128 v[188:191], v150 offset:2048
	ds_read_b128 v[192:195], v150 offset:3072
	s_mov_b32 m0, s30
	v_lshl_add_u64 v[234:235], s[52:53], 0, v[146:147]
	ds_read_b128 v[196:199], v167 offset:32768
	ds_read_b128 v[200:203], v167 offset:33792
	ds_read_b128 v[204:207], v167 offset:34816
	ds_read_b128 v[208:211], v167 offset:35840
	ds_read_b128 v[212:215], v167 offset:36864
	ds_read_b128 v[216:219], v167 offset:37888
	ds_read_b128 v[220:223], v167 offset:38912
	ds_read_b128 v[224:227], v167 offset:39936
	global_load_lds_dwordx4 v[234:235], off
	v_lshl_add_u64 v[234:235], s[52:53], 0, v[148:149]
	s_mov_b32 m0, s31
	s_nop 0
	global_load_lds_dwordx4 v[234:235], off
	s_waitcnt vmcnt(8)
	s_waitcnt lgkmcnt(0)
	s_barrier
	s_setprio 1
	s_waitcnt lgkmcnt(0)
	v_mfma_f32_16x16x32_bf16 v[126:129], v[130:133], v[196:199], v[126:129]
	v_mfma_f32_16x16x32_bf16 v[122:125], v[172:175], v[196:199], v[122:125]
	v_mfma_f32_16x16x32_bf16 v[118:121], v[130:133], v[204:207], v[118:121]
	v_mfma_f32_16x16x32_bf16 v[110:113], v[172:175], v[204:207], v[110:113]
	v_mfma_f32_16x16x32_bf16 v[102:105], v[130:133], v[212:215], v[102:105]
	v_mfma_f32_16x16x32_bf16 v[94:97], v[172:175], v[212:215], v[94:97]
	v_mfma_f32_16x16x32_bf16 v[86:89], v[130:133], v[220:223], v[86:89]
	v_mfma_f32_16x16x32_bf16 v[78:81], v[172:175], v[220:223], v[78:81]
	v_mfma_f32_16x16x32_bf16 v[126:129], v[134:137], v[200:203], v[126:129]
	v_mfma_f32_16x16x32_bf16 v[122:125], v[176:179], v[200:203], v[122:125]
	v_mfma_f32_16x16x32_bf16 v[118:121], v[134:137], v[208:211], v[118:121]
	v_mfma_f32_16x16x32_bf16 v[110:113], v[176:179], v[208:211], v[110:113]
	v_mfma_f32_16x16x32_bf16 v[102:105], v[134:137], v[216:219], v[102:105]
	v_mfma_f32_16x16x32_bf16 v[94:97], v[176:179], v[216:219], v[94:97]
	v_mfma_f32_16x16x32_bf16 v[86:89], v[134:137], v[224:227], v[86:89]
	v_mfma_f32_16x16x32_bf16 v[78:81], v[176:179], v[224:227], v[78:81]
	v_mfma_f32_16x16x32_bf16 v[114:117], v[180:183], v[196:199], v[114:117]
	v_mfma_f32_16x16x32_bf16 v[106:109], v[188:191], v[196:199], v[106:109]
	v_mfma_f32_16x16x32_bf16 v[98:101], v[180:183], v[204:207], v[98:101]
	v_mfma_f32_16x16x32_bf16 v[90:93], v[188:191], v[204:207], v[90:93]
	v_mfma_f32_16x16x32_bf16 v[82:85], v[180:183], v[212:215], v[82:85]
	v_mfma_f32_16x16x32_bf16 v[74:77], v[188:191], v[212:215], v[74:77]
	v_mfma_f32_16x16x32_bf16 v[70:73], v[180:183], v[220:223], v[70:73]
	v_mfma_f32_16x16x32_bf16 v[66:69], v[188:191], v[220:223], v[66:69]
	v_mfma_f32_16x16x32_bf16 v[114:117], v[184:187], v[200:203], v[114:117]
	v_mfma_f32_16x16x32_bf16 v[106:109], v[192:195], v[200:203], v[106:109]
	v_mfma_f32_16x16x32_bf16 v[98:101], v[184:187], v[208:211], v[98:101]
	v_mfma_f32_16x16x32_bf16 v[90:93], v[192:195], v[208:211], v[90:93]
	v_mfma_f32_16x16x32_bf16 v[82:85], v[184:187], v[216:219], v[82:85]
	v_mfma_f32_16x16x32_bf16 v[74:77], v[192:195], v[216:219], v[74:77]
	v_mfma_f32_16x16x32_bf16 v[70:73], v[184:187], v[224:227], v[70:73]
	v_mfma_f32_16x16x32_bf16 v[66:69], v[192:195], v[224:227], v[66:69]
	s_setprio 0
	s_barrier
; #define FG_STAGE(bufoff, gbase, v0, v1) do { \
;         __builtin_amdgcn_global_load_lds((const unsigned*)((const char*)(gbase) + (v0)), (LAS unsigned*)(lds + (bufoff) + ldsw), 16, 0, 0); \
;         __builtin_amdgcn_global_load_lds((const unsigned*)((const char*)(gbase) + (v1)), (LAS unsigned*)(lds + (bufoff) + ldsw + 8192), 16, 0, 0); } while (0)
; #define FG_LDA(dst, b, h) do { _Pragma("unroll") for (int m = 0; m < 4; ++m) _Pragma("unroll") for (int k = 0; k < 2; ++k) dst[m][k] = *(const LAS bf16x8*)(lds + FG_SA(b, h) + aoff + m * 2048 + k * 1024); } while (0)
; #define FG_MMA(ai, bj, At, Bt) do { __builtin_amdgcn_s_setprio(1); _Pragma("unroll") for (int m = 0; m < 4; ++m) _Pragma("unroll") for (int n = 0; n < 2; ++n) _Pragma("unroll") for (int k = 0; k < 2; ++k) \
;         acc[ai][bj][m][n] = __builtin_amdgcn_mfma_f32_16x16x32_bf16(Bt[n][k], At[m][k], acc[ai][bj][m][n], 0, 0, 0); __builtin_amdgcn_s_setprio(0); } while (0)
; #define FG_WAIT_V(n) asm volatile("s_waitcnt vmcnt(" #n ")" ::: "memory")
; #define FG_WAIT_L(n) asm volatile("s_waitcnt lgkmcnt(" #n ")" ::: "memory")
; #define FG_BAR __builtin_amdgcn_s_barrier()
; #define FG_SCHED __builtin_amdgcn_sched_barrier(0)
; template <bool GATHER, class Unit, class Epi, class Sched>
; __device__ __forceinline__ void gemm_phase(LAS unsigned char* lds, const int K, const Sched& S, const Epi& E) {
;     ...
;             FG_LDA(At, 1, 1); FG_STAGE(FG_SB(1, 0), b3, voffB0, voffB1); FG_STAGE(FG_SB(1, 1), b3 + hstepB, voffB0, voffB1); FG_STAGE(FG_SA(1, 0), a3, x00, x01);
;             FG_WAIT_V(8); FG_WAIT_L(0); FG_BAR; if (hi_on) { FG_MMA(1, 0, At, B0); FG_MMA(1, 1, At, B1); } FG_BAR; FG_SCHED;
;         }
;         if (wr == 0) FG_BAR;
	s_add_i32 s46, s46, s27
	v_lshl_add_u64 v[164:165], v[164:165], 0, s[12:13]
	s_mov_b32 m0, s46
	ds_read_b128 v[196:199], v167 offset:49152
	ds_read_b128 v[200:203], v167 offset:50176
	ds_read_b128 v[204:207], v167 offset:51200
	ds_read_b128 v[208:211], v167 offset:52224
	ds_read_b128 v[212:215], v167 offset:53248
	ds_read_b128 v[216:219], v167 offset:54272
	ds_read_b128 v[220:223], v167 offset:55296
	ds_read_b128 v[224:227], v167 offset:56320
	global_load_lds_dwordx4 v[164:165], off
	s_add_i32 m0, s46, 0x2000
	s_add_u32 s46, s50, 0x80080
	v_lshl_add_u64 v[164:165], v[228:229], 0, s[12:13]
	s_addc_u32 s47, s51, 0
	s_add_i32 s50, s70, s27
	global_load_lds_dwordx4 v[164:165], off
	v_lshl_add_u64 v[164:165], s[46:47], 0, v[138:139]
	s_mov_b32 m0, s50
	s_nop 0
	global_load_lds_dwordx4 v[164:165], off
	v_lshl_add_u64 v[164:165], s[46:47], 0, v[140:141]
	s_add_i32 m0, s50, 0x2000
	s_nop 0
	global_load_lds_dwordx4 v[164:165], off
	v_lshl_add_u64 v[164:165], v[230:231], 0, s[12:13]
	s_mov_b32 m0, s55
	s_nop 0
	global_load_lds_dwordx4 v[164:165], off
	v_lshl_add_u64 v[164:165], v[232:233], 0, s[12:13]
	s_mov_b32 m0, s56
	s_nop 0
	global_load_lds_dwordx4 v[164:165], off
	s_waitcnt vmcnt(8)
	s_waitcnt lgkmcnt(0)
	s_barrier
	s_setprio 1
	s_waitcnt lgkmcnt(0)
	v_mfma_f32_16x16x32_bf16 v[62:65], v[130:133], v[196:199], v[62:65]
	v_mfma_f32_16x16x32_bf16 v[58:61], v[172:175], v[196:199], v[58:61]
	v_mfma_f32_16x16x32_bf16 v[54:57], v[130:133], v[204:207], v[54:57]
	v_mfma_f32_16x16x32_bf16 v[46:49], v[172:175], v[204:207], v[46:49]
	v_mfma_f32_16x16x32_bf16 v[38:41], v[130:133], v[212:215], v[38:41]
	v_mfma_f32_16x16x32_bf16 v[30:33], v[172:175], v[212:215], v[30:33]
	v_mfma_f32_16x16x32_bf16 v[22:25], v[130:133], v[220:223], v[22:25]
	v_mfma_f32_16x16x32_bf16 v[14:17], v[172:175], v[220:223], v[14:17]
	v_mfma_f32_16x16x32_bf16 v[62:65], v[134:137], v[200:203], v[62:65]
	v_mfma_f32_16x16x32_bf16 v[58:61], v[176:179], v[200:203], v[58:61]
	v_mfma_f32_16x16x32_bf16 v[54:57], v[134:137], v[208:211], v[54:57]
	v_mfma_f32_16x16x32_bf16 v[46:49], v[176:179], v[208:211], v[46:49]
	v_mfma_f32_16x16x32_bf16 v[38:41], v[134:137], v[216:219], v[38:41]
	v_mfma_f32_16x16x32_bf16 v[30:33], v[176:179], v[216:219], v[30:33]
	v_mfma_f32_16x16x32_bf16 v[22:25], v[134:137], v[224:227], v[22:25]
	v_mfma_f32_16x16x32_bf16 v[14:17], v[176:179], v[224:227], v[14:17]
	v_mfma_f32_16x16x32_bf16 v[50:53], v[180:183], v[196:199], v[50:53]
	v_mfma_f32_16x16x32_bf16 v[42:45], v[188:191], v[196:199], v[42:45]
	v_mfma_f32_16x16x32_bf16 v[34:37], v[180:183], v[204:207], v[34:37]
	v_mfma_f32_16x16x32_bf16 v[26:29], v[188:191], v[204:207], v[26:29]
	v_mfma_f32_16x16x32_bf16 v[18:21], v[180:183], v[212:215], v[18:21]
	v_mfma_f32_16x16x32_bf16 v[10:13], v[188:191], v[212:215], v[10:13]
	v_mfma_f32_16x16x32_bf16 v[6:9], v[180:183], v[220:223], v[6:9]
	v_mfma_f32_16x16x32_bf16 v[2:5], v[188:191], v[220:223], v[2:5]
	v_mfma_f32_16x16x32_bf16 v[50:53], v[184:187], v[200:203], v[50:53]
	v_mfma_f32_16x16x32_bf16 v[42:45], v[192:195], v[200:203], v[42:45]
	v_mfma_f32_16x16x32_bf16 v[34:37], v[184:187], v[208:211], v[34:37]
	v_mfma_f32_16x16x32_bf16 v[26:29], v[192:195], v[208:211], v[26:29]
	v_mfma_f32_16x16x32_bf16 v[18:21], v[184:187], v[216:219], v[18:21]
	v_mfma_f32_16x16x32_bf16 v[10:13], v[192:195], v[216:219], v[10:13]
	v_mfma_f32_16x16x32_bf16 v[6:9], v[184:187], v[224:227], v[6:9]
	v_mfma_f32_16x16x32_bf16 v[2:5], v[192:195], v[224:227], v[2:5]
	s_setprio 0
	s_barrier
	s_add_i32 s69, s69, 2
	s_add_u32 s67, s67, 0x100
	s_addc_u32 s68, s68, 0
	s_cmp_gt_u32 s69, 29
	s_mov_b64 s[46:47], s[48:49]
	s_cbranch_scc0 .LBB0_1239
	s_and_b64 vcc, exec, s[14:15]
	s_cbranch_vccz .LBB0_1242
	s_barrier

; #define FG_STAGE(bufoff, gbase, v0, v1) do { \
;         __builtin_amdgcn_global_load_lds((const unsigned*)((const char*)(gbase) + (v0)), (LAS unsigned*)(lds + (bufoff) + ldsw), 16, 0, 0); \
;         __builtin_amdgcn_global_load_lds((const unsigned*)((const char*)(gbase) + (v1)), (LAS unsigned*)(lds + (bufoff) + ldsw + 8192), 16, 0, 0); } while (0)
; #define FG_LDA(dst, b, h) do { _Pragma("unroll") for (int m = 0; m < 4; ++m) _Pragma("unroll") for (int k = 0; k < 2; ++k) dst[m][k] = *(const LAS bf16x8*)(lds + FG_SA(b, h) + aoff + m * 2048 + k * 1024); } while (0)
; #define FG_LDB(dst, b, h) do { _Pragma("unroll") for (int n = 0; n < 2; ++n) _Pragma("unroll") for (int k = 0; k < 2; ++k) dst[n][k] = *(const LAS bf16x8*)(lds + FG_SB(b, h) + boff + n * 2048 + k * 1024); } while (0)
; #define FG_MMA(ai, bj, At, Bt) do { __builtin_amdgcn_s_setprio(1); _Pragma("unroll") for (int m = 0; m < 4; ++m) _Pragma("unroll") for (int n = 0; n < 2; ++n) _Pragma("unroll") for (int k = 0; k < 2; ++k) \
;         acc[ai][bj][m][n] = __builtin_amdgcn_mfma_f32_16x16x32_bf16(Bt[n][k], At[m][k], acc[ai][bj][m][n], 0, 0, 0); __builtin_amdgcn_s_setprio(0); } while (0)
; template <bool GATHER, class Unit, class Epi, class Sched>
; __device__ __forceinline__ void gemm_phase(LAS unsigned char* lds, const int K, const Sched& S, const Epi& E) {
;     ...
;         for (int t = 0; t < nt; t += 2) {
;             const bool last = (t == nt - 2);
;             const char* a1 = cA + (size_t)(t + 1) * kstep;
;             const char* a2 = last ? nA : cA + (size_t)(t + 2) * kstep; const char* b2 = last ? nB : cB + (size_t)(t + 2) * kstep;
;             const char* a3 = a2 + kstep; const char* b3 = b2 + kstep;
;             const unsigned x00 = (GATHER && last) ? vN00 : vA00, x01 = (GATHER && last) ? vN01 : vA01, x10 = (GATHER && last) ? vN10 : vA10, x11 = (GATHER && last) ? vN11 : vA11;
;             FG_LDB(B0, 0, 0); FG_LDB(B1, 0, 1); FG_SCHED; FG_LDA(At, 0, 0); FG_STAGE(FG_SA(1, 1), a1, vA10, vA11);
;             FG_WAIT_V(8); FG_WAIT_L(0); FG_BAR; FG_MMA(0, 0, At, B0); FG_MMA(0, 1, At, B1); FG_BAR; FG_SCHED;
;             FG_LDA(At, 0, 1); FG_STAGE(FG_SB(0, 0), b2, voffB0, voffB1); FG_STAGE(FG_SB(0, 1), b2 + hstepB, voffB0, voffB1); FG_STAGE(FG_SA(0, 0), a2, x00, x01);
;             FG_WAIT_V(8); FG_WAIT_L(0); FG_BAR; if (hi_on) { FG_MMA(1, 0, At, B0); FG_MMA(1, 1, At, B1); } FG_BAR; FG_SCHED;
.LBB0_1289:
	ds_read_b128 v[86:89], v84
	ds_read_b128 v[90:93], v84 offset:1024
	ds_read_b128 v[94:97], v84 offset:2048
	ds_read_b128 v[98:101], v84 offset:3072
	s_add_u32 s46, s44, 0x80
	s_addc_u32 s47, s45, 0
	s_cmp_eq_u32 s65, 4
	s_cselect_b32 s49, s59, s47
	s_cselect_b32 s48, s60, s46
	s_cselect_b32 s47, s61, s64
	s_cselect_b32 s46, s62, s63
	v_lshl_add_u64 v[134:135], s[44:45], 0, v[82:83]
	s_add_i32 m0, s5, 0xc000
	ds_read_b128 v[102:105], v85
	ds_read_b128 v[106:109], v85 offset:1024
	ds_read_b128 v[110:113], v85 offset:2048
	ds_read_b128 v[114:117], v85 offset:3072
	ds_read_b128 v[118:121], v85 offset:4096
	ds_read_b128 v[122:125], v85 offset:5120
	ds_read_b128 v[126:129], v85 offset:6144
	ds_read_b128 v[130:133], v85 offset:7168
	global_load_lds_dwordx4 v[134:135], off
	v_lshl_add_u64 v[134:135], s[44:45], 0, v[80:81]
	s_add_i32 m0, s5, 0xe000
	s_nop 0
	global_load_lds_dwordx4 v[134:135], off
	s_waitcnt vmcnt(8)
	s_waitcnt lgkmcnt(0)
	s_barrier
	s_setprio 1
	s_waitcnt lgkmcnt(0)
	v_mfma_f32_16x16x32_bf16 v[62:65], v[86:89], v[102:105], v[62:65]
	v_mfma_f32_16x16x32_bf16 v[58:61], v[94:97], v[102:105], v[58:61]
	v_mfma_f32_16x16x32_bf16 v[54:57], v[86:89], v[110:113], v[54:57]
	v_mfma_f32_16x16x32_bf16 v[50:53], v[94:97], v[110:113], v[50:53]
	v_mfma_f32_16x16x32_bf16 v[46:49], v[86:89], v[118:121], v[46:49]
	v_mfma_f32_16x16x32_bf16 v[42:45], v[94:97], v[118:121], v[42:45]
	v_mfma_f32_16x16x32_bf16 v[38:41], v[86:89], v[126:129], v[38:41]
	v_mfma_f32_16x16x32_bf16 v[34:37], v[94:97], v[126:129], v[34:37]
	v_mfma_f32_16x16x32_bf16 v[62:65], v[90:93], v[106:109], v[62:65]
	v_mfma_f32_16x16x32_bf16 v[58:61], v[98:101], v[106:109], v[58:61]
	v_mfma_f32_16x16x32_bf16 v[54:57], v[90:93], v[114:117], v[54:57]
	v_mfma_f32_16x16x32_bf16 v[50:53], v[98:101], v[114:117], v[50:53]
	v_mfma_f32_16x16x32_bf16 v[46:49], v[90:93], v[122:125], v[46:49]
	v_mfma_f32_16x16x32_bf16 v[42:45], v[98:101], v[122:125], v[42:45]
	v_mfma_f32_16x16x32_bf16 v[38:41], v[90:93], v[130:133], v[38:41]
	v_mfma_f32_16x16x32_bf16 v[34:37], v[98:101], v[130:133], v[34:37]
	s_setprio 0
	s_barrier
	s_add_i32 s66, s57, s26
	v_lshl_add_u64 v[134:135], s[46:47], 0, v[68:69]
	s_mov_b32 m0, s66
	ds_read_b128 v[102:105], v85 offset:16384
	ds_read_b128 v[106:109], v85 offset:17408
	ds_read_b128 v[110:113], v85 offset:18432
	ds_read_b128 v[114:117], v85 offset:19456
	ds_read_b128 v[118:121], v85 offset:20480
	ds_read_b128 v[122:125], v85 offset:21504
	ds_read_b128 v[126:129], v85 offset:22528
	ds_read_b128 v[130:133], v85 offset:23552
	global_load_lds_dwordx4 v[134:135], off
	s_add_i32 m0, s66, 0x2000
	s_add_u32 s66, s46, 0x20000
	v_lshl_add_u64 v[136:137], s[46:47], 0, v[66:67]
	s_addc_u32 s67, s47, 0
	global_load_lds_dwordx4 v[136:137], off
	v_lshl_add_u64 v[138:139], s[66:67], 0, v[68:69]
	s_mov_b32 m0, s28
	v_lshl_add_u64 v[140:141], s[48:49], 0, v[72:73]
	global_load_lds_dwordx4 v[138:139], off
	v_lshl_add_u64 v[138:139], s[66:67], 0, v[66:67]
	s_mov_b32 m0, s29
	s_nop 0
	global_load_lds_dwordx4 v[138:139], off
	v_lshl_add_u64 v[138:139], s[48:49], 0, v[70:71]
	s_mov_b32 m0, s5
	s_nop 0
	global_load_lds_dwordx4 v[138:139], off
	s_mov_b32 m0, s30
	s_nop 0
	global_load_lds_dwordx4 v[140:141], off
	s_waitcnt vmcnt(8)
	s_waitcnt lgkmcnt(0)
	s_barrier
	s_setprio 1
	s_waitcnt lgkmcnt(0)
	v_mfma_f32_16x16x32_bf16 v[30:33], v[86:89], v[102:105], v[30:33]
	v_mfma_f32_16x16x32_bf16 v[26:29], v[94:97], v[102:105], v[26:29]
	v_mfma_f32_16x16x32_bf16 v[22:25], v[86:89], v[110:113], v[22:25]
	v_mfma_f32_16x16x32_bf16 v[18:21], v[94:97], v[110:113], v[18:21]
	v_mfma_f32_16x16x32_bf16 v[14:17], v[86:89], v[118:121], v[14:17]
	v_mfma_f32_16x16x32_bf16 v[10:13], v[94:97], v[118:121], v[10:13]
	v_mfma_f32_16x16x32_bf16 v[6:9], v[86:89], v[126:129], v[6:9]
	v_mfma_f32_16x16x32_bf16 v[2:5], v[94:97], v[126:129], v[2:5]
	v_mfma_f32_16x16x32_bf16 v[30:33], v[90:93], v[106:109], v[30:33]
	v_mfma_f32_16x16x32_bf16 v[26:29], v[98:101], v[106:109], v[26:29]
	v_mfma_f32_16x16x32_bf16 v[22:25], v[90:93], v[114:117], v[22:25]
	v_mfma_f32_16x16x32_bf16 v[18:21], v[98:101], v[114:117], v[18:21]
	v_mfma_f32_16x16x32_bf16 v[14:17], v[90:93], v[122:125], v[14:17]
	v_mfma_f32_16x16x32_bf16 v[10:13], v[98:101], v[122:125], v[10:13]
	v_mfma_f32_16x16x32_bf16 v[6:9], v[90:93], v[130:133], v[6:9]
	v_mfma_f32_16x16x32_bf16 v[2:5], v[98:101], v[130:133], v[2:5]
	s_setprio 0
	s_barrier
; #define FG_STAGE(bufoff, gbase, v0, v1) do { \
;         __builtin_amdgcn_global_load_lds((const unsigned*)((const char*)(gbase) + (v0)), (LAS unsigned*)(lds + (bufoff) + ldsw), 16, 0, 0); \
;         __builtin_amdgcn_global_load_lds((const unsigned*)((const char*)(gbase) + (v1)), (LAS unsigned*)(lds + (bufoff) + ldsw + 8192), 16, 0, 0); } while (0)
; #define FG_LDA(dst, b, h) do { _Pragma("unroll") for (int m = 0; m < 4; ++m) _Pragma("unroll") for (int k = 0; k < 2; ++k) dst[m][k] = *(const LAS bf16x8*)(lds + FG_SA(b, h) + aoff + m * 2048 + k * 1024); } while (0)
; #define FG_LDB(dst, b, h) do { _Pragma("unroll") for (int n = 0; n < 2; ++n) _Pragma("unroll") for (int k = 0; k < 2; ++k) dst[n][k] = *(const LAS bf16x8*)(lds + FG_SB(b, h) + boff + n * 2048 + k * 1024); } while (0)
; #define FG_MMA(ai, bj, At, Bt) do { __builtin_amdgcn_s_setprio(1); _Pragma("unroll") for (int m = 0; m < 4; ++m) _Pragma("unroll") for (int n = 0; n < 2; ++n) _Pragma("unroll") for (int k = 0; k < 2; ++k) \
;         acc[ai][bj][m][n] = __builtin_amdgcn_mfma_f32_16x16x32_bf16(Bt[n][k], At[m][k], acc[ai][bj][m][n], 0, 0, 0); __builtin_amdgcn_s_setprio(0); } while (0)
; #define FG_WAIT_V(n) asm volatile("s_waitcnt vmcnt(" #n ")" ::: "memory")
; #define FG_WAIT_L(n) asm volatile("s_waitcnt lgkmcnt(" #n ")" ::: "memory")
; #define FG_BAR __builtin_amdgcn_s_barrier()
; #define FG_SCHED __builtin_amdgcn_sched_barrier(0)
; template <bool GATHER, class Unit, class Epi, class Sched>
; __device__ __forceinline__ void gemm_phase(LAS unsigned char* lds, const int K, const Sched& S, const Epi& E) {
;     ...
;             FG_LDB(B0, 1, 0); FG_LDB(B1, 1, 1); FG_SCHED; FG_LDA(At, 1, 0); FG_STAGE(FG_SA(0, 1), a2, x10, x11);
;             FG_WAIT_V(8); FG_WAIT_L(0); FG_BAR; FG_MMA(0, 0, At, B0); FG_MMA(0, 1, At, B1); FG_BAR; FG_SCHED;
;             FG_LDA(At, 1, 1); FG_STAGE(FG_SB(1, 0), b3, voffB0, voffB1); FG_STAGE(FG_SB(1, 1), b3 + hstepB, voffB0, voffB1); FG_STAGE(FG_SA(1, 0), a3, x00, x01);
;             FG_WAIT_V(8); FG_WAIT_L(0); FG_BAR; if (hi_on) { FG_MMA(1, 0, At, B0); FG_MMA(1, 1, At, B1); } FG_BAR; FG_SCHED;
;         }
;         if (wr == 0) FG_BAR;
	s_add_i32 s66, 0, 0x18000
	v_add_u32_e32 v78, s66, v1
	ds_read_b128 v[86:89], v78
	ds_read_b128 v[90:93], v78 offset:1024
	ds_read_b128 v[94:97], v78 offset:2048
	ds_read_b128 v[98:101], v78 offset:3072
	s_mov_b32 m0, s31
	v_lshl_add_u64 v[142:143], s[48:49], 0, v[74:75]
	ds_read_b128 v[102:105], v85 offset:32768
	ds_read_b128 v[106:109], v85 offset:33792
	ds_read_b128 v[110:113], v85 offset:34816
	ds_read_b128 v[114:117], v85 offset:35840
	ds_read_b128 v[118:121], v85 offset:36864
	ds_read_b128 v[122:125], v85 offset:37888
	ds_read_b128 v[126:129], v85 offset:38912
	ds_read_b128 v[130:133], v85 offset:39936
	global_load_lds_dwordx4 v[142:143], off
	v_lshl_add_u64 v[142:143], s[48:49], 0, v[76:77]
	s_mov_b32 m0, s33
	s_nop 0
	global_load_lds_dwordx4 v[142:143], off
	s_waitcnt vmcnt(8)
	s_waitcnt lgkmcnt(0)
	s_barrier
	s_setprio 1
	s_waitcnt lgkmcnt(0)
	v_mfma_f32_16x16x32_bf16 v[62:65], v[86:89], v[102:105], v[62:65]
	v_mfma_f32_16x16x32_bf16 v[58:61], v[94:97], v[102:105], v[58:61]
	v_mfma_f32_16x16x32_bf16 v[54:57], v[86:89], v[110:113], v[54:57]
	v_mfma_f32_16x16x32_bf16 v[50:53], v[94:97], v[110:113], v[50:53]
	v_mfma_f32_16x16x32_bf16 v[46:49], v[86:89], v[118:121], v[46:49]
	v_mfma_f32_16x16x32_bf16 v[42:45], v[94:97], v[118:121], v[42:45]
	v_mfma_f32_16x16x32_bf16 v[38:41], v[86:89], v[126:129], v[38:41]
	v_mfma_f32_16x16x32_bf16 v[34:37], v[94:97], v[126:129], v[34:37]
	v_mfma_f32_16x16x32_bf16 v[62:65], v[90:93], v[106:109], v[62:65]
	v_mfma_f32_16x16x32_bf16 v[58:61], v[98:101], v[106:109], v[58:61]
	v_mfma_f32_16x16x32_bf16 v[54:57], v[90:93], v[114:117], v[54:57]
	v_mfma_f32_16x16x32_bf16 v[50:53], v[98:101], v[114:117], v[50:53]
	v_mfma_f32_16x16x32_bf16 v[46:49], v[90:93], v[122:125], v[46:49]
	v_mfma_f32_16x16x32_bf16 v[42:45], v[98:101], v[122:125], v[42:45]
	v_mfma_f32_16x16x32_bf16 v[38:41], v[90:93], v[130:133], v[38:41]
	v_mfma_f32_16x16x32_bf16 v[34:37], v[98:101], v[130:133], v[34:37]
	s_setprio 0
	s_barrier
	s_add_i32 s48, s66, s26
	v_lshl_add_u64 v[134:135], v[134:135], 0, s[6:7]
	s_mov_b32 m0, s48
	ds_read_b128 v[102:105], v85 offset:49152
	ds_read_b128 v[106:109], v85 offset:50176
	ds_read_b128 v[110:113], v85 offset:51200
	ds_read_b128 v[114:117], v85 offset:52224
	ds_read_b128 v[118:121], v85 offset:53248
	ds_read_b128 v[122:125], v85 offset:54272
	ds_read_b128 v[126:129], v85 offset:55296
	ds_read_b128 v[130:133], v85 offset:56320
	global_load_lds_dwordx4 v[134:135], off
	s_add_i32 m0, s48, 0x2000
	s_add_u32 s46, s46, 0x20080
	v_lshl_add_u64 v[134:135], v[136:137], 0, s[6:7]
	s_addc_u32 s47, s47, 0
	global_load_lds_dwordx4 v[134:135], off
	v_lshl_add_u64 v[134:135], s[46:47], 0, v[68:69]
	s_mov_b32 m0, s55
	s_nop 0
	global_load_lds_dwordx4 v[134:135], off
	v_lshl_add_u64 v[134:135], s[46:47], 0, v[66:67]
	s_mov_b32 m0, s56
	s_nop 0
	global_load_lds_dwordx4 v[134:135], off
	v_lshl_add_u64 v[134:135], v[138:139], 0, s[6:7]
	s_mov_b32 m0, s53
	s_nop 0
	global_load_lds_dwordx4 v[134:135], off
	v_lshl_add_u64 v[134:135], v[140:141], 0, s[6:7]
	s_mov_b32 m0, s54
	s_nop 0
	global_load_lds_dwordx4 v[134:135], off
	s_waitcnt vmcnt(8)
	s_waitcnt lgkmcnt(0)
	s_barrier
	s_setprio 1
	s_waitcnt lgkmcnt(0)
	v_mfma_f32_16x16x32_bf16 v[30:33], v[86:89], v[102:105], v[30:33]
	v_mfma_f32_16x16x32_bf16 v[26:29], v[94:97], v[102:105], v[26:29]
	v_mfma_f32_16x16x32_bf16 v[22:25], v[86:89], v[110:113], v[22:25]
	v_mfma_f32_16x16x32_bf16 v[18:21], v[94:97], v[110:113], v[18:21]
	v_mfma_f32_16x16x32_bf16 v[14:17], v[86:89], v[118:121], v[14:17]
	v_mfma_f32_16x16x32_bf16 v[10:13], v[94:97], v[118:121], v[10:13]
	v_mfma_f32_16x16x32_bf16 v[6:9], v[86:89], v[126:129], v[6:9]
	v_mfma_f32_16x16x32_bf16 v[2:5], v[94:97], v[126:129], v[2:5]
	v_mfma_f32_16x16x32_bf16 v[30:33], v[90:93], v[106:109], v[30:33]
	v_mfma_f32_16x16x32_bf16 v[26:29], v[98:101], v[106:109], v[26:29]
	v_mfma_f32_16x16x32_bf16 v[22:25], v[90:93], v[114:117], v[22:25]
	v_mfma_f32_16x16x32_bf16 v[18:21], v[98:101], v[114:117], v[18:21]
	v_mfma_f32_16x16x32_bf16 v[14:17], v[90:93], v[122:125], v[14:17]
	v_mfma_f32_16x16x32_bf16 v[10:13], v[98:101], v[122:125], v[10:13]
	v_mfma_f32_16x16x32_bf16 v[6:9], v[90:93], v[130:133], v[6:9]
	v_mfma_f32_16x16x32_bf16 v[2:5], v[98:101], v[130:133], v[2:5]
	s_setprio 0
	s_barrier
	s_add_i32 s65, s65, 2
	s_add_u32 s63, s63, 0x100
	s_addc_u32 s64, s64, 0
	s_add_u32 s44, s44, 0x100
	s_addc_u32 s45, s45, 0
	s_cmp_gt_u32 s65, 5
	s_cbranch_scc0 .LBB0_1289
	s_and_b64 vcc, exec, s[16:17]
	s_cbranch_vccz .LBB0_1292
	s_barrier

; #define FG_STAGE(bufoff, gbase, v0, v1) do { \
;         __builtin_amdgcn_global_load_lds((const unsigned*)((const char*)(gbase) + (v0)), (LAS unsigned*)(lds + (bufoff) + ldsw), 16, 0, 0); \
;         __builtin_amdgcn_global_load_lds((const unsigned*)((const char*)(gbase) + (v1)), (LAS unsigned*)(lds + (bufoff) + ldsw + 8192), 16, 0, 0); } while (0)
; #define FG_LDA(dst, b, h) do { _Pragma("unroll") for (int m = 0; m < 4; ++m) _Pragma("unroll") for (int k = 0; k < 2; ++k) dst[m][k] = *(const LAS bf16x8*)(lds + FG_SA(b, h) + aoff + m * 2048 + k * 1024); } while (0)
; #define FG_LDB(dst, b, h) do { _Pragma("unroll") for (int n = 0; n < 2; ++n) _Pragma("unroll") for (int k = 0; k < 2; ++k) dst[n][k] = *(const LAS bf16x8*)(lds + FG_SB(b, h) + boff + n * 2048 + k * 1024); } while (0)
; #define FG_MMA(ai, bj, At, Bt) do { __builtin_amdgcn_s_setprio(1); _Pragma("unroll") for (int m = 0; m < 4; ++m) _Pragma("unroll") for (int n = 0; n < 2; ++n) _Pragma("unroll") for (int k = 0; k < 2; ++k) \
;         acc[ai][bj][m][n] = __builtin_amdgcn_mfma_f32_16x16x32_bf16(Bt[n][k], At[m][k], acc[ai][bj][m][n], 0, 0, 0); __builtin_amdgcn_s_setprio(0); } while (0)
; template <bool GATHER, class Unit, class Epi, class Sched>
; __device__ __forceinline__ void gemm_phase(LAS unsigned char* lds, const int K, const Sched& S, const Epi& E) {
;     ...
;         for (int t = 0; t < nt; t += 2) {
;             const bool last = (t == nt - 2);
;             const char* a1 = cA + (size_t)(t + 1) * kstep;
;             const char* a2 = last ? nA : cA + (size_t)(t + 2) * kstep; const char* b2 = last ? nB : cB + (size_t)(t + 2) * kstep;
;             const char* a3 = a2 + kstep; const char* b3 = b2 + kstep;
;             const unsigned x00 = (GATHER && last) ? vN00 : vA00, x01 = (GATHER && last) ? vN01 : vA01, x10 = (GATHER && last) ? vN10 : vA10, x11 = (GATHER && last) ? vN11 : vA11;
;             FG_LDB(B0, 0, 0); FG_LDB(B1, 0, 1); FG_SCHED; FG_LDA(At, 0, 0); FG_STAGE(FG_SA(1, 1), a1, vA10, vA11);
;             FG_WAIT_V(8); FG_WAIT_L(0); FG_BAR; FG_MMA(0, 0, At, B0); FG_MMA(0, 1, At, B1); FG_BAR; FG_SCHED;
;             FG_LDA(At, 0, 1); FG_STAGE(FG_SB(0, 0), b2, voffB0, voffB1); FG_STAGE(FG_SB(0, 1), b2 + hstepB, voffB0, voffB1); FG_STAGE(FG_SA(0, 0), a2, x00, x01);
;             FG_WAIT_V(8); FG_WAIT_L(0); FG_BAR; if (hi_on) { FG_MMA(1, 0, At, B0); FG_MMA(1, 1, At, B1); } FG_BAR; FG_SCHED;
.LBB0_1546:
	ds_read_b128 v[66:69], v210
	ds_read_b128 v[70:73], v210 offset:1024
	ds_read_b128 v[74:77], v210 offset:2048
	ds_read_b128 v[78:81], v210 offset:3072
	ds_read_b128 v[146:149], v211
	ds_read_b128 v[150:153], v211 offset:1024
	ds_read_b128 v[154:157], v211 offset:2048
	ds_read_b128 v[158:161], v211 offset:3072
	s_add_u32 s42, s38, 0x100
	s_addc_u32 s43, s39, 0
	s_cmp_eq_u32 s58, 28
	s_cselect_b32 s47, s7, s43
	s_cselect_b32 s46, s25, s42
	s_cselect_b32 s45, s21, s57
	s_cselect_b32 s44, s41, s56
	v_lshl_add_u64 v[208:209], s[38:39], 0, v[186:187]
	s_add_i32 m0, s28, 0xc000
	ds_read_b128 v[162:165], v212
	ds_read_b128 v[166:169], v212 offset:1024
	ds_read_b128 v[192:195], v212 offset:2048
	ds_read_b128 v[196:199], v212 offset:3072
	ds_read_b128 v[200:203], v212 offset:4096
	ds_read_b128 v[204:207], v212 offset:5120
	ds_read_b128 v[214:217], v212 offset:6144
	ds_read_b128 v[218:221], v212 offset:7168
	global_load_lds_dwordx4 v[208:209], off
	v_lshl_add_u64 v[208:209], s[38:39], 0, v[184:185]
	s_add_i32 m0, s28, 0xe000
	s_nop 0
	global_load_lds_dwordx4 v[208:209], off
	s_waitcnt vmcnt(8)
	s_waitcnt lgkmcnt(0)
	s_barrier
	s_setprio 1
	s_waitcnt lgkmcnt(0)
	v_mfma_f32_16x16x32_bf16 v[142:145], v[66:69], v[162:165], v[142:145]
	v_mfma_f32_16x16x32_bf16 v[138:141], v[74:77], v[162:165], v[138:141]
	v_mfma_f32_16x16x32_bf16 v[126:129], v[66:69], v[192:195], v[126:129]
	v_mfma_f32_16x16x32_bf16 v[122:125], v[74:77], v[192:195], v[122:125]
	v_mfma_f32_16x16x32_bf16 v[110:113], v[66:69], v[200:203], v[110:113]
	v_mfma_f32_16x16x32_bf16 v[106:109], v[74:77], v[200:203], v[106:109]
	v_mfma_f32_16x16x32_bf16 v[94:97], v[66:69], v[214:217], v[94:97]
	v_mfma_f32_16x16x32_bf16 v[90:93], v[74:77], v[214:217], v[90:93]
	v_mfma_f32_16x16x32_bf16 v[142:145], v[70:73], v[166:169], v[142:145]
	v_mfma_f32_16x16x32_bf16 v[138:141], v[78:81], v[166:169], v[138:141]
	v_mfma_f32_16x16x32_bf16 v[126:129], v[70:73], v[196:199], v[126:129]
	v_mfma_f32_16x16x32_bf16 v[122:125], v[78:81], v[196:199], v[122:125]
	v_mfma_f32_16x16x32_bf16 v[110:113], v[70:73], v[204:207], v[110:113]
	v_mfma_f32_16x16x32_bf16 v[106:109], v[78:81], v[204:207], v[106:109]
	v_mfma_f32_16x16x32_bf16 v[94:97], v[70:73], v[218:221], v[94:97]
	v_mfma_f32_16x16x32_bf16 v[90:93], v[78:81], v[218:221], v[90:93]
	v_mfma_f32_16x16x32_bf16 v[134:137], v[146:149], v[162:165], v[134:137]
	v_mfma_f32_16x16x32_bf16 v[130:133], v[154:157], v[162:165], v[130:133]
	v_mfma_f32_16x16x32_bf16 v[118:121], v[146:149], v[192:195], v[118:121]
	v_mfma_f32_16x16x32_bf16 v[114:117], v[154:157], v[192:195], v[114:117]
	v_mfma_f32_16x16x32_bf16 v[102:105], v[146:149], v[200:203], v[102:105]
	v_mfma_f32_16x16x32_bf16 v[98:101], v[154:157], v[200:203], v[98:101]
	v_mfma_f32_16x16x32_bf16 v[86:89], v[146:149], v[214:217], v[86:89]
	v_mfma_f32_16x16x32_bf16 v[82:85], v[154:157], v[214:217], v[82:85]
	v_mfma_f32_16x16x32_bf16 v[134:137], v[150:153], v[166:169], v[134:137]
	v_mfma_f32_16x16x32_bf16 v[130:133], v[158:161], v[166:169], v[130:133]
	v_mfma_f32_16x16x32_bf16 v[118:121], v[150:153], v[196:199], v[118:121]
	v_mfma_f32_16x16x32_bf16 v[114:117], v[158:161], v[196:199], v[114:117]
	v_mfma_f32_16x16x32_bf16 v[102:105], v[150:153], v[204:207], v[102:105]
	v_mfma_f32_16x16x32_bf16 v[98:101], v[158:161], v[204:207], v[98:101]
	v_mfma_f32_16x16x32_bf16 v[86:89], v[150:153], v[218:221], v[86:89]
	v_mfma_f32_16x16x32_bf16 v[82:85], v[158:161], v[218:221], v[82:85]
	s_setprio 0
	s_barrier
	s_add_i32 s38, s54, s27
	v_lshl_add_u64 v[208:209], s[44:45], 0, v[170:171]
	s_mov_b32 m0, s38
	ds_read_b128 v[162:165], v212 offset:16384
	ds_read_b128 v[166:169], v212 offset:17408
	ds_read_b128 v[192:195], v212 offset:18432
	ds_read_b128 v[196:199], v212 offset:19456
	ds_read_b128 v[200:203], v212 offset:20480
	ds_read_b128 v[204:207], v212 offset:21504
	ds_read_b128 v[214:217], v212 offset:22528
	ds_read_b128 v[218:221], v212 offset:23552
	global_load_lds_dwordx4 v[208:209], off
	s_add_i32 m0, s38, 0x2000
	s_add_u32 s38, s44, 0x80000
	v_lshl_add_u64 v[222:223], s[44:45], 0, v[172:173]
	s_addc_u32 s39, s45, 0
	s_add_i32 s59, s55, s27
	global_load_lds_dwordx4 v[222:223], off
	v_lshl_add_u64 v[224:225], s[38:39], 0, v[170:171]
	s_mov_b32 m0, s59
	v_lshl_add_u64 v[226:227], s[46:47], 0, v[176:177]
	global_load_lds_dwordx4 v[224:225], off
	v_lshl_add_u64 v[224:225], s[38:39], 0, v[172:173]
	s_add_i32 m0, s59, 0x2000
	s_nop 0
	global_load_lds_dwordx4 v[224:225], off
	v_lshl_add_u64 v[224:225], s[46:47], 0, v[174:175]
	s_mov_b32 m0, s28
	s_nop 0
	global_load_lds_dwordx4 v[224:225], off
	s_mov_b32 m0, s29
	s_nop 0
	global_load_lds_dwordx4 v[226:227], off
	s_waitcnt vmcnt(8)
	s_waitcnt lgkmcnt(0)
	s_barrier
; #define FG_STAGE(bufoff, gbase, v0, v1) do { \
;         __builtin_amdgcn_global_load_lds((const unsigned*)((const char*)(gbase) + (v0)), (LAS unsigned*)(lds + (bufoff) + ldsw), 16, 0, 0); \
;         __builtin_amdgcn_global_load_lds((const unsigned*)((const char*)(gbase) + (v1)), (LAS unsigned*)(lds + (bufoff) + ldsw + 8192), 16, 0, 0); } while (0)
; #define FG_LDA(dst, b, h) do { _Pragma("unroll") for (int m = 0; m < 4; ++m) _Pragma("unroll") for (int k = 0; k < 2; ++k) dst[m][k] = *(const LAS bf16x8*)(lds + FG_SA(b, h) + aoff + m * 2048 + k * 1024); } while (0)
; #define FG_LDB(dst, b, h) do { _Pragma("unroll") for (int n = 0; n < 2; ++n) _Pragma("unroll") for (int k = 0; k < 2; ++k) dst[n][k] = *(const LAS bf16x8*)(lds + FG_SB(b, h) + boff + n * 2048 + k * 1024); } while (0)
; #define FG_MMA(ai, bj, At, Bt) do { __builtin_amdgcn_s_setprio(1); _Pragma("unroll") for (int m = 0; m < 4; ++m) _Pragma("unroll") for (int n = 0; n < 2; ++n) _Pragma("unroll") for (int k = 0; k < 2; ++k) \
;         acc[ai][bj][m][n] = __builtin_amdgcn_mfma_f32_16x16x32_bf16(Bt[n][k], At[m][k], acc[ai][bj][m][n], 0, 0, 0); __builtin_amdgcn_s_setprio(0); } while (0)
; #define FG_WAIT_V(n) asm volatile("s_waitcnt vmcnt(" #n ")" ::: "memory")
; #define FG_WAIT_L(n) asm volatile("s_waitcnt lgkmcnt(" #n ")" ::: "memory")
; #define FG_BAR __builtin_amdgcn_s_barrier()
; #define FG_SCHED __builtin_amdgcn_sched_barrier(0)
; template <bool GATHER, class Unit, class Epi, class Sched>
; __device__ __forceinline__ void gemm_phase(LAS unsigned char* lds, const int K, const Sched& S, const Epi& E) {
;     ...
;             FG_WAIT_V(8); FG_WAIT_L(0); FG_BAR; if (hi_on) { FG_MMA(1, 0, At, B0); FG_MMA(1, 1, At, B1); } FG_BAR; FG_SCHED;
;             FG_LDB(B0, 1, 0); FG_LDB(B1, 1, 1); FG_SCHED; FG_LDA(At, 1, 0); FG_STAGE(FG_SA(0, 1), a2, x10, x11);
;             FG_WAIT_V(8); FG_WAIT_L(0); FG_BAR; FG_MMA(0, 0, At, B0); FG_MMA(0, 1, At, B1); FG_BAR; FG_SCHED;
	s_setprio 1
	s_waitcnt lgkmcnt(0)
	v_mfma_f32_16x16x32_bf16 v[62:65], v[66:69], v[162:165], v[62:65]
	v_mfma_f32_16x16x32_bf16 v[58:61], v[74:77], v[162:165], v[58:61]
	v_mfma_f32_16x16x32_bf16 v[46:49], v[66:69], v[192:195], v[46:49]
	v_mfma_f32_16x16x32_bf16 v[42:45], v[74:77], v[192:195], v[42:45]
	v_mfma_f32_16x16x32_bf16 v[30:33], v[66:69], v[200:203], v[30:33]
	v_mfma_f32_16x16x32_bf16 v[26:29], v[74:77], v[200:203], v[26:29]
	v_mfma_f32_16x16x32_bf16 v[14:17], v[66:69], v[214:217], v[14:17]
	v_mfma_f32_16x16x32_bf16 v[10:13], v[74:77], v[214:217], v[10:13]
	v_mfma_f32_16x16x32_bf16 v[62:65], v[70:73], v[166:169], v[62:65]
	v_mfma_f32_16x16x32_bf16 v[58:61], v[78:81], v[166:169], v[58:61]
	v_mfma_f32_16x16x32_bf16 v[46:49], v[70:73], v[196:199], v[46:49]
	v_mfma_f32_16x16x32_bf16 v[42:45], v[78:81], v[196:199], v[42:45]
	v_mfma_f32_16x16x32_bf16 v[30:33], v[70:73], v[204:207], v[30:33]
	v_mfma_f32_16x16x32_bf16 v[26:29], v[78:81], v[204:207], v[26:29]
	v_mfma_f32_16x16x32_bf16 v[14:17], v[70:73], v[218:221], v[14:17]
	v_mfma_f32_16x16x32_bf16 v[10:13], v[78:81], v[218:221], v[10:13]
	v_mfma_f32_16x16x32_bf16 v[54:57], v[146:149], v[162:165], v[54:57]
	v_mfma_f32_16x16x32_bf16 v[50:53], v[154:157], v[162:165], v[50:53]
	v_mfma_f32_16x16x32_bf16 v[38:41], v[146:149], v[192:195], v[38:41]
	v_mfma_f32_16x16x32_bf16 v[34:37], v[154:157], v[192:195], v[34:37]
	v_mfma_f32_16x16x32_bf16 v[22:25], v[146:149], v[200:203], v[22:25]
	v_mfma_f32_16x16x32_bf16 v[18:21], v[154:157], v[200:203], v[18:21]
	v_mfma_f32_16x16x32_bf16 v[6:9], v[146:149], v[214:217], v[6:9]
	v_mfma_f32_16x16x32_bf16 v[2:5], v[154:157], v[214:217], v[2:5]
	v_mfma_f32_16x16x32_bf16 v[54:57], v[150:153], v[166:169], v[54:57]
	v_mfma_f32_16x16x32_bf16 v[50:53], v[158:161], v[166:169], v[50:53]
	v_mfma_f32_16x16x32_bf16 v[38:41], v[150:153], v[196:199], v[38:41]
	v_mfma_f32_16x16x32_bf16 v[34:37], v[158:161], v[196:199], v[34:37]
	v_mfma_f32_16x16x32_bf16 v[22:25], v[150:153], v[204:207], v[22:25]
	v_mfma_f32_16x16x32_bf16 v[18:21], v[158:161], v[204:207], v[18:21]
	v_mfma_f32_16x16x32_bf16 v[6:9], v[150:153], v[218:221], v[6:9]
	v_mfma_f32_16x16x32_bf16 v[2:5], v[158:161], v[218:221], v[2:5]
	s_setprio 0
	s_barrier
	s_add_i32 s38, 0, 0x18000
	s_add_i32 s59, 0, 0x1c000
	v_add_u32_e32 v78, s38, v1
	v_add_u32_e32 v158, s59, v1
	ds_read_b128 v[66:69], v78
	ds_read_b128 v[70:73], v78 offset:1024
	ds_read_b128 v[74:77], v78 offset:2048
	ds_read_b128 v[78:81], v78 offset:3072
	ds_read_b128 v[146:149], v158
	ds_read_b128 v[150:153], v158 offset:1024
	ds_read_b128 v[154:157], v158 offset:2048
	ds_read_b128 v[158:161], v158 offset:3072
	s_mov_b32 m0, s30
	v_lshl_add_u64 v[228:229], s[46:47], 0, v[178:179]
	ds_read_b128 v[162:165], v212 offset:32768
	ds_read_b128 v[166:169], v212 offset:33792
	ds_read_b128 v[192:195], v212 offset:34816
	ds_read_b128 v[196:199], v212 offset:35840
	ds_read_b128 v[200:203], v212 offset:36864
	ds_read_b128 v[204:207], v212 offset:37888
	ds_read_b128 v[214:217], v212 offset:38912
	ds_read_b128 v[218:221], v212 offset:39936
	global_load_lds_dwordx4 v[228:229], off
	v_lshl_add_u64 v[228:229], s[46:47], 0, v[180:181]
	s_mov_b32 m0, s31
	s_nop 0
	global_load_lds_dwordx4 v[228:229], off
	s_waitcnt vmcnt(8)
	s_waitcnt lgkmcnt(0)
	s_barrier
	s_setprio 1
	s_waitcnt lgkmcnt(0)
	v_mfma_f32_16x16x32_bf16 v[142:145], v[66:69], v[162:165], v[142:145]
	v_mfma_f32_16x16x32_bf16 v[138:141], v[74:77], v[162:165], v[138:141]
	v_mfma_f32_16x16x32_bf16 v[126:129], v[66:69], v[192:195], v[126:129]
	v_mfma_f32_16x16x32_bf16 v[122:125], v[74:77], v[192:195], v[122:125]
	v_mfma_f32_16x16x32_bf16 v[110:113], v[66:69], v[200:203], v[110:113]
	v_mfma_f32_16x16x32_bf16 v[106:109], v[74:77], v[200:203], v[106:109]
	v_mfma_f32_16x16x32_bf16 v[94:97], v[66:69], v[214:217], v[94:97]
	v_mfma_f32_16x16x32_bf16 v[90:93], v[74:77], v[214:217], v[90:93]
	v_mfma_f32_16x16x32_bf16 v[142:145], v[70:73], v[166:169], v[142:145]
	v_mfma_f32_16x16x32_bf16 v[138:141], v[78:81], v[166:169], v[138:141]
	v_mfma_f32_16x16x32_bf16 v[126:129], v[70:73], v[196:199], v[126:129]
	v_mfma_f32_16x16x32_bf16 v[122:125], v[78:81], v[196:199], v[122:125]
	v_mfma_f32_16x16x32_bf16 v[110:113], v[70:73], v[204:207], v[110:113]
	v_mfma_f32_16x16x32_bf16 v[106:109], v[78:81], v[204:207], v[106:109]
	v_mfma_f32_16x16x32_bf16 v[94:97], v[70:73], v[218:221], v[94:97]
	v_mfma_f32_16x16x32_bf16 v[90:93], v[78:81], v[218:221], v[90:93]
	v_mfma_f32_16x16x32_bf16 v[134:137], v[146:149], v[162:165], v[134:137]
	v_mfma_f32_16x16x32_bf16 v[130:133], v[154:157], v[162:165], v[130:133]
	v_mfma_f32_16x16x32_bf16 v[118:121], v[146:149], v[192:195], v[118:121]
	v_mfma_f32_16x16x32_bf16 v[114:117], v[154:157], v[192:195], v[114:117]
	v_mfma_f32_16x16x32_bf16 v[102:105], v[146:149], v[200:203], v[102:105]
	v_mfma_f32_16x16x32_bf16 v[98:101], v[154:157], v[200:203], v[98:101]
	v_mfma_f32_16x16x32_bf16 v[86:89], v[146:149], v[214:217], v[86:89]
	v_mfma_f32_16x16x32_bf16 v[82:85], v[154:157], v[214:217], v[82:85]
	v_mfma_f32_16x16x32_bf16 v[134:137], v[150:153], v[166:169], v[134:137]
	v_mfma_f32_16x16x32_bf16 v[130:133], v[158:161], v[166:169], v[130:133]
	v_mfma_f32_16x16x32_bf16 v[118:121], v[150:153], v[196:199], v[118:121]
	v_mfma_f32_16x16x32_bf16 v[114:117], v[158:161], v[196:199], v[114:117]
	v_mfma_f32_16x16x32_bf16 v[102:105], v[150:153], v[204:207], v[102:105]
	v_mfma_f32_16x16x32_bf16 v[98:101], v[158:161], v[204:207], v[98:101]
	v_mfma_f32_16x16x32_bf16 v[86:89], v[150:153], v[218:221], v[86:89]
	v_mfma_f32_16x16x32_bf16 v[82:85], v[158:161], v[218:221], v[82:85]
	s_setprio 0
	s_barrier
; #define FG_STAGE(bufoff, gbase, v0, v1) do { \
;         __builtin_amdgcn_global_load_lds((const unsigned*)((const char*)(gbase) + (v0)), (LAS unsigned*)(lds + (bufoff) + ldsw), 16, 0, 0); \
;         __builtin_amdgcn_global_load_lds((const unsigned*)((const char*)(gbase) + (v1)), (LAS unsigned*)(lds + (bufoff) + ldsw + 8192), 16, 0, 0); } while (0)
; #define FG_LDA(dst, b, h) do { _Pragma("unroll") for (int m = 0; m < 4; ++m) _Pragma("unroll") for (int k = 0; k < 2; ++k) dst[m][k] = *(const LAS bf16x8*)(lds + FG_SA(b, h) + aoff + m * 2048 + k * 1024); } while (0)
; #define FG_MMA(ai, bj, At, Bt) do { __builtin_amdgcn_s_setprio(1); _Pragma("unroll") for (int m = 0; m < 4; ++m) _Pragma("unroll") for (int n = 0; n < 2; ++n) _Pragma("unroll") for (int k = 0; k < 2; ++k) \
;         acc[ai][bj][m][n] = __builtin_amdgcn_mfma_f32_16x16x32_bf16(Bt[n][k], At[m][k], acc[ai][bj][m][n], 0, 0, 0); __builtin_amdgcn_s_setprio(0); } while (0)
; #define FG_WAIT_V(n) asm volatile("s_waitcnt vmcnt(" #n ")" ::: "memory")
; #define FG_WAIT_L(n) asm volatile("s_waitcnt lgkmcnt(" #n ")" ::: "memory")
; #define FG_BAR __builtin_amdgcn_s_barrier()
; #define FG_SCHED __builtin_amdgcn_sched_barrier(0)
; template <bool GATHER, class Unit, class Epi, class Sched>
; __device__ __forceinline__ void gemm_phase(LAS unsigned char* lds, const int K, const Sched& S, const Epi& E) {
;     ...
;             FG_LDA(At, 1, 1); FG_STAGE(FG_SB(1, 0), b3, voffB0, voffB1); FG_STAGE(FG_SB(1, 1), b3 + hstepB, voffB0, voffB1); FG_STAGE(FG_SA(1, 0), a3, x00, x01);
;             FG_WAIT_V(8); FG_WAIT_L(0); FG_BAR; if (hi_on) { FG_MMA(1, 0, At, B0); FG_MMA(1, 1, At, B1); } FG_BAR; FG_SCHED;
;         }
;         if (wr == 0) FG_BAR;
	s_add_i32 s38, s38, s27
	v_lshl_add_u64 v[208:209], v[208:209], 0, s[16:17]
	s_mov_b32 m0, s38
	ds_read_b128 v[162:165], v212 offset:49152
	ds_read_b128 v[166:169], v212 offset:50176
	ds_read_b128 v[192:195], v212 offset:51200
	ds_read_b128 v[196:199], v212 offset:52224
	ds_read_b128 v[200:203], v212 offset:53248
	ds_read_b128 v[204:207], v212 offset:54272
	ds_read_b128 v[214:217], v212 offset:55296
	ds_read_b128 v[218:221], v212 offset:56320
	global_load_lds_dwordx4 v[208:209], off
	s_add_i32 m0, s38, 0x2000
	s_add_u32 s38, s44, 0x80080
	v_lshl_add_u64 v[208:209], v[222:223], 0, s[16:17]
	s_addc_u32 s39, s45, 0
	s_add_i32 s44, s59, s27
	global_load_lds_dwordx4 v[208:209], off
	v_lshl_add_u64 v[208:209], s[38:39], 0, v[170:171]
	s_mov_b32 m0, s44
	s_nop 0
	global_load_lds_dwordx4 v[208:209], off
	v_lshl_add_u64 v[208:209], s[38:39], 0, v[172:173]
	s_add_i32 m0, s44, 0x2000
	s_nop 0
	global_load_lds_dwordx4 v[208:209], off
	v_lshl_add_u64 v[208:209], v[224:225], 0, s[16:17]
	s_mov_b32 m0, s50
	s_nop 0
	global_load_lds_dwordx4 v[208:209], off
	v_lshl_add_u64 v[208:209], v[226:227], 0, s[16:17]
	s_mov_b32 m0, s51
	s_nop 0
	global_load_lds_dwordx4 v[208:209], off
	s_waitcnt vmcnt(8)
	s_waitcnt lgkmcnt(0)
	s_barrier
	s_setprio 1
	s_waitcnt lgkmcnt(0)
	v_mfma_f32_16x16x32_bf16 v[62:65], v[66:69], v[162:165], v[62:65]
	v_mfma_f32_16x16x32_bf16 v[58:61], v[74:77], v[162:165], v[58:61]
	v_mfma_f32_16x16x32_bf16 v[46:49], v[66:69], v[192:195], v[46:49]
	v_mfma_f32_16x16x32_bf16 v[42:45], v[74:77], v[192:195], v[42:45]
	v_mfma_f32_16x16x32_bf16 v[30:33], v[66:69], v[200:203], v[30:33]
	v_mfma_f32_16x16x32_bf16 v[26:29], v[74:77], v[200:203], v[26:29]
	v_mfma_f32_16x16x32_bf16 v[14:17], v[66:69], v[214:217], v[14:17]
	v_mfma_f32_16x16x32_bf16 v[10:13], v[74:77], v[214:217], v[10:13]
	v_mfma_f32_16x16x32_bf16 v[62:65], v[70:73], v[166:169], v[62:65]
	v_mfma_f32_16x16x32_bf16 v[58:61], v[78:81], v[166:169], v[58:61]
	v_mfma_f32_16x16x32_bf16 v[46:49], v[70:73], v[196:199], v[46:49]
	v_mfma_f32_16x16x32_bf16 v[42:45], v[78:81], v[196:199], v[42:45]
	v_mfma_f32_16x16x32_bf16 v[30:33], v[70:73], v[204:207], v[30:33]
	v_mfma_f32_16x16x32_bf16 v[26:29], v[78:81], v[204:207], v[26:29]
	v_mfma_f32_16x16x32_bf16 v[14:17], v[70:73], v[218:221], v[14:17]
	v_mfma_f32_16x16x32_bf16 v[10:13], v[78:81], v[218:221], v[10:13]
	v_mfma_f32_16x16x32_bf16 v[54:57], v[146:149], v[162:165], v[54:57]
	v_mfma_f32_16x16x32_bf16 v[50:53], v[154:157], v[162:165], v[50:53]
	v_mfma_f32_16x16x32_bf16 v[38:41], v[146:149], v[192:195], v[38:41]
	v_mfma_f32_16x16x32_bf16 v[34:37], v[154:157], v[192:195], v[34:37]
	v_mfma_f32_16x16x32_bf16 v[22:25], v[146:149], v[200:203], v[22:25]
	v_mfma_f32_16x16x32_bf16 v[18:21], v[154:157], v[200:203], v[18:21]
	v_mfma_f32_16x16x32_bf16 v[6:9], v[146:149], v[214:217], v[6:9]
	v_mfma_f32_16x16x32_bf16 v[2:5], v[154:157], v[214:217], v[2:5]
	v_mfma_f32_16x16x32_bf16 v[54:57], v[150:153], v[166:169], v[54:57]
	v_mfma_f32_16x16x32_bf16 v[50:53], v[158:161], v[166:169], v[50:53]
	v_mfma_f32_16x16x32_bf16 v[38:41], v[150:153], v[196:199], v[38:41]
	v_mfma_f32_16x16x32_bf16 v[34:37], v[158:161], v[196:199], v[34:37]
	v_mfma_f32_16x16x32_bf16 v[22:25], v[150:153], v[204:207], v[22:25]
	v_mfma_f32_16x16x32_bf16 v[18:21], v[158:161], v[204:207], v[18:21]
	v_mfma_f32_16x16x32_bf16 v[6:9], v[150:153], v[218:221], v[6:9]
	v_mfma_f32_16x16x32_bf16 v[2:5], v[158:161], v[218:221], v[2:5]
	s_setprio 0
	s_barrier
	s_add_i32 s58, s58, 2
	s_add_u32 s56, s56, 0x100
	s_addc_u32 s57, s57, 0
	s_cmp_gt_u32 s58, 29
	s_mov_b64 s[38:39], s[42:43]
	s_cbranch_scc0 .LBB0_1546
	s_and_b64 vcc, exec, s[18:19]
	s_cbranch_vccz .LBB0_1549
	s_barrier
